# GEMM K-loops: redundant back-to-back lgkmcnt(0) waits and the s_nop M0 pads removed (address VALU moved between the M0 write and the LDS-DMA); on top of v58
# speedup vs baseline: 1.0002x; 1.0002x over previous
.LBB0_545:
	s_add_u32 s34, s30, 0xfffc0080
	s_addc_u32 s35, s31, -1
	s_add_i32 s48, 0, 0x10000
	v_add_u32_e32 v142, s48, v143
	ds_read_b128 v[148:151], v142
	ds_read_b128 v[152:155], v142 offset:1024
	ds_read_b128 v[156:159], v142 offset:2048
	ds_read_b128 v[160:163], v142 offset:3072
	s_cmp_eq_u32 s47, 12
	s_cselect_b32 s37, s25, s35
	s_cselect_b32 s36, s43, s34
	s_cselect_b32 s35, s23, s46
	s_cselect_b32 s34, s44, s45
	v_lshl_add_u64 v[144:145], s[30:31], 0, v[138:139]
	s_add_i32 m0, s9, 0xc000
	ds_read_b128 v[166:169], v165
	ds_read_b128 v[170:173], v165 offset:1024
	ds_read_b128 v[180:183], v165 offset:2048
	ds_read_b128 v[184:187], v165 offset:3072
	ds_read_b128 v[188:191], v165 offset:4096
	ds_read_b128 v[192:195], v165 offset:5120
	ds_read_b128 v[196:199], v165 offset:6144
	ds_read_b128 v[200:203], v165 offset:7168
	global_load_lds_dwordx4 v[144:145], off
	s_add_i32 m0, s9, 0xe000
	v_lshl_add_u64 v[144:145], s[30:31], 0, v[140:141]
	global_load_lds_dwordx4 v[144:145], off
	s_waitcnt lgkmcnt(8)
	s_barrier
	s_waitcnt lgkmcnt(0)
	v_mfma_i32_16x16x64_i8 v[128:131], v[148:151], v[166:169], v[128:131]
	v_mfma_i32_16x16x64_i8 v[124:127], v[156:159], v[166:169], v[124:127]
	v_mfma_i32_16x16x64_i8 v[120:123], v[148:151], v[180:183], v[120:123]
	v_mfma_i32_16x16x64_i8 v[116:119], v[156:159], v[180:183], v[116:119]
	v_mfma_i32_16x16x64_i8 v[112:115], v[148:151], v[188:191], v[112:115]
	v_mfma_i32_16x16x64_i8 v[108:111], v[156:159], v[188:191], v[108:111]
	v_mfma_i32_16x16x64_i8 v[104:107], v[148:151], v[196:199], v[104:107]
	v_mfma_i32_16x16x64_i8 v[100:103], v[156:159], v[196:199], v[100:103]
	v_mfma_i32_16x16x64_i8 v[128:131], v[152:155], v[170:173], v[128:131]
	v_mfma_i32_16x16x64_i8 v[124:127], v[160:163], v[170:173], v[124:127]
	v_mfma_i32_16x16x64_i8 v[120:123], v[152:155], v[184:187], v[120:123]
	v_mfma_i32_16x16x64_i8 v[116:119], v[160:163], v[184:187], v[116:119]
	v_mfma_i32_16x16x64_i8 v[112:115], v[152:155], v[192:195], v[112:115]
	v_mfma_i32_16x16x64_i8 v[108:111], v[160:163], v[192:195], v[108:111]
	v_mfma_i32_16x16x64_i8 v[104:107], v[152:155], v[200:203], v[104:107]
	v_mfma_i32_16x16x64_i8 v[100:103], v[160:163], v[200:203], v[100:103]
	s_barrier
	s_add_i32 s50, 0, 0x14000
	s_add_i32 s48, s48, s8
	v_add_u32_e32 v142, s50, v143
	v_lshl_add_u64 v[144:145], s[34:35], 0, v[98:99]
	s_mov_b32 m0, s48
	ds_read_b128 v[204:207], v142
	ds_read_b128 v[208:211], v142 offset:1024
	ds_read_b128 v[230:233], v142 offset:2048
	ds_read_b128 v[236:239], v142 offset:3072
	global_load_lds_dwordx4 v[144:145], off
	s_add_i32 m0, s48, 0x2000
	v_lshl_add_u64 v[174:175], s[34:35], 0, v[132:133]
	global_load_lds_dwordx4 v[174:175], off
	s_barrier
	s_waitcnt lgkmcnt(0)
	v_mfma_i32_16x16x64_i8 v[94:97], v[204:207], v[166:169], v[94:97]
	v_mfma_i32_16x16x64_i8 v[90:93], v[230:233], v[166:169], v[90:93]
	v_mfma_i32_16x16x64_i8 v[86:89], v[204:207], v[180:183], v[86:89]
	v_mfma_i32_16x16x64_i8 v[82:85], v[230:233], v[180:183], v[82:85]
	v_mfma_i32_16x16x64_i8 v[78:81], v[204:207], v[188:191], v[78:81]
	v_mfma_i32_16x16x64_i8 v[74:77], v[230:233], v[188:191], v[74:77]
	v_mfma_i32_16x16x64_i8 v[70:73], v[204:207], v[196:199], v[70:73]
	v_mfma_i32_16x16x64_i8 v[66:69], v[230:233], v[196:199], v[66:69]
	v_mfma_i32_16x16x64_i8 v[94:97], v[208:211], v[170:173], v[94:97]
	v_mfma_i32_16x16x64_i8 v[90:93], v[236:239], v[170:173], v[90:93]
	v_mfma_i32_16x16x64_i8 v[86:89], v[208:211], v[184:187], v[86:89]
	v_mfma_i32_16x16x64_i8 v[82:85], v[236:239], v[184:187], v[82:85]
	v_mfma_i32_16x16x64_i8 v[78:81], v[208:211], v[192:195], v[78:81]
	v_mfma_i32_16x16x64_i8 v[74:77], v[236:239], v[192:195], v[74:77]
	v_mfma_i32_16x16x64_i8 v[70:73], v[208:211], v[200:203], v[70:73]
	v_mfma_i32_16x16x64_i8 v[66:69], v[236:239], v[200:203], v[66:69]
	s_mov_b32 m0, s9
	v_lshl_add_u64 v[176:177], s[36:37], 0, v[136:137]
	s_barrier
	ds_read_b128 v[166:169], v165 offset:16384
	ds_read_b128 v[170:173], v165 offset:17408
	ds_read_b128 v[180:183], v165 offset:18432
	ds_read_b128 v[184:187], v165 offset:19456
	ds_read_b128 v[188:191], v165 offset:20480
	ds_read_b128 v[192:195], v165 offset:21504
	ds_read_b128 v[196:199], v165 offset:22528
	ds_read_b128 v[200:203], v165 offset:23552
	global_load_lds_dwordx4 v[176:177], off
	s_mov_b32 m0, s20
	v_lshl_add_u64 v[178:179], s[36:37], 0, v[134:135]
	global_load_lds_dwordx4 v[178:179], off
	s_barrier
	s_waitcnt lgkmcnt(0)
	v_mfma_i32_16x16x64_i8 v[62:65], v[148:151], v[166:169], v[62:65]
	v_mfma_i32_16x16x64_i8 v[58:61], v[156:159], v[166:169], v[58:61]
	v_mfma_i32_16x16x64_i8 v[54:57], v[148:151], v[180:183], v[54:57]
	v_mfma_i32_16x16x64_i8 v[50:53], v[156:159], v[180:183], v[50:53]
	v_mfma_i32_16x16x64_i8 v[46:49], v[148:151], v[188:191], v[46:49]
	v_mfma_i32_16x16x64_i8 v[42:45], v[156:159], v[188:191], v[42:45]
	v_mfma_i32_16x16x64_i8 v[38:41], v[148:151], v[196:199], v[38:41]
	v_mfma_i32_16x16x64_i8 v[34:37], v[156:159], v[196:199], v[34:37]
	v_mfma_i32_16x16x64_i8 v[62:65], v[152:155], v[170:173], v[62:65]
	v_mfma_i32_16x16x64_i8 v[58:61], v[160:163], v[170:173], v[58:61]
	v_mfma_i32_16x16x64_i8 v[54:57], v[152:155], v[184:187], v[54:57]
	v_mfma_i32_16x16x64_i8 v[50:53], v[160:163], v[184:187], v[50:53]
	v_mfma_i32_16x16x64_i8 v[46:49], v[152:155], v[192:195], v[46:49]
	v_mfma_i32_16x16x64_i8 v[42:45], v[160:163], v[192:195], v[42:45]
	v_mfma_i32_16x16x64_i8 v[38:41], v[152:155], v[200:203], v[38:41]
	v_mfma_i32_16x16x64_i8 v[34:37], v[160:163], v[200:203], v[34:37]
	s_barrier
	s_add_u32 s48, s34, 0x40000
	s_addc_u32 s49, s35, 0
	s_add_i32 s50, s50, s8
	s_mov_b32 m0, s50
	v_lshl_add_u64 v[148:149], s[48:49], 0, v[98:99]
	global_load_lds_dwordx4 v[148:149], off
	s_add_i32 m0, s50, 0x2000
	v_lshl_add_u64 v[148:149], s[48:49], 0, v[132:133]
	global_load_lds_dwordx4 v[148:149], off
	s_waitcnt vmcnt(6)
	s_barrier
	v_mfma_i32_16x16x64_i8 v[30:33], v[204:207], v[166:169], v[30:33]
	v_mfma_i32_16x16x64_i8 v[26:29], v[230:233], v[166:169], v[26:29]
	v_mfma_i32_16x16x64_i8 v[22:25], v[204:207], v[180:183], v[22:25]
	v_mfma_i32_16x16x64_i8 v[18:21], v[230:233], v[180:183], v[18:21]
	v_mfma_i32_16x16x64_i8 v[14:17], v[204:207], v[188:191], v[14:17]
	v_mfma_i32_16x16x64_i8 v[10:13], v[230:233], v[188:191], v[10:13]
	v_mfma_i32_16x16x64_i8 v[6:9], v[204:207], v[196:199], v[6:9]
	v_mfma_i32_16x16x64_i8 v[2:5], v[230:233], v[196:199], v[2:5]
	v_mfma_i32_16x16x64_i8 v[30:33], v[208:211], v[170:173], v[30:33]
	v_mfma_i32_16x16x64_i8 v[26:29], v[236:239], v[170:173], v[26:29]
	v_mfma_i32_16x16x64_i8 v[22:25], v[208:211], v[184:187], v[22:25]
	v_mfma_i32_16x16x64_i8 v[18:21], v[236:239], v[184:187], v[18:21]
	v_mfma_i32_16x16x64_i8 v[14:17], v[208:211], v[192:195], v[14:17]
	v_mfma_i32_16x16x64_i8 v[10:13], v[236:239], v[192:195], v[10:13]
	v_mfma_i32_16x16x64_i8 v[6:9], v[208:211], v[200:203], v[6:9]
	v_mfma_i32_16x16x64_i8 v[2:5], v[236:239], v[200:203], v[2:5]
	s_add_i32 s48, 0, 0x18000
	v_add_u32_e32 v142, s48, v143
	s_barrier
	ds_read_b128 v[148:151], v142
	ds_read_b128 v[152:155], v142 offset:1024
	ds_read_b128 v[156:159], v142 offset:2048
	ds_read_b128 v[160:163], v142 offset:3072
	s_add_u32 s36, s36, 0x40000
	s_addc_u32 s37, s37, 0
	s_mov_b32 m0, s21
	v_lshl_add_u64 v[204:205], s[36:37], 0, v[136:137]
	ds_read_b128 v[166:169], v165 offset:32768
	ds_read_b128 v[170:173], v165 offset:33792
	ds_read_b128 v[180:183], v165 offset:34816
	ds_read_b128 v[184:187], v165 offset:35840
	ds_read_b128 v[188:191], v165 offset:36864
	ds_read_b128 v[192:195], v165 offset:37888
	ds_read_b128 v[196:199], v165 offset:38912
	ds_read_b128 v[200:203], v165 offset:39936
	global_load_lds_dwordx4 v[204:205], off
	s_mov_b32 m0, s33
	v_lshl_add_u64 v[204:205], s[36:37], 0, v[134:135]
	global_load_lds_dwordx4 v[204:205], off
	s_waitcnt lgkmcnt(8)
	s_barrier
	s_waitcnt lgkmcnt(0)
	v_mfma_i32_16x16x64_i8 v[128:131], v[148:151], v[166:169], v[128:131]
	v_mfma_i32_16x16x64_i8 v[124:127], v[156:159], v[166:169], v[124:127]
	v_mfma_i32_16x16x64_i8 v[120:123], v[148:151], v[180:183], v[120:123]
	v_mfma_i32_16x16x64_i8 v[116:119], v[156:159], v[180:183], v[116:119]
	v_mfma_i32_16x16x64_i8 v[112:115], v[148:151], v[188:191], v[112:115]
	v_mfma_i32_16x16x64_i8 v[108:111], v[156:159], v[188:191], v[108:111]
	v_mfma_i32_16x16x64_i8 v[104:107], v[148:151], v[196:199], v[104:107]
	v_mfma_i32_16x16x64_i8 v[100:103], v[156:159], v[196:199], v[100:103]
	v_mfma_i32_16x16x64_i8 v[128:131], v[152:155], v[170:173], v[128:131]
	v_mfma_i32_16x16x64_i8 v[124:127], v[160:163], v[170:173], v[124:127]
	v_mfma_i32_16x16x64_i8 v[120:123], v[152:155], v[184:187], v[120:123]
	v_mfma_i32_16x16x64_i8 v[116:119], v[160:163], v[184:187], v[116:119]
	v_mfma_i32_16x16x64_i8 v[112:115], v[152:155], v[192:195], v[112:115]
	v_mfma_i32_16x16x64_i8 v[108:111], v[160:163], v[192:195], v[108:111]
	v_mfma_i32_16x16x64_i8 v[104:107], v[152:155], v[200:203], v[104:107]
	v_mfma_i32_16x16x64_i8 v[100:103], v[160:163], v[200:203], v[100:103]
	s_barrier
	s_add_i32 s36, 0, 0x1c000
	s_add_i32 s37, s48, s8
	v_add_u32_e32 v142, s36, v143
	v_lshl_add_u64 v[144:145], v[144:145], 0, s[68:69]
	s_mov_b32 m0, s37
	ds_read_b128 v[204:207], v142
	ds_read_b128 v[208:211], v142 offset:1024
	ds_read_b128 v[230:233], v142 offset:2048
	ds_read_b128 v[236:239], v142 offset:3072
	global_load_lds_dwordx4 v[144:145], off
	s_add_i32 m0, s37, 0x2000
	v_lshl_add_u64 v[144:145], v[174:175], 0, s[68:69]
	global_load_lds_dwordx4 v[144:145], off
	s_barrier
	s_waitcnt lgkmcnt(0)
	v_mfma_i32_16x16x64_i8 v[94:97], v[204:207], v[166:169], v[94:97]
	v_mfma_i32_16x16x64_i8 v[90:93], v[230:233], v[166:169], v[90:93]
	v_mfma_i32_16x16x64_i8 v[86:89], v[204:207], v[180:183], v[86:89]
	v_mfma_i32_16x16x64_i8 v[82:85], v[230:233], v[180:183], v[82:85]
	v_mfma_i32_16x16x64_i8 v[78:81], v[204:207], v[188:191], v[78:81]
	v_mfma_i32_16x16x64_i8 v[74:77], v[230:233], v[188:191], v[74:77]
	v_mfma_i32_16x16x64_i8 v[70:73], v[204:207], v[196:199], v[70:73]
	v_mfma_i32_16x16x64_i8 v[66:69], v[230:233], v[196:199], v[66:69]
	v_mfma_i32_16x16x64_i8 v[94:97], v[208:211], v[170:173], v[94:97]
	v_mfma_i32_16x16x64_i8 v[90:93], v[236:239], v[170:173], v[90:93]
	v_mfma_i32_16x16x64_i8 v[86:89], v[208:211], v[184:187], v[86:89]
	v_mfma_i32_16x16x64_i8 v[82:85], v[236:239], v[184:187], v[82:85]
	v_mfma_i32_16x16x64_i8 v[78:81], v[208:211], v[192:195], v[78:81]
	v_mfma_i32_16x16x64_i8 v[74:77], v[236:239], v[192:195], v[74:77]
	v_mfma_i32_16x16x64_i8 v[70:73], v[208:211], v[200:203], v[70:73]
	v_mfma_i32_16x16x64_i8 v[66:69], v[236:239], v[200:203], v[66:69]
	s_mov_b32 m0, s38
	v_lshl_add_u64 v[144:145], v[176:177], 0, s[68:69]
	s_barrier
	ds_read_b128 v[166:169], v165 offset:49152
	ds_read_b128 v[170:173], v165 offset:50176
	ds_read_b128 v[180:183], v165 offset:51200
	ds_read_b128 v[184:187], v165 offset:52224
	ds_read_b128 v[188:191], v165 offset:53248
	ds_read_b128 v[192:195], v165 offset:54272
	ds_read_b128 v[196:199], v165 offset:55296
	ds_read_b128 v[200:203], v165 offset:56320
	global_load_lds_dwordx4 v[144:145], off
	s_mov_b32 m0, s39
	v_lshl_add_u64 v[144:145], v[178:179], 0, s[68:69]
	global_load_lds_dwordx4 v[144:145], off
	s_barrier
	s_waitcnt lgkmcnt(0)
	v_mfma_i32_16x16x64_i8 v[62:65], v[148:151], v[166:169], v[62:65]
	v_mfma_i32_16x16x64_i8 v[58:61], v[156:159], v[166:169], v[58:61]
	v_mfma_i32_16x16x64_i8 v[54:57], v[148:151], v[180:183], v[54:57]
	v_mfma_i32_16x16x64_i8 v[50:53], v[156:159], v[180:183], v[50:53]
	v_mfma_i32_16x16x64_i8 v[46:49], v[148:151], v[188:191], v[46:49]
	v_mfma_i32_16x16x64_i8 v[42:45], v[156:159], v[188:191], v[42:45]
	v_mfma_i32_16x16x64_i8 v[38:41], v[148:151], v[196:199], v[38:41]
	v_mfma_i32_16x16x64_i8 v[34:37], v[156:159], v[196:199], v[34:37]
	v_mfma_i32_16x16x64_i8 v[62:65], v[152:155], v[170:173], v[62:65]
	v_mfma_i32_16x16x64_i8 v[58:61], v[160:163], v[170:173], v[58:61]
	v_mfma_i32_16x16x64_i8 v[54:57], v[152:155], v[184:187], v[54:57]
	v_mfma_i32_16x16x64_i8 v[50:53], v[160:163], v[184:187], v[50:53]
	v_mfma_i32_16x16x64_i8 v[46:49], v[152:155], v[192:195], v[46:49]
	v_mfma_i32_16x16x64_i8 v[42:45], v[160:163], v[192:195], v[42:45]
	v_mfma_i32_16x16x64_i8 v[38:41], v[152:155], v[200:203], v[38:41]
	v_mfma_i32_16x16x64_i8 v[34:37], v[160:163], v[200:203], v[34:37]
	s_barrier
	s_add_u32 s34, s34, 0x40080
	s_addc_u32 s35, s35, 0
	s_add_i32 s36, s36, s8
	s_mov_b32 m0, s36
	v_lshl_add_u64 v[144:145], s[34:35], 0, v[98:99]
	global_load_lds_dwordx4 v[144:145], off
	s_add_i32 m0, s36, 0x2000
	v_lshl_add_u64 v[144:145], s[34:35], 0, v[132:133]
	global_load_lds_dwordx4 v[144:145], off
	s_waitcnt vmcnt(6)
	s_barrier
	v_mfma_i32_16x16x64_i8 v[30:33], v[204:207], v[166:169], v[30:33]
	v_mfma_i32_16x16x64_i8 v[26:29], v[230:233], v[166:169], v[26:29]
	v_mfma_i32_16x16x64_i8 v[22:25], v[204:207], v[180:183], v[22:25]
	v_mfma_i32_16x16x64_i8 v[18:21], v[230:233], v[180:183], v[18:21]
	v_mfma_i32_16x16x64_i8 v[14:17], v[204:207], v[188:191], v[14:17]
	v_mfma_i32_16x16x64_i8 v[10:13], v[230:233], v[188:191], v[10:13]
	v_mfma_i32_16x16x64_i8 v[6:9], v[204:207], v[196:199], v[6:9]
	v_mfma_i32_16x16x64_i8 v[2:5], v[230:233], v[196:199], v[2:5]
	v_mfma_i32_16x16x64_i8 v[30:33], v[208:211], v[170:173], v[30:33]
	v_mfma_i32_16x16x64_i8 v[26:29], v[236:239], v[170:173], v[26:29]
	v_mfma_i32_16x16x64_i8 v[22:25], v[208:211], v[184:187], v[22:25]
	v_mfma_i32_16x16x64_i8 v[18:21], v[236:239], v[184:187], v[18:21]
	v_mfma_i32_16x16x64_i8 v[14:17], v[208:211], v[192:195], v[14:17]
	v_mfma_i32_16x16x64_i8 v[10:13], v[236:239], v[192:195], v[10:13]
	v_mfma_i32_16x16x64_i8 v[6:9], v[208:211], v[200:203], v[6:9]
	v_mfma_i32_16x16x64_i8 v[2:5], v[236:239], v[200:203], v[2:5]
	s_add_i32 s47, s47, 2
	s_add_u32 s30, s30, 0x100
	s_addc_u32 s31, s31, 0
	s_add_u32 s45, s45, 0x100
	s_addc_u32 s46, s46, 0
	s_cmp_gt_u32 s47, 13
	s_barrier
	s_cbranch_scc0 .LBB0_545
	v_lshl_add_u32 v144, s42, 8, v1
	v_or_b32_e32 v182, 16, v144
	v_ashrrev_i32_e32 v145, 31, v144
	v_ashrrev_i32_e32 v183, 31, v182
	v_or_b32_e32 v174, 32, v144
	v_lshl_add_u64 v[148:149], v[144:145], 2, s[54:55]
	v_lshl_add_u64 v[150:151], v[182:183], 2, s[54:55]
	v_ashrrev_i32_e32 v175, 31, v174
	v_or_b32_e32 v170, 48, v144
	v_lshl_or_b32 v186, s41, 8, v147
	global_load_dword v184, v[148:149], off
	global_load_dword v180, v[150:151], off
	v_lshl_add_u64 v[150:151], v[174:175], 2, s[54:55]
	v_ashrrev_i32_e32 v171, 31, v170
	v_ashrrev_i32_e32 v187, 31, v186
	global_load_dword v172, v[150:151], off
	v_lshl_add_u64 v[150:151], v[170:171], 2, s[54:55]
	v_lshl_add_u64 v[158:159], v[186:187], 2, s[18:19]
	global_load_dword v168, v[150:151], off
	global_load_dword v166, v[148:149], off offset:512
	global_load_dword v164, v[148:149], off offset:576
	global_load_dword v146, v[148:149], off offset:640
	global_load_dword v142, v[148:149], off offset:704
	global_load_dwordx4 v[154:157], v[158:159], off offset:16
	global_load_dwordx4 v[150:153], v[158:159], off
	global_load_dwordx4 v[188:191], v[158:159], off offset:528
	s_nop 0
	global_load_dwordx4 v[158:161], v[158:159], off offset:512
	v_cvt_f32_i32_e32 v129, v129
	v_cvt_f32_i32_e32 v128, v128
	v_cvt_f32_i32_e32 v127, v127
	v_cvt_f32_i32_e32 v126, v126
	v_cvt_f32_i32_e32 v131, v131
	v_cvt_f32_i32_e32 v130, v130
	v_readlane_b32 s30, v252, 59
	v_cvt_f32_i32_e32 v177, v125
	v_cvt_f32_i32_e32 v176, v124
	v_readlane_b32 s31, v252, 60
	v_cvt_f32_i32_e32 v97, v97
	v_cvt_f32_i32_e32 v96, v96
	v_cvt_f32_i32_e32 v179, v95
	v_cvt_f32_i32_e32 v178, v94
	v_cvt_f32_i32_e32 v95, v93
	v_cvt_f32_i32_e32 v94, v92
	v_cvt_f32_i32_e32 v93, v79
	v_cvt_f32_i32_e32 v92, v78
	v_cvt_f32_i32_e32 v79, v77
	v_cvt_f32_i32_e32 v78, v76
	v_cvt_f32_i32_e32 v77, v71
	v_cvt_f32_i32_e32 v76, v70
	v_cvt_f32_i32_e32 v71, v69
	v_cvt_f32_i32_e32 v70, v68
	v_cvt_f32_i32_e32 v69, v63
	v_cvt_f32_i32_e32 v68, v62
	v_cvt_f32_i32_e32 v63, v59
	v_cvt_f32_i32_e32 v62, v58
	v_cvt_f32_i32_e32 v59, v27
	v_cvt_f32_i32_e32 v58, v26
	v_cvt_f32_i32_e32 v27, v19
	v_cvt_f32_i32_e32 v26, v18
	v_cvt_f32_i32_e32 v19, v11
	v_cvt_f32_i32_e32 v18, v10
	v_mov_b64_e32 v[10:11], s[30:31]
	s_movk_i32 s23, 0x3200
	v_cvt_f32_i32_e32 v125, v91
	v_cvt_f32_i32_e32 v124, v90
	v_cvt_f32_i32_e32 v91, v75
	v_cvt_f32_i32_e32 v90, v74
	v_cvt_f32_i32_e32 v75, v67
	v_cvt_f32_i32_e32 v74, v66
	v_cvt_f32_i32_e32 v67, v31
	v_cvt_f32_i32_e32 v66, v30
	v_cvt_f32_i32_e32 v31, v29
	v_cvt_f32_i32_e32 v30, v28
	v_cvt_f32_i32_e32 v29, v23
	v_cvt_f32_i32_e32 v28, v22
	v_cvt_f32_i32_e32 v23, v21
	v_cvt_f32_i32_e32 v22, v20
	v_cvt_f32_i32_e32 v21, v15
	v_cvt_f32_i32_e32 v20, v14
	v_cvt_f32_i32_e32 v15, v13
	v_cvt_f32_i32_e32 v14, v12
	v_lshlrev_b64 v[12:13], 1, v[186:187]
	v_cvt_f32_i32_e32 v121, v121
	v_cvt_f32_i32_e32 v120, v120
	v_cvt_f32_i32_e32 v123, v123
	v_cvt_f32_i32_e32 v122, v122
	v_cvt_f32_i32_e32 v119, v119
	v_cvt_f32_i32_e32 v118, v118
	v_cvt_f32_i32_e32 v117, v117
	v_cvt_f32_i32_e32 v116, v116
	v_cvt_f32_i32_e32 v89, v89
	v_cvt_f32_i32_e32 v88, v88
	v_cvt_f32_i32_e32 v87, v87
	v_cvt_f32_i32_e32 v86, v86
	v_cvt_f32_i32_e32 v85, v85
	s_waitcnt vmcnt(0)
	v_pk_mul_f32 v[128:129], v[184:185], v[128:129] op_sel_hi:[0,1]
	v_pk_mul_f32 v[126:127], v[184:185], v[126:127] op_sel_hi:[0,1]
	v_pk_mul_f32 v[130:131], v[184:185], v[130:131] op_sel_hi:[0,1]
	v_pk_mul_f32 v[176:177], v[184:185], v[176:177] op_sel_hi:[0,1]
	v_pk_mul_f32 v[96:97], v[184:185], v[96:97] op_sel_hi:[0,1]
	v_pk_mul_f32 v[94:95], v[184:185], v[94:95] op_sel_hi:[0,1]
	v_cvt_f32_i32_e32 v84, v84
	v_cvt_f32_i32_e32 v83, v83
	v_cvt_f32_i32_e32 v82, v82
	v_pk_mul_f32 v[154:155], v[154:155], s[58:59] op_sel_hi:[1,0]
	v_pk_mul_f32 v[148:149], v[152:153], s[58:59] op_sel_hi:[1,0]
	v_pk_mul_f32 v[150:151], v[150:151], s[58:59] op_sel_hi:[1,0]
	v_pk_mul_f32 v[152:153], v[156:157], s[58:59] op_sel_hi:[1,0]
	v_pk_mul_f32 v[162:163], v[188:189], s[58:59] op_sel_hi:[1,0]
	v_mad_i64_i32 v[188:189], s[30:31], v144, s23, v[10:11]
	v_lshl_add_u64 v[186:187], v[188:189], 0, v[12:13]
	v_pk_mul_f32 v[188:189], v[152:153], v[126:127]
	v_pk_mul_f32 v[126:127], v[150:151], v[128:129]
	v_pk_mul_f32 v[130:131], v[148:149], v[130:131]
	v_cvt_pk_bf16_f32 v126, v126, v127
	v_pk_mul_f32 v[156:157], v[160:161], s[58:59] op_sel_hi:[1,0]
	v_cvt_pk_bf16_f32 v127, v130, v131
	v_pk_mul_f32 v[158:159], v[158:159], s[58:59] op_sel_hi:[1,0]
	v_pk_mul_f32 v[160:161], v[190:191], s[58:59] op_sel_hi:[1,0]
	v_pk_mul_f32 v[176:177], v[154:155], v[176:177]
	v_pk_mul_f32 v[124:125], v[184:185], v[124:125] op_sel_hi:[0,1]
	v_cvt_pk_bf16_f32 v128, v176, v177
	v_cvt_pk_bf16_f32 v129, v188, v189
	global_store_dwordx4 v[186:187], v[126:129], off
	v_pk_mul_f32 v[96:97], v[156:157], v[96:97]
	v_pk_mul_f32 v[124:125], v[162:163], v[124:125]
	v_pk_mul_f32 v[126:127], v[184:185], v[178:179] op_sel_hi:[0,1]
	v_pk_mul_f32 v[126:127], v[158:159], v[126:127]
	v_pk_mul_f32 v[128:129], v[160:161], v[94:95]
	v_cvt_pk_bf16_f32 v94, v126, v127
	v_cvt_pk_bf16_f32 v95, v96, v97
	v_cvt_pk_bf16_f32 v96, v124, v125
	v_cvt_f32_i32_e32 v113, v113
	v_cvt_pk_bf16_f32 v97, v128, v129
	global_store_dwordx4 v[186:187], v[94:97], off offset:256
	v_cvt_f32_i32_e32 v112, v112
	v_cvt_f32_i32_e32 v115, v115
	v_mad_i64_i32 v[94:95], s[30:31], v182, s23, v[10:11]
	v_lshl_add_u64 v[124:125], v[94:95], 0, v[12:13]
	v_pk_mul_f32 v[94:95], v[180:181], v[120:121] op_sel_hi:[0,1]
	v_pk_mul_f32 v[96:97], v[180:181], v[122:123] op_sel_hi:[0,1]
	v_pk_mul_f32 v[94:95], v[150:151], v[94:95]
	v_cvt_f32_i32_e32 v114, v114
	v_pk_mul_f32 v[116:117], v[180:181], v[116:117] op_sel_hi:[0,1]
	v_pk_mul_f32 v[118:119], v[180:181], v[118:119] op_sel_hi:[0,1]
	v_pk_mul_f32 v[96:97], v[148:149], v[96:97]
	v_cvt_pk_bf16_f32 v94, v94, v95
	v_pk_mul_f32 v[86:87], v[180:181], v[86:87] op_sel_hi:[0,1]
	v_cvt_pk_bf16_f32 v95, v96, v97
	v_pk_mul_f32 v[88:89], v[180:181], v[88:89] op_sel_hi:[0,1]
	v_pk_mul_f32 v[82:83], v[180:181], v[82:83] op_sel_hi:[0,1]
	v_pk_mul_f32 v[84:85], v[180:181], v[84:85] op_sel_hi:[0,1]
	v_cvt_f32_i32_e32 v111, v111
	v_cvt_f32_i32_e32 v110, v110
	v_cvt_f32_i32_e32 v109, v109
	v_cvt_f32_i32_e32 v108, v108
	v_pk_mul_f32 v[118:119], v[152:153], v[118:119]
	v_pk_mul_f32 v[116:117], v[154:155], v[116:117]
	v_pk_mul_f32 v[88:89], v[156:157], v[88:89]
	v_cvt_pk_bf16_f32 v96, v116, v117
	v_cvt_pk_bf16_f32 v97, v118, v119
	global_store_dwordx4 v[124:125], v[94:97], off
	v_pk_mul_f32 v[86:87], v[158:159], v[86:87]
	v_cvt_f32_i32_e32 v81, v81
	v_pk_mul_f32 v[94:95], v[160:161], v[84:85]
	v_pk_mul_f32 v[84:85], v[162:163], v[82:83]
	v_cvt_pk_bf16_f32 v82, v86, v87
	v_cvt_pk_bf16_f32 v83, v88, v89
	v_cvt_f32_i32_e32 v80, v80
	v_cvt_pk_bf16_f32 v84, v84, v85
	v_cvt_pk_bf16_f32 v85, v94, v95
	global_store_dwordx4 v[124:125], v[82:85], off offset:256
	v_cvt_f32_i32_e32 v105, v105
	v_cvt_f32_i32_e32 v104, v104
	v_mad_i64_i32 v[82:83], s[30:31], v174, s23, v[10:11]
	v_lshl_add_u64 v[86:87], v[82:83], 0, v[12:13]
	v_pk_mul_f32 v[82:83], v[172:173], v[112:113] op_sel_hi:[0,1]
	v_pk_mul_f32 v[84:85], v[172:173], v[114:115] op_sel_hi:[0,1]
	v_pk_mul_f32 v[82:83], v[150:151], v[82:83]
	v_pk_mul_f32 v[88:89], v[172:173], v[108:109] op_sel_hi:[0,1]
	v_pk_mul_f32 v[94:95], v[172:173], v[110:111] op_sel_hi:[0,1]
	v_pk_mul_f32 v[84:85], v[148:149], v[84:85]
	v_cvt_pk_bf16_f32 v82, v82, v83
	v_cvt_f32_i32_e32 v107, v107
	v_cvt_pk_bf16_f32 v83, v84, v85
	v_cvt_f32_i32_e32 v106, v106
	v_cvt_f32_i32_e32 v73, v73
	v_cvt_f32_i32_e32 v72, v72
	v_pk_mul_f32 v[94:95], v[152:153], v[94:95]
	v_pk_mul_f32 v[88:89], v[154:155], v[88:89]
	v_pk_mul_f32 v[80:81], v[172:173], v[80:81] op_sel_hi:[0,1]
	v_cvt_pk_bf16_f32 v84, v88, v89
	v_cvt_pk_bf16_f32 v85, v94, v95
	global_store_dwordx4 v[86:87], v[82:85], off
	v_pk_mul_f32 v[78:79], v[172:173], v[78:79] op_sel_hi:[0,1]
	v_cvt_f32_i32_e32 v103, v103
	v_pk_mul_f32 v[82:83], v[172:173], v[92:93] op_sel_hi:[0,1]
	v_cvt_f32_i32_e32 v102, v102
	v_cvt_f32_i32_e32 v101, v101
	v_cvt_f32_i32_e32 v100, v100
	v_pk_mul_f32 v[84:85], v[172:173], v[90:91] op_sel_hi:[0,1]
	v_pk_mul_f32 v[80:81], v[156:157], v[80:81]
	v_pk_mul_f32 v[82:83], v[158:159], v[82:83]
	v_pk_mul_f32 v[88:89], v[160:161], v[78:79]
	v_cvt_pk_bf16_f32 v78, v82, v83
	v_cvt_pk_bf16_f32 v79, v80, v81
	v_cvt_f32_i32_e32 v61, v61
	v_cvt_f32_i32_e32 v60, v60
	v_pk_mul_f32 v[84:85], v[162:163], v[84:85]
	v_cvt_f32_i32_e32 v65, v65
	v_cvt_pk_bf16_f32 v80, v84, v85
	v_cvt_pk_bf16_f32 v81, v88, v89
	global_store_dwordx4 v[86:87], v[78:81], off offset:256
	v_cvt_f32_i32_e32 v64, v64
	v_pk_mul_f32 v[72:73], v[168:169], v[72:73] op_sel_hi:[0,1]
	v_mad_i64_i32 v[78:79], s[30:31], v170, s23, v[10:11]
	v_lshl_add_u64 v[82:83], v[78:79], 0, v[12:13]
	v_pk_mul_f32 v[78:79], v[168:169], v[104:105] op_sel_hi:[0,1]
	v_pk_mul_f32 v[80:81], v[168:169], v[106:107] op_sel_hi:[0,1]
	v_pk_mul_f32 v[78:79], v[150:151], v[78:79]
	v_cvt_f32_i32_e32 v33, v33
	v_cvt_f32_i32_e32 v32, v32
	v_pk_mul_f32 v[84:85], v[168:169], v[100:101] op_sel_hi:[0,1]
	v_pk_mul_f32 v[86:87], v[168:169], v[102:103] op_sel_hi:[0,1]
	v_pk_mul_f32 v[80:81], v[148:149], v[80:81]
	v_cvt_pk_bf16_f32 v78, v78, v79
	v_pk_mul_f32 v[76:77], v[168:169], v[76:77] op_sel_hi:[0,1]
	v_cvt_pk_bf16_f32 v79, v80, v81
	v_pk_mul_f32 v[74:75], v[168:169], v[74:75] op_sel_hi:[0,1]
	v_pk_mul_f32 v[70:71], v[168:169], v[70:71] op_sel_hi:[0,1]
	v_pk_mul_f32 v[72:73], v[156:157], v[72:73]
	v_add_u32_e32 v145, 0x80, v144
	v_pk_mul_f32 v[86:87], v[152:153], v[86:87]
	v_pk_mul_f32 v[84:85], v[154:155], v[84:85]
	v_pk_mul_f32 v[76:77], v[158:159], v[76:77]
	v_cvt_pk_bf16_f32 v80, v84, v85
	v_cvt_pk_bf16_f32 v81, v86, v87
	global_store_dwordx4 v[82:83], v[78:81], off
	v_pk_mul_f32 v[74:75], v[162:163], v[74:75]
	v_pk_mul_f32 v[68:69], v[166:167], v[68:69] op_sel_hi:[0,1]
	v_pk_mul_f32 v[78:79], v[160:161], v[70:71]
	v_cvt_pk_bf16_f32 v70, v76, v77
	v_cvt_pk_bf16_f32 v71, v72, v73
	v_cvt_pk_bf16_f32 v72, v74, v75
	v_pk_mul_f32 v[60:61], v[166:167], v[60:61] op_sel_hi:[0,1]
	v_cvt_pk_bf16_f32 v73, v78, v79
	global_store_dwordx4 v[82:83], v[70:73], off offset:256
	v_pk_mul_f32 v[64:65], v[166:167], v[64:65] op_sel_hi:[0,1]
	v_pk_mul_f32 v[62:63], v[166:167], v[62:63] op_sel_hi:[0,1]
	v_mad_i64_i32 v[70:71], s[30:31], v145, s23, v[10:11]
	v_pk_mul_f32 v[72:73], v[152:153], v[60:61]
	v_pk_mul_f32 v[60:61], v[150:151], v[68:69]
	v_lshl_add_u64 v[70:71], v[70:71], 0, v[12:13]
	v_pk_mul_f32 v[62:63], v[154:155], v[62:63]
	v_pk_mul_f32 v[64:65], v[148:149], v[64:65]
	v_cvt_pk_bf16_f32 v60, v60, v61
	v_cvt_f32_i32_e32 v55, v55
	v_cvt_pk_bf16_f32 v61, v64, v65
	v_cvt_f32_i32_e32 v54, v54
	v_cvt_pk_bf16_f32 v62, v62, v63
	v_cvt_pk_bf16_f32 v63, v72, v73
	global_store_dwordx4 v[70:71], v[60:63], off
	v_pk_mul_f32 v[32:33], v[166:167], v[32:33] op_sel_hi:[0,1]
	v_pk_mul_f32 v[30:31], v[166:167], v[30:31] op_sel_hi:[0,1]
	v_pk_mul_f32 v[60:61], v[166:167], v[66:67] op_sel_hi:[0,1]
	v_cvt_f32_i32_e32 v57, v57
	v_cvt_f32_i32_e32 v56, v56
	v_pk_mul_f32 v[58:59], v[166:167], v[58:59] op_sel_hi:[0,1]
	v_pk_mul_f32 v[32:33], v[156:157], v[32:33]
	v_pk_mul_f32 v[60:61], v[158:159], v[60:61]
	v_pk_mul_f32 v[62:63], v[160:161], v[30:31]
	v_cvt_pk_bf16_f32 v30, v60, v61
	v_cvt_f32_i32_e32 v53, v53
	v_cvt_f32_i32_e32 v52, v52
	v_cvt_f32_i32_e32 v51, v51
	v_cvt_f32_i32_e32 v50, v50
	v_cvt_f32_i32_e32 v25, v25
	v_cvt_f32_i32_e32 v24, v24
	v_pk_mul_f32 v[58:59], v[162:163], v[58:59]
	v_cvt_pk_bf16_f32 v31, v32, v33
	v_cvt_f32_i32_e32 v47, v47
	v_cvt_pk_bf16_f32 v32, v58, v59
	v_cvt_pk_bf16_f32 v33, v62, v63
	global_store_dwordx4 v[70:71], v[30:33], off offset:256
	v_cvt_f32_i32_e32 v46, v46
	v_pk_mul_f32 v[50:51], v[164:165], v[50:51] op_sel_hi:[0,1]
	v_add_u32_e32 v30, 0x90, v144
	v_mad_i64_i32 v[30:31], s[30:31], v30, s23, v[10:11]
	v_lshl_add_u64 v[58:59], v[30:31], 0, v[12:13]
	v_pk_mul_f32 v[30:31], v[164:165], v[54:55] op_sel_hi:[0,1]
	v_pk_mul_f32 v[32:33], v[164:165], v[56:57] op_sel_hi:[0,1]
	v_pk_mul_f32 v[30:31], v[150:151], v[30:31]
	v_pk_mul_f32 v[52:53], v[164:165], v[52:53] op_sel_hi:[0,1]
	v_pk_mul_f32 v[32:33], v[148:149], v[32:33]
	v_cvt_pk_bf16_f32 v30, v30, v31
	v_pk_mul_f32 v[28:29], v[164:165], v[28:29] op_sel_hi:[0,1]
	v_cvt_pk_bf16_f32 v31, v32, v33
	v_pk_mul_f32 v[24:25], v[164:165], v[24:25] op_sel_hi:[0,1]
	v_pk_mul_f32 v[22:23], v[164:165], v[22:23] op_sel_hi:[0,1]
	v_cvt_f32_i32_e32 v49, v49
	v_cvt_f32_i32_e32 v48, v48
	v_pk_mul_f32 v[52:53], v[152:153], v[52:53]
	v_pk_mul_f32 v[50:51], v[154:155], v[50:51]
	v_pk_mul_f32 v[26:27], v[164:165], v[26:27] op_sel_hi:[0,1]
	v_cvt_pk_bf16_f32 v32, v50, v51
	v_cvt_pk_bf16_f32 v33, v52, v53
	global_store_dwordx4 v[58:59], v[30:33], off
	v_pk_mul_f32 v[24:25], v[156:157], v[24:25]
	v_pk_mul_f32 v[28:29], v[158:159], v[28:29]
	v_pk_mul_f32 v[30:31], v[160:161], v[22:23]
	v_cvt_pk_bf16_f32 v22, v28, v29
	v_cvt_f32_i32_e32 v45, v45
	v_cvt_f32_i32_e32 v44, v44
	v_cvt_f32_i32_e32 v43, v43
	v_cvt_f32_i32_e32 v42, v42
	v_cvt_f32_i32_e32 v17, v17
	v_cvt_f32_i32_e32 v16, v16
	v_pk_mul_f32 v[26:27], v[162:163], v[26:27]
	v_cvt_pk_bf16_f32 v23, v24, v25
	v_cvt_f32_i32_e32 v39, v39
	v_cvt_pk_bf16_f32 v24, v26, v27
	v_cvt_pk_bf16_f32 v25, v30, v31
	global_store_dwordx4 v[58:59], v[22:25], off offset:256
	v_cvt_f32_i32_e32 v38, v38
	v_pk_mul_f32 v[28:29], v[146:147], v[42:43] op_sel_hi:[0,1]
	v_add_u32_e32 v22, 0xa0, v144
	v_mad_i64_i32 v[22:23], s[30:31], v22, s23, v[10:11]
	v_lshl_add_u64 v[26:27], v[22:23], 0, v[12:13]
	v_pk_mul_f32 v[22:23], v[146:147], v[46:47] op_sel_hi:[0,1]
	v_pk_mul_f32 v[24:25], v[146:147], v[48:49] op_sel_hi:[0,1]
	v_pk_mul_f32 v[22:23], v[150:151], v[22:23]
	v_pk_mul_f32 v[30:31], v[146:147], v[44:45] op_sel_hi:[0,1]
	v_pk_mul_f32 v[24:25], v[148:149], v[24:25]
	v_cvt_pk_bf16_f32 v22, v22, v23
	v_pk_mul_f32 v[20:21], v[146:147], v[20:21] op_sel_hi:[0,1]
	v_cvt_pk_bf16_f32 v23, v24, v25
	v_pk_mul_f32 v[16:17], v[146:147], v[16:17] op_sel_hi:[0,1]
	v_pk_mul_f32 v[14:15], v[146:147], v[14:15] op_sel_hi:[0,1]
	v_cvt_f32_i32_e32 v41, v41
	v_cvt_f32_i32_e32 v40, v40
	v_pk_mul_f32 v[30:31], v[152:153], v[30:31]
	v_pk_mul_f32 v[28:29], v[154:155], v[28:29]
	v_pk_mul_f32 v[18:19], v[146:147], v[18:19] op_sel_hi:[0,1]
	v_cvt_pk_bf16_f32 v24, v28, v29
	v_cvt_pk_bf16_f32 v25, v30, v31
	global_store_dwordx4 v[26:27], v[22:25], off
	v_pk_mul_f32 v[16:17], v[156:157], v[16:17]
	v_pk_mul_f32 v[20:21], v[158:159], v[20:21]
	v_pk_mul_f32 v[22:23], v[160:161], v[14:15]
	v_cvt_pk_bf16_f32 v14, v20, v21
	v_cvt_f32_i32_e32 v37, v37
	v_cvt_f32_i32_e32 v36, v36
	v_cvt_f32_i32_e32 v35, v35
	v_cvt_f32_i32_e32 v34, v34
	v_cvt_f32_i32_e32 v5, v5
	v_cvt_f32_i32_e32 v4, v4
	v_cvt_f32_i32_e32 v3, v3
	v_cvt_f32_i32_e32 v2, v2
	v_pk_mul_f32 v[18:19], v[162:163], v[18:19]
	v_cvt_pk_bf16_f32 v15, v16, v17
	v_cvt_f32_i32_e32 v9, v9
	v_cvt_pk_bf16_f32 v16, v18, v19
	v_cvt_pk_bf16_f32 v17, v22, v23
	global_store_dwordx4 v[26:27], v[14:17], off offset:256
	v_cvt_f32_i32_e32 v8, v8
	v_cvt_f32_i32_e32 v7, v7
	v_add_u32_e32 v14, 0xb0, v144
	v_cvt_f32_i32_e32 v6, v6
	v_mad_i64_i32 v[10:11], s[30:31], v14, s23, v[10:11]
	v_lshl_add_u64 v[14:15], v[10:11], 0, v[12:13]
	v_pk_mul_f32 v[10:11], v[142:143], v[38:39] op_sel_hi:[0,1]
	v_pk_mul_f32 v[12:13], v[142:143], v[40:41] op_sel_hi:[0,1]
	v_pk_mul_f32 v[10:11], v[150:151], v[10:11]
	v_pk_mul_f32 v[16:17], v[142:143], v[34:35] op_sel_hi:[0,1]
	v_pk_mul_f32 v[18:19], v[142:143], v[36:37] op_sel_hi:[0,1]
	v_pk_mul_f32 v[12:13], v[148:149], v[12:13]
	v_cvt_pk_bf16_f32 v10, v10, v11
	v_pk_mul_f32 v[2:3], v[142:143], v[2:3] op_sel_hi:[0,1]
	v_cvt_pk_bf16_f32 v11, v12, v13
	v_pk_mul_f32 v[4:5], v[142:143], v[4:5] op_sel_hi:[0,1]
	v_pk_mul_f32 v[18:19], v[152:153], v[18:19]
	v_pk_mul_f32 v[16:17], v[154:155], v[16:17]
	v_pk_mul_f32 v[6:7], v[142:143], v[6:7] op_sel_hi:[0,1]
	v_cvt_pk_bf16_f32 v12, v16, v17
	v_cvt_pk_bf16_f32 v13, v18, v19
	global_store_dwordx4 v[14:15], v[10:13], off
	v_pk_mul_f32 v[8:9], v[142:143], v[8:9] op_sel_hi:[0,1]
	s_and_b64 vcc, exec, s[0:1]
	v_pk_mul_f32 v[10:11], v[160:161], v[4:5]
	v_pk_mul_f32 v[4:5], v[162:163], v[2:3]
	s_mov_b32 s42, s24
	s_mov_b32 s41, s22
	s_mov_b64 s[34:35], s[28:29]
	s_mov_b64 s[30:31], s[26:27]
	v_pk_mul_f32 v[8:9], v[156:157], v[8:9]
	v_pk_mul_f32 v[6:7], v[158:159], v[6:7]
	s_nop 0
	v_cvt_pk_bf16_f32 v2, v6, v7
	v_cvt_pk_bf16_f32 v3, v8, v9
	v_cvt_pk_bf16_f32 v4, v4, v5
	v_cvt_pk_bf16_f32 v5, v10, v11
	global_store_dwordx4 v[14:15], v[2:5], off offset:256
	s_cbranch_vccz .LBB0_538
	s_waitcnt vmcnt(0)
	s_cmpk_gt_u32 s3, 0xff
	s_cbranch_scc1 .LBB0_549
	s_barrier

.LBB0_690:
	s_add_u32 s26, s24, 0x100
	s_addc_u32 s27, s25, 0
	s_add_i32 s45, 0, 0x10000
	v_add_u32_e32 v142, s45, v143
	ds_read_b128 v[146:149], v142
	ds_read_b128 v[152:155], v142 offset:1024
	ds_read_b128 v[156:159], v142 offset:2048
	ds_read_b128 v[160:163], v142 offset:3072
	s_cmp_eq_u32 s44, 6
	s_cselect_b32 s31, s19, s27
	s_cselect_b32 s30, s18, s26
	s_cselect_b32 s29, s23, s43
	s_cselect_b32 s28, s22, s42
	v_lshl_add_u64 v[176:177], s[24:25], 0, v[138:139]
	s_add_i32 m0, s9, 0xc000
	ds_read_b128 v[164:167], v151
	ds_read_b128 v[168:171], v151 offset:1024
	ds_read_b128 v[172:175], v151 offset:2048
	ds_read_b128 v[180:183], v151 offset:3072
	ds_read_b128 v[184:187], v151 offset:4096
	ds_read_b128 v[188:191], v151 offset:5120
	ds_read_b128 v[192:195], v151 offset:6144
	ds_read_b128 v[196:199], v151 offset:7168
	global_load_lds_dwordx4 v[176:177], off
	s_add_i32 m0, s9, 0xe000
	v_lshl_add_u64 v[176:177], s[24:25], 0, v[140:141]
	global_load_lds_dwordx4 v[176:177], off
	s_waitcnt lgkmcnt(8)
	s_barrier
	s_waitcnt lgkmcnt(0)
	v_mfma_f32_16x16x32_bf16 v[128:131], v[146:149], v[164:167], v[128:131]
	v_mfma_f32_16x16x32_bf16 v[124:127], v[156:159], v[164:167], v[124:127]
	v_mfma_f32_16x16x32_bf16 v[112:115], v[146:149], v[172:175], v[112:115]
	v_mfma_f32_16x16x32_bf16 v[108:111], v[156:159], v[172:175], v[108:111]
	v_mfma_f32_16x16x32_bf16 v[94:97], v[146:149], v[184:187], v[94:97]
	v_mfma_f32_16x16x32_bf16 v[90:93], v[156:159], v[184:187], v[90:93]
	v_mfma_f32_16x16x32_bf16 v[78:81], v[146:149], v[192:195], v[78:81]
	v_mfma_f32_16x16x32_bf16 v[74:77], v[156:159], v[192:195], v[74:77]
	v_mfma_f32_16x16x32_bf16 v[128:131], v[152:155], v[168:171], v[128:131]
	v_mfma_f32_16x16x32_bf16 v[124:127], v[160:163], v[168:171], v[124:127]
	v_mfma_f32_16x16x32_bf16 v[112:115], v[152:155], v[180:183], v[112:115]
	v_mfma_f32_16x16x32_bf16 v[108:111], v[160:163], v[180:183], v[108:111]
	v_mfma_f32_16x16x32_bf16 v[94:97], v[152:155], v[188:191], v[94:97]
	v_mfma_f32_16x16x32_bf16 v[90:93], v[160:163], v[188:191], v[90:93]
	v_mfma_f32_16x16x32_bf16 v[78:81], v[152:155], v[196:199], v[78:81]
	v_mfma_f32_16x16x32_bf16 v[74:77], v[160:163], v[196:199], v[74:77]
	s_barrier
	s_add_i32 s46, 0, 0x14000
	s_add_i32 s24, s45, s8
	v_add_u32_e32 v142, s46, v143
	v_lshl_add_u64 v[176:177], s[28:29], 0, v[98:99]
	s_mov_b32 m0, s24
	ds_read_b128 v[200:203], v142
	ds_read_b128 v[204:207], v142 offset:1024
	ds_read_b128 v[208:211], v142 offset:2048
	ds_read_b128 v[230:233], v142 offset:3072
	global_load_lds_dwordx4 v[176:177], off
	s_add_i32 m0, s24, 0x2000
	v_lshl_add_u64 v[178:179], s[28:29], 0, v[132:133]
	global_load_lds_dwordx4 v[178:179], off
	s_barrier
	s_waitcnt lgkmcnt(0)
	v_mfma_f32_16x16x32_bf16 v[120:123], v[200:203], v[164:167], v[120:123]
	v_mfma_f32_16x16x32_bf16 v[116:119], v[208:211], v[164:167], v[116:119]
	v_mfma_f32_16x16x32_bf16 v[104:107], v[200:203], v[172:175], v[104:107]
	v_mfma_f32_16x16x32_bf16 v[100:103], v[208:211], v[172:175], v[100:103]
	v_mfma_f32_16x16x32_bf16 v[86:89], v[200:203], v[184:187], v[86:89]
	v_mfma_f32_16x16x32_bf16 v[82:85], v[208:211], v[184:187], v[82:85]
	v_mfma_f32_16x16x32_bf16 v[70:73], v[200:203], v[192:195], v[70:73]
	v_mfma_f32_16x16x32_bf16 v[66:69], v[208:211], v[192:195], v[66:69]
	v_mfma_f32_16x16x32_bf16 v[120:123], v[204:207], v[168:171], v[120:123]
	v_mfma_f32_16x16x32_bf16 v[116:119], v[230:233], v[168:171], v[116:119]
	v_mfma_f32_16x16x32_bf16 v[104:107], v[204:207], v[180:183], v[104:107]
	v_mfma_f32_16x16x32_bf16 v[100:103], v[230:233], v[180:183], v[100:103]
	v_mfma_f32_16x16x32_bf16 v[86:89], v[204:207], v[188:191], v[86:89]
	v_mfma_f32_16x16x32_bf16 v[82:85], v[230:233], v[188:191], v[82:85]
	v_mfma_f32_16x16x32_bf16 v[70:73], v[204:207], v[196:199], v[70:73]
	v_mfma_f32_16x16x32_bf16 v[66:69], v[230:233], v[196:199], v[66:69]
	s_mov_b32 m0, s9
	v_lshl_add_u64 v[212:213], s[30:31], 0, v[136:137]
	s_barrier
	ds_read_b128 v[164:167], v151 offset:16384
	ds_read_b128 v[168:171], v151 offset:17408
	ds_read_b128 v[172:175], v151 offset:18432
	ds_read_b128 v[180:183], v151 offset:19456
	ds_read_b128 v[184:187], v151 offset:20480
	ds_read_b128 v[188:191], v151 offset:21504
	ds_read_b128 v[192:195], v151 offset:22528
	ds_read_b128 v[196:199], v151 offset:23552
	global_load_lds_dwordx4 v[212:213], off
	s_mov_b32 m0, s20
	v_lshl_add_u64 v[214:215], s[30:31], 0, v[134:135]
	global_load_lds_dwordx4 v[214:215], off
	s_barrier
	s_waitcnt lgkmcnt(0)
	v_mfma_f32_16x16x32_bf16 v[62:65], v[146:149], v[164:167], v[62:65]
	v_mfma_f32_16x16x32_bf16 v[58:61], v[156:159], v[164:167], v[58:61]
	v_mfma_f32_16x16x32_bf16 v[50:53], v[146:149], v[172:175], v[50:53]
	v_mfma_f32_16x16x32_bf16 v[42:45], v[156:159], v[172:175], v[42:45]
	v_mfma_f32_16x16x32_bf16 v[34:37], v[146:149], v[184:187], v[34:37]
	v_mfma_f32_16x16x32_bf16 v[26:29], v[156:159], v[184:187], v[26:29]
	v_mfma_f32_16x16x32_bf16 v[18:21], v[146:149], v[192:195], v[18:21]
	v_mfma_f32_16x16x32_bf16 v[10:13], v[156:159], v[192:195], v[10:13]
	v_mfma_f32_16x16x32_bf16 v[62:65], v[152:155], v[168:171], v[62:65]
	v_mfma_f32_16x16x32_bf16 v[58:61], v[160:163], v[168:171], v[58:61]
	v_mfma_f32_16x16x32_bf16 v[50:53], v[152:155], v[180:183], v[50:53]
	v_mfma_f32_16x16x32_bf16 v[42:45], v[160:163], v[180:183], v[42:45]
	v_mfma_f32_16x16x32_bf16 v[34:37], v[152:155], v[188:191], v[34:37]
	v_mfma_f32_16x16x32_bf16 v[26:29], v[160:163], v[188:191], v[26:29]
	v_mfma_f32_16x16x32_bf16 v[18:21], v[152:155], v[196:199], v[18:21]
	v_mfma_f32_16x16x32_bf16 v[10:13], v[160:163], v[196:199], v[10:13]
	s_barrier
	s_add_u32 s24, s28, 0x28000
	s_addc_u32 s25, s29, 0
	s_add_i32 s45, s46, s8
	s_mov_b32 m0, s45
	v_lshl_add_u64 v[146:147], s[24:25], 0, v[98:99]
	global_load_lds_dwordx4 v[146:147], off
	s_add_i32 m0, s45, 0x2000
	v_lshl_add_u64 v[146:147], s[24:25], 0, v[132:133]
	global_load_lds_dwordx4 v[146:147], off
	s_waitcnt vmcnt(6)
	s_barrier
	v_mfma_f32_16x16x32_bf16 v[54:57], v[200:203], v[164:167], v[54:57]
	v_mfma_f32_16x16x32_bf16 v[46:49], v[208:211], v[164:167], v[46:49]
	v_mfma_f32_16x16x32_bf16 v[38:41], v[200:203], v[172:175], v[38:41]
	v_mfma_f32_16x16x32_bf16 v[30:33], v[208:211], v[172:175], v[30:33]
	v_mfma_f32_16x16x32_bf16 v[22:25], v[200:203], v[184:187], v[22:25]
	v_mfma_f32_16x16x32_bf16 v[14:17], v[208:211], v[184:187], v[14:17]
	v_mfma_f32_16x16x32_bf16 v[6:9], v[200:203], v[192:195], v[6:9]
	v_mfma_f32_16x16x32_bf16 v[2:5], v[208:211], v[192:195], v[2:5]
	v_mfma_f32_16x16x32_bf16 v[54:57], v[204:207], v[168:171], v[54:57]
	v_mfma_f32_16x16x32_bf16 v[46:49], v[230:233], v[168:171], v[46:49]
	v_mfma_f32_16x16x32_bf16 v[38:41], v[204:207], v[180:183], v[38:41]
	v_mfma_f32_16x16x32_bf16 v[30:33], v[230:233], v[180:183], v[30:33]
	v_mfma_f32_16x16x32_bf16 v[22:25], v[204:207], v[188:191], v[22:25]
	v_mfma_f32_16x16x32_bf16 v[14:17], v[230:233], v[188:191], v[14:17]
	v_mfma_f32_16x16x32_bf16 v[6:9], v[204:207], v[196:199], v[6:9]
	v_mfma_f32_16x16x32_bf16 v[2:5], v[230:233], v[196:199], v[2:5]
	s_add_i32 s45, 0, 0x18000
	v_add_u32_e32 v142, s45, v143
	s_barrier
	ds_read_b128 v[146:149], v142
	ds_read_b128 v[152:155], v142 offset:1024
	ds_read_b128 v[156:159], v142 offset:2048
	ds_read_b128 v[160:163], v142 offset:3072
	s_add_u32 s24, s30, 0x190000
	s_addc_u32 s25, s31, 0
	s_mov_b32 m0, s21
	v_lshl_add_u64 v[200:201], s[24:25], 0, v[136:137]
	ds_read_b128 v[164:167], v151 offset:32768
	ds_read_b128 v[168:171], v151 offset:33792
	ds_read_b128 v[172:175], v151 offset:34816
	ds_read_b128 v[180:183], v151 offset:35840
	ds_read_b128 v[184:187], v151 offset:36864
	ds_read_b128 v[188:191], v151 offset:37888
	ds_read_b128 v[192:195], v151 offset:38912
	ds_read_b128 v[196:199], v151 offset:39936
	global_load_lds_dwordx4 v[200:201], off
	s_mov_b32 m0, s33
	v_lshl_add_u64 v[200:201], s[24:25], 0, v[134:135]
	global_load_lds_dwordx4 v[200:201], off
	s_waitcnt lgkmcnt(8)
	s_barrier
	s_waitcnt lgkmcnt(0)
	v_mfma_f32_16x16x32_bf16 v[128:131], v[146:149], v[164:167], v[128:131]
	v_mfma_f32_16x16x32_bf16 v[124:127], v[156:159], v[164:167], v[124:127]
	v_mfma_f32_16x16x32_bf16 v[112:115], v[146:149], v[172:175], v[112:115]
	v_mfma_f32_16x16x32_bf16 v[108:111], v[156:159], v[172:175], v[108:111]
	v_mfma_f32_16x16x32_bf16 v[94:97], v[146:149], v[184:187], v[94:97]
	v_mfma_f32_16x16x32_bf16 v[90:93], v[156:159], v[184:187], v[90:93]
	v_mfma_f32_16x16x32_bf16 v[78:81], v[146:149], v[192:195], v[78:81]
	v_mfma_f32_16x16x32_bf16 v[74:77], v[156:159], v[192:195], v[74:77]
	v_mfma_f32_16x16x32_bf16 v[128:131], v[152:155], v[168:171], v[128:131]
	v_mfma_f32_16x16x32_bf16 v[124:127], v[160:163], v[168:171], v[124:127]
	v_mfma_f32_16x16x32_bf16 v[112:115], v[152:155], v[180:183], v[112:115]
	v_mfma_f32_16x16x32_bf16 v[108:111], v[160:163], v[180:183], v[108:111]
	v_mfma_f32_16x16x32_bf16 v[94:97], v[152:155], v[188:191], v[94:97]
	v_mfma_f32_16x16x32_bf16 v[90:93], v[160:163], v[188:191], v[90:93]
	v_mfma_f32_16x16x32_bf16 v[78:81], v[152:155], v[196:199], v[78:81]
	v_mfma_f32_16x16x32_bf16 v[74:77], v[160:163], v[196:199], v[74:77]
	s_barrier
	s_add_i32 s30, 0, 0x1c000
	s_add_i32 s24, s45, s8
	v_add_u32_e32 v142, s30, v143
	v_lshl_add_u64 v[176:177], v[176:177], 0, s[68:69]
	s_mov_b32 m0, s24
	ds_read_b128 v[200:203], v142
	ds_read_b128 v[204:207], v142 offset:1024
	ds_read_b128 v[208:211], v142 offset:2048
	ds_read_b128 v[230:233], v142 offset:3072
	global_load_lds_dwordx4 v[176:177], off
	s_add_i32 m0, s24, 0x2000
	v_lshl_add_u64 v[176:177], v[178:179], 0, s[68:69]
	global_load_lds_dwordx4 v[176:177], off
	s_barrier
	s_waitcnt lgkmcnt(0)
	v_mfma_f32_16x16x32_bf16 v[120:123], v[200:203], v[164:167], v[120:123]
	v_mfma_f32_16x16x32_bf16 v[116:119], v[208:211], v[164:167], v[116:119]
	v_mfma_f32_16x16x32_bf16 v[104:107], v[200:203], v[172:175], v[104:107]
	v_mfma_f32_16x16x32_bf16 v[100:103], v[208:211], v[172:175], v[100:103]
	v_mfma_f32_16x16x32_bf16 v[86:89], v[200:203], v[184:187], v[86:89]
	v_mfma_f32_16x16x32_bf16 v[82:85], v[208:211], v[184:187], v[82:85]
	v_mfma_f32_16x16x32_bf16 v[70:73], v[200:203], v[192:195], v[70:73]
	v_mfma_f32_16x16x32_bf16 v[66:69], v[208:211], v[192:195], v[66:69]
	v_mfma_f32_16x16x32_bf16 v[120:123], v[204:207], v[168:171], v[120:123]
	v_mfma_f32_16x16x32_bf16 v[116:119], v[230:233], v[168:171], v[116:119]
	v_mfma_f32_16x16x32_bf16 v[104:107], v[204:207], v[180:183], v[104:107]
	v_mfma_f32_16x16x32_bf16 v[100:103], v[230:233], v[180:183], v[100:103]
	v_mfma_f32_16x16x32_bf16 v[86:89], v[204:207], v[188:191], v[86:89]
	v_mfma_f32_16x16x32_bf16 v[82:85], v[230:233], v[188:191], v[82:85]
	v_mfma_f32_16x16x32_bf16 v[70:73], v[204:207], v[196:199], v[70:73]
	v_mfma_f32_16x16x32_bf16 v[66:69], v[230:233], v[196:199], v[66:69]
	s_mov_b32 m0, s34
	v_lshl_add_u64 v[176:177], v[212:213], 0, s[68:69]
	s_barrier
	ds_read_b128 v[164:167], v151 offset:49152
	ds_read_b128 v[168:171], v151 offset:50176
	ds_read_b128 v[172:175], v151 offset:51200
	ds_read_b128 v[180:183], v151 offset:52224
	ds_read_b128 v[184:187], v151 offset:53248
	ds_read_b128 v[188:191], v151 offset:54272
	ds_read_b128 v[192:195], v151 offset:55296
	ds_read_b128 v[196:199], v151 offset:56320
	global_load_lds_dwordx4 v[176:177], off
	s_mov_b32 m0, s35
	v_lshl_add_u64 v[176:177], v[214:215], 0, s[68:69]
	global_load_lds_dwordx4 v[176:177], off
	s_barrier
	s_waitcnt lgkmcnt(0)
	v_mfma_f32_16x16x32_bf16 v[62:65], v[146:149], v[164:167], v[62:65]
	v_mfma_f32_16x16x32_bf16 v[58:61], v[156:159], v[164:167], v[58:61]
	v_mfma_f32_16x16x32_bf16 v[50:53], v[146:149], v[172:175], v[50:53]
	v_mfma_f32_16x16x32_bf16 v[42:45], v[156:159], v[172:175], v[42:45]
	v_mfma_f32_16x16x32_bf16 v[34:37], v[146:149], v[184:187], v[34:37]
	v_mfma_f32_16x16x32_bf16 v[26:29], v[156:159], v[184:187], v[26:29]
	v_mfma_f32_16x16x32_bf16 v[18:21], v[146:149], v[192:195], v[18:21]
	v_mfma_f32_16x16x32_bf16 v[10:13], v[156:159], v[192:195], v[10:13]
	v_mfma_f32_16x16x32_bf16 v[62:65], v[152:155], v[168:171], v[62:65]
	v_mfma_f32_16x16x32_bf16 v[58:61], v[160:163], v[168:171], v[58:61]
	v_mfma_f32_16x16x32_bf16 v[50:53], v[152:155], v[180:183], v[50:53]
	v_mfma_f32_16x16x32_bf16 v[42:45], v[160:163], v[180:183], v[42:45]
	v_mfma_f32_16x16x32_bf16 v[34:37], v[152:155], v[188:191], v[34:37]
	v_mfma_f32_16x16x32_bf16 v[26:29], v[160:163], v[188:191], v[26:29]
	v_mfma_f32_16x16x32_bf16 v[18:21], v[152:155], v[196:199], v[18:21]
	v_mfma_f32_16x16x32_bf16 v[10:13], v[160:163], v[196:199], v[10:13]
	s_barrier
	s_add_u32 s24, s28, 0x28080
	s_addc_u32 s25, s29, 0
	s_add_i32 s28, s30, s8
	s_mov_b32 m0, s28
	v_lshl_add_u64 v[146:147], s[24:25], 0, v[98:99]
	global_load_lds_dwordx4 v[146:147], off
	s_add_i32 m0, s28, 0x2000
	v_lshl_add_u64 v[146:147], s[24:25], 0, v[132:133]
	global_load_lds_dwordx4 v[146:147], off
	s_waitcnt vmcnt(6)
	s_barrier
	v_mfma_f32_16x16x32_bf16 v[54:57], v[200:203], v[164:167], v[54:57]
	v_mfma_f32_16x16x32_bf16 v[46:49], v[208:211], v[164:167], v[46:49]
	v_mfma_f32_16x16x32_bf16 v[38:41], v[200:203], v[172:175], v[38:41]
	v_mfma_f32_16x16x32_bf16 v[30:33], v[208:211], v[172:175], v[30:33]
	v_mfma_f32_16x16x32_bf16 v[22:25], v[200:203], v[184:187], v[22:25]
	v_mfma_f32_16x16x32_bf16 v[14:17], v[208:211], v[184:187], v[14:17]
	v_mfma_f32_16x16x32_bf16 v[6:9], v[200:203], v[192:195], v[6:9]
	v_mfma_f32_16x16x32_bf16 v[2:5], v[208:211], v[192:195], v[2:5]
	v_mfma_f32_16x16x32_bf16 v[54:57], v[204:207], v[168:171], v[54:57]
	v_mfma_f32_16x16x32_bf16 v[46:49], v[230:233], v[168:171], v[46:49]
	v_mfma_f32_16x16x32_bf16 v[38:41], v[204:207], v[180:183], v[38:41]
	v_mfma_f32_16x16x32_bf16 v[30:33], v[230:233], v[180:183], v[30:33]
	v_mfma_f32_16x16x32_bf16 v[22:25], v[204:207], v[188:191], v[22:25]
	v_mfma_f32_16x16x32_bf16 v[14:17], v[230:233], v[188:191], v[14:17]
	v_mfma_f32_16x16x32_bf16 v[6:9], v[204:207], v[196:199], v[6:9]
	v_mfma_f32_16x16x32_bf16 v[2:5], v[230:233], v[196:199], v[2:5]
	s_add_i32 s44, s44, 2
	s_add_u32 s42, s42, 0x100
	s_addc_u32 s43, s43, 0
	s_cmp_gt_u32 s44, 7
	s_mov_b64 s[24:25], s[26:27]
	s_barrier
	s_cbranch_scc0 .LBB0_690
	s_cmp_gt_i32 s40, 2
	s_cselect_b64 s[24:25], -1, 0
	v_cndmask_b32_e64 v142, 0, 1, s[24:25]
	v_lshl_add_u32 v153, s41, 8, v1
	v_lshl_or_b32 v146, v153, 1, v142
	v_readlane_b32 s24, v253, 3
	v_ashrrev_i32_e32 v147, 31, v146
	v_readlane_b32 s25, v253, 4
	v_or_b32_e32 v159, 16, v153
	v_or_b32_e32 v161, 32, v153
	v_lshl_add_u64 v[146:147], v[146:147], 2, s[24:25]
	global_load_dword v158, v[146:147], off
	v_lshl_or_b32 v146, v159, 1, v142
	v_ashrrev_i32_e32 v147, 31, v146
	v_lshl_add_u64 v[146:147], v[146:147], 2, s[24:25]
	global_load_dword v160, v[146:147], off
	v_lshl_or_b32 v146, v161, 1, v142
	v_ashrrev_i32_e32 v147, 31, v146
	v_lshl_add_u64 v[146:147], v[146:147], 2, s[24:25]
	v_or_b32_e32 v157, 48, v153
	global_load_dword v156, v[146:147], off
	v_lshl_or_b32 v146, v157, 1, v142
	v_ashrrev_i32_e32 v147, 31, v146
	v_lshl_add_u64 v[146:147], v[146:147], 2, s[24:25]
	global_load_dword v154, v[146:147], off
	v_add_u32_e32 v155, 0x80, v153
	v_lshl_or_b32 v146, v155, 1, v142
	v_ashrrev_i32_e32 v147, 31, v146
	v_lshl_add_u64 v[146:147], v[146:147], 2, s[24:25]
	global_load_dword v152, v[146:147], off
	global_load_dword v150, v[146:147], off offset:128
	global_load_dword v144, v[146:147], off offset:256
	global_load_dword v142, v[146:147], off offset:384
	v_readlane_b32 s24, v253, 7
	v_lshl_or_b32 v148, s40, 8, v145
	v_readlane_b32 s25, v253, 8
	v_ashrrev_i32_e32 v149, 31, v148
	v_lshlrev_b64 v[148:149], 1, v[148:149]
	v_mov_b64_e32 v[146:147], s[24:25]
	v_mad_i64_i32 v[162:163], s[24:25], v153, s49, v[146:147]
	v_lshl_add_u64 v[162:163], v[162:163], 0, v[148:149]
	s_and_b64 vcc, exec, s[0:1]
	s_mov_b32 s41, s39
	s_mov_b32 s40, s37
	s_mov_b64 s[26:27], s[22:23]
	s_waitcnt vmcnt(0)
	v_pk_mul_f32 v[130:131], v[130:131], v[158:159] op_sel_hi:[1,0]
	v_pk_mul_f32 v[128:129], v[128:129], v[158:159] op_sel_hi:[1,0]
	v_pk_mul_f32 v[164:165], v[126:127], v[158:159] op_sel_hi:[1,0]
	v_pk_mul_f32 v[126:127], v[124:125], v[158:159] op_sel_hi:[1,0]
	v_cvt_pk_bf16_f32 v124, v128, v129
	v_cvt_pk_bf16_f32 v125, v130, v131
	v_pk_mul_f32 v[122:123], v[122:123], v[158:159] op_sel_hi:[1,0]
	v_cvt_pk_bf16_f32 v126, v126, v127
	v_cvt_pk_bf16_f32 v127, v164, v165
	global_store_dwordx4 v[162:163], v[124:127], off
	v_pk_mul_f32 v[120:121], v[120:121], v[158:159] op_sel_hi:[1,0]
	v_pk_mul_f32 v[114:115], v[114:115], v[160:161] op_sel_hi:[1,0]
	v_pk_mul_f32 v[124:125], v[118:119], v[158:159] op_sel_hi:[1,0]
	v_pk_mul_f32 v[118:119], v[116:117], v[158:159] op_sel_hi:[1,0]
	v_cvt_pk_bf16_f32 v116, v120, v121
	v_cvt_pk_bf16_f32 v117, v122, v123
	v_pk_mul_f32 v[112:113], v[112:113], v[160:161] op_sel_hi:[1,0]
	v_cvt_pk_bf16_f32 v118, v118, v119
	v_cvt_pk_bf16_f32 v119, v124, v125
	global_store_dwordx4 v[162:163], v[116:119], off offset:256
	v_pk_mul_f32 v[106:107], v[106:107], v[160:161] op_sel_hi:[1,0]
	v_pk_mul_f32 v[104:105], v[104:105], v[160:161] op_sel_hi:[1,0]
	v_mad_i64_i32 v[116:117], s[24:25], v159, s49, v[146:147]
	v_lshl_add_u64 v[116:117], v[116:117], 0, v[148:149]
	v_pk_mul_f32 v[118:119], v[110:111], v[160:161] op_sel_hi:[1,0]
	v_pk_mul_f32 v[110:111], v[108:109], v[160:161] op_sel_hi:[1,0]
	v_cvt_pk_bf16_f32 v108, v112, v113
	v_cvt_pk_bf16_f32 v109, v114, v115
	v_pk_mul_f32 v[96:97], v[96:97], v[156:157] op_sel_hi:[1,0]
	v_cvt_pk_bf16_f32 v110, v110, v111
	v_cvt_pk_bf16_f32 v111, v118, v119
	global_store_dwordx4 v[116:117], v[108:111], off
	v_pk_mul_f32 v[94:95], v[94:95], v[156:157] op_sel_hi:[1,0]
	v_pk_mul_f32 v[88:89], v[88:89], v[156:157] op_sel_hi:[1,0]
	v_pk_mul_f32 v[108:109], v[102:103], v[160:161] op_sel_hi:[1,0]
	v_pk_mul_f32 v[102:103], v[100:101], v[160:161] op_sel_hi:[1,0]
	v_cvt_pk_bf16_f32 v100, v104, v105
	v_cvt_pk_bf16_f32 v101, v106, v107
	v_pk_mul_f32 v[86:87], v[86:87], v[156:157] op_sel_hi:[1,0]
	v_cvt_pk_bf16_f32 v102, v102, v103
	v_cvt_pk_bf16_f32 v103, v108, v109
	global_store_dwordx4 v[116:117], v[100:103], off offset:256
	v_pk_mul_f32 v[80:81], v[80:81], v[154:155] op_sel_hi:[1,0]
	v_pk_mul_f32 v[78:79], v[78:79], v[154:155] op_sel_hi:[1,0]
	v_mad_i64_i32 v[100:101], s[24:25], v161, s49, v[146:147]
	v_lshl_add_u64 v[100:101], v[100:101], 0, v[148:149]
	v_pk_mul_f32 v[102:103], v[92:93], v[156:157] op_sel_hi:[1,0]
	v_pk_mul_f32 v[92:93], v[90:91], v[156:157] op_sel_hi:[1,0]
	v_cvt_pk_bf16_f32 v90, v94, v95
	v_cvt_pk_bf16_f32 v91, v96, v97
	v_pk_mul_f32 v[72:73], v[72:73], v[154:155] op_sel_hi:[1,0]
	v_cvt_pk_bf16_f32 v92, v92, v93
	v_cvt_pk_bf16_f32 v93, v102, v103
	global_store_dwordx4 v[100:101], v[90:93], off
	v_pk_mul_f32 v[70:71], v[70:71], v[154:155] op_sel_hi:[1,0]
	v_pk_mul_f32 v[64:65], v[64:65], v[152:153] op_sel_hi:[1,0]
	v_pk_mul_f32 v[90:91], v[84:85], v[156:157] op_sel_hi:[1,0]
	v_pk_mul_f32 v[84:85], v[82:83], v[156:157] op_sel_hi:[1,0]
	v_cvt_pk_bf16_f32 v82, v86, v87
	v_cvt_pk_bf16_f32 v83, v88, v89
	v_pk_mul_f32 v[62:63], v[62:63], v[152:153] op_sel_hi:[1,0]
	v_cvt_pk_bf16_f32 v84, v84, v85
	v_cvt_pk_bf16_f32 v85, v90, v91
	global_store_dwordx4 v[100:101], v[82:85], off offset:256
	v_pk_mul_f32 v[54:55], v[54:55], v[152:153] op_sel_hi:[1,0]
	v_pk_mul_f32 v[56:57], v[56:57], v[152:153] op_sel_hi:[1,0]
	v_mad_i64_i32 v[82:83], s[24:25], v157, s49, v[146:147]
	v_lshl_add_u64 v[82:83], v[82:83], 0, v[148:149]
	v_pk_mul_f32 v[84:85], v[76:77], v[154:155] op_sel_hi:[1,0]
	v_pk_mul_f32 v[76:77], v[74:75], v[154:155] op_sel_hi:[1,0]
	v_cvt_pk_bf16_f32 v74, v78, v79
	v_cvt_pk_bf16_f32 v75, v80, v81
	v_pk_mul_f32 v[50:51], v[50:51], v[150:151] op_sel_hi:[1,0]
	v_cvt_pk_bf16_f32 v76, v76, v77
	v_cvt_pk_bf16_f32 v77, v84, v85
	global_store_dwordx4 v[82:83], v[74:77], off
	v_pk_mul_f32 v[38:39], v[38:39], v[150:151] op_sel_hi:[1,0]
	v_pk_mul_f32 v[40:41], v[40:41], v[150:151] op_sel_hi:[1,0]
	v_pk_mul_f32 v[74:75], v[68:69], v[154:155] op_sel_hi:[1,0]
	v_pk_mul_f32 v[68:69], v[66:67], v[154:155] op_sel_hi:[1,0]
	v_cvt_pk_bf16_f32 v66, v70, v71
	v_cvt_pk_bf16_f32 v67, v72, v73
	v_pk_mul_f32 v[34:35], v[34:35], v[144:145] op_sel_hi:[1,0]
	v_cvt_pk_bf16_f32 v68, v68, v69
	v_cvt_pk_bf16_f32 v69, v74, v75
	global_store_dwordx4 v[82:83], v[66:69], off offset:256
	v_pk_mul_f32 v[22:23], v[22:23], v[144:145] op_sel_hi:[1,0]
	v_pk_mul_f32 v[24:25], v[24:25], v[144:145] op_sel_hi:[1,0]
	v_mad_i64_i32 v[66:67], s[24:25], v155, s49, v[146:147]
	v_lshl_add_u64 v[66:67], v[66:67], 0, v[148:149]
	v_pk_mul_f32 v[68:69], v[60:61], v[152:153] op_sel_hi:[1,0]
	v_pk_mul_f32 v[60:61], v[58:59], v[152:153] op_sel_hi:[1,0]
	v_cvt_pk_bf16_f32 v58, v62, v63
	v_cvt_pk_bf16_f32 v59, v64, v65
	v_pk_mul_f32 v[18:19], v[18:19], v[142:143] op_sel_hi:[1,0]
	v_cvt_pk_bf16_f32 v60, v60, v61
	v_cvt_pk_bf16_f32 v61, v68, v69
	global_store_dwordx4 v[66:67], v[58:61], off
	v_pk_mul_f32 v[8:9], v[8:9], v[142:143] op_sel_hi:[1,0]
	v_pk_mul_f32 v[6:7], v[6:7], v[142:143] op_sel_hi:[1,0]
	v_pk_mul_f32 v[58:59], v[48:49], v[152:153] op_sel_hi:[1,0]
	v_pk_mul_f32 v[48:49], v[46:47], v[152:153] op_sel_hi:[1,0]
	v_cvt_pk_bf16_f32 v46, v54, v55
	v_cvt_pk_bf16_f32 v47, v56, v57
	s_nop 0
	v_cvt_pk_bf16_f32 v48, v48, v49
	v_cvt_pk_bf16_f32 v49, v58, v59
	global_store_dwordx4 v[66:67], v[46:49], off offset:256
	s_nop 1
	v_add_u32_e32 v46, 0x90, v153
	v_mad_i64_i32 v[46:47], s[24:25], v46, s49, v[146:147]
	v_lshl_add_u64 v[46:47], v[46:47], 0, v[148:149]
	v_pk_mul_f32 v[48:49], v[52:53], v[150:151] op_sel_hi:[1,0]
	v_pk_mul_f32 v[52:53], v[44:45], v[150:151] op_sel_hi:[1,0]
	v_pk_mul_f32 v[44:45], v[42:43], v[150:151] op_sel_hi:[1,0]
	v_cvt_pk_bf16_f32 v42, v50, v51
	v_cvt_pk_bf16_f32 v43, v48, v49
	s_nop 0
	v_cvt_pk_bf16_f32 v44, v44, v45
	v_cvt_pk_bf16_f32 v45, v52, v53
	global_store_dwordx4 v[46:47], v[42:45], off
	s_nop 1
	v_pk_mul_f32 v[42:43], v[32:33], v[150:151] op_sel_hi:[1,0]
	v_pk_mul_f32 v[32:33], v[30:31], v[150:151] op_sel_hi:[1,0]
	v_cvt_pk_bf16_f32 v30, v38, v39
	v_cvt_pk_bf16_f32 v31, v40, v41
	s_nop 0
	v_cvt_pk_bf16_f32 v32, v32, v33
	v_cvt_pk_bf16_f32 v33, v42, v43
	global_store_dwordx4 v[46:47], v[30:33], off offset:256
	s_nop 1
	v_add_u32_e32 v30, 0xa0, v153
	v_mad_i64_i32 v[30:31], s[24:25], v30, s49, v[146:147]
	v_lshl_add_u64 v[30:31], v[30:31], 0, v[148:149]
	v_pk_mul_f32 v[32:33], v[36:37], v[144:145] op_sel_hi:[1,0]
	v_pk_mul_f32 v[36:37], v[28:29], v[144:145] op_sel_hi:[1,0]
	v_pk_mul_f32 v[28:29], v[26:27], v[144:145] op_sel_hi:[1,0]
	v_cvt_pk_bf16_f32 v26, v34, v35
	v_cvt_pk_bf16_f32 v27, v32, v33
	s_nop 0
	v_cvt_pk_bf16_f32 v28, v28, v29
	v_cvt_pk_bf16_f32 v29, v36, v37
	global_store_dwordx4 v[30:31], v[26:29], off
	s_nop 1
	v_pk_mul_f32 v[26:27], v[16:17], v[144:145] op_sel_hi:[1,0]
	v_pk_mul_f32 v[16:17], v[14:15], v[144:145] op_sel_hi:[1,0]
	v_cvt_pk_bf16_f32 v14, v22, v23
	v_cvt_pk_bf16_f32 v15, v24, v25
	s_nop 0
	v_cvt_pk_bf16_f32 v16, v16, v17
	v_cvt_pk_bf16_f32 v17, v26, v27
	global_store_dwordx4 v[30:31], v[14:17], off offset:256
	s_nop 1
	v_add_u32_e32 v14, 0xb0, v153
	v_mad_i64_i32 v[14:15], s[24:25], v14, s49, v[146:147]
	v_lshl_add_u64 v[14:15], v[14:15], 0, v[148:149]
	v_pk_mul_f32 v[16:17], v[20:21], v[142:143] op_sel_hi:[1,0]
	v_pk_mul_f32 v[20:21], v[12:13], v[142:143] op_sel_hi:[1,0]
	v_pk_mul_f32 v[12:13], v[10:11], v[142:143] op_sel_hi:[1,0]
	v_cvt_pk_bf16_f32 v10, v18, v19
	v_cvt_pk_bf16_f32 v11, v16, v17
	s_mov_b64 s[24:25], s[18:19]
	v_cvt_pk_bf16_f32 v12, v12, v13
	v_cvt_pk_bf16_f32 v13, v20, v21
	global_store_dwordx4 v[14:15], v[10:13], off
	s_nop 1
	v_pk_mul_f32 v[10:11], v[4:5], v[142:143] op_sel_hi:[1,0]
	v_pk_mul_f32 v[4:5], v[2:3], v[142:143] op_sel_hi:[1,0]
	v_cvt_pk_bf16_f32 v2, v6, v7
	v_cvt_pk_bf16_f32 v3, v8, v9
	s_nop 0
	v_cvt_pk_bf16_f32 v4, v4, v5
	v_cvt_pk_bf16_f32 v5, v10, v11
	global_store_dwordx4 v[14:15], v[2:5], off offset:256
	s_cbranch_vccz .LBB0_683
	s_waitcnt vmcnt(0)
	s_cmpk_gt_u32 s3, 0xff
	s_cbranch_scc1 .LBB0_694
	s_barrier

.LBB0_1592:
	s_add_u32 s34, s30, 0xfff80080
	s_addc_u32 s35, s31, -1
	s_add_i32 s46, 0, 0x10000
	v_add_u32_e32 v86, s46, v160
	ds_read_b128 v[70:73], v86
	ds_read_b128 v[78:81], v86 offset:1024
	ds_read_b128 v[82:85], v86 offset:2048
	ds_read_b128 v[86:89], v86 offset:3072
	s_cmp_eq_u32 s45, 28
	s_cselect_b32 s37, s25, s35
	s_cselect_b32 s36, s41, s34
	s_cselect_b32 s35, s19, s44
	s_cselect_b32 s34, s42, s43
	v_lshl_add_u64 v[158:159], s[30:31], 0, v[150:151]
	s_add_i32 m0, s5, 0xc000
	ds_read_b128 v[154:157], v162
	ds_read_b128 v[164:167], v162 offset:1024
	ds_read_b128 v[168:171], v162 offset:2048
	ds_read_b128 v[172:175], v162 offset:3072
	ds_read_b128 v[176:179], v162 offset:4096
	ds_read_b128 v[180:183], v162 offset:5120
	ds_read_b128 v[184:187], v162 offset:6144
	ds_read_b128 v[188:191], v162 offset:7168
	global_load_lds_dwordx4 v[158:159], off
	s_add_i32 m0, s5, 0xe000
	v_lshl_add_u64 v[158:159], s[30:31], 0, v[152:153]
	global_load_lds_dwordx4 v[158:159], off
	s_waitcnt lgkmcnt(8)
	s_barrier
	s_waitcnt lgkmcnt(0)
	v_mfma_f32_16x16x32_bf16 v[144:147], v[70:73], v[154:157], v[144:147]
	v_mfma_f32_16x16x32_bf16 v[140:143], v[82:85], v[154:157], v[140:143]
	v_mfma_f32_16x16x32_bf16 v[128:131], v[70:73], v[168:171], v[128:131]
	v_mfma_f32_16x16x32_bf16 v[124:127], v[82:85], v[168:171], v[124:127]
	v_mfma_f32_16x16x32_bf16 v[112:115], v[70:73], v[176:179], v[112:115]
	v_mfma_f32_16x16x32_bf16 v[108:111], v[82:85], v[176:179], v[108:111]
	v_mfma_f32_16x16x32_bf16 v[94:97], v[70:73], v[184:187], v[94:97]
	v_mfma_f32_16x16x32_bf16 v[90:93], v[82:85], v[184:187], v[90:93]
	v_mfma_f32_16x16x32_bf16 v[144:147], v[78:81], v[164:167], v[144:147]
	v_mfma_f32_16x16x32_bf16 v[140:143], v[86:89], v[164:167], v[140:143]
	v_mfma_f32_16x16x32_bf16 v[128:131], v[78:81], v[172:175], v[128:131]
	v_mfma_f32_16x16x32_bf16 v[124:127], v[86:89], v[172:175], v[124:127]
	v_mfma_f32_16x16x32_bf16 v[112:115], v[78:81], v[180:183], v[112:115]
	v_mfma_f32_16x16x32_bf16 v[108:111], v[86:89], v[180:183], v[108:111]
	v_mfma_f32_16x16x32_bf16 v[94:97], v[78:81], v[188:191], v[94:97]
	v_mfma_f32_16x16x32_bf16 v[90:93], v[86:89], v[188:191], v[90:93]
	s_barrier
	s_add_i32 s48, 0, 0x14000
	v_add_u32_e32 v158, s48, v160
	s_add_i32 s46, s46, s4
	ds_read_b128 v[192:195], v158
	ds_read_b128 v[196:199], v158 offset:1024
	ds_read_b128 v[200:203], v158 offset:2048
	ds_read_b128 v[204:207], v158 offset:3072
	v_lshl_add_u64 v[158:159], s[34:35], 0, v[98:99]
	s_mov_b32 m0, s46
	v_lshl_add_u64 v[208:209], s[34:35], 0, v[148:149]
	global_load_lds_dwordx4 v[158:159], off
	s_add_i32 m0, s46, 0x2000
	s_nop 0
	global_load_lds_dwordx4 v[208:209], off
	s_barrier
	s_waitcnt lgkmcnt(0)
	v_mfma_f32_16x16x32_bf16 v[136:139], v[192:195], v[154:157], v[136:139]
	v_mfma_f32_16x16x32_bf16 v[132:135], v[200:203], v[154:157], v[132:135]
	v_mfma_f32_16x16x32_bf16 v[120:123], v[192:195], v[168:171], v[120:123]
	v_mfma_f32_16x16x32_bf16 v[116:119], v[200:203], v[168:171], v[116:119]
	v_mfma_f32_16x16x32_bf16 v[104:107], v[192:195], v[176:179], v[104:107]
	v_mfma_f32_16x16x32_bf16 v[100:103], v[200:203], v[176:179], v[100:103]
	v_mfma_f32_16x16x32_bf16 v[74:77], v[192:195], v[184:187], v[74:77]
	v_mfma_f32_16x16x32_bf16 v[66:69], v[200:203], v[184:187], v[66:69]
	v_mfma_f32_16x16x32_bf16 v[136:139], v[196:199], v[164:167], v[136:139]
	v_mfma_f32_16x16x32_bf16 v[132:135], v[204:207], v[164:167], v[132:135]
	v_mfma_f32_16x16x32_bf16 v[120:123], v[196:199], v[172:175], v[120:123]
	v_mfma_f32_16x16x32_bf16 v[116:119], v[204:207], v[172:175], v[116:119]
	v_mfma_f32_16x16x32_bf16 v[104:107], v[196:199], v[180:183], v[104:107]
	v_mfma_f32_16x16x32_bf16 v[100:103], v[204:207], v[180:183], v[100:103]
	v_mfma_f32_16x16x32_bf16 v[74:77], v[196:199], v[188:191], v[74:77]
	v_mfma_f32_16x16x32_bf16 v[66:69], v[204:207], v[188:191], v[66:69]
	s_mov_b32 m0, s5
	v_lshl_add_u64 v[210:211], s[36:37], 0, v[98:99]
	s_barrier
	ds_read_b128 v[154:157], v162 offset:16384
	ds_read_b128 v[164:167], v162 offset:17408
	ds_read_b128 v[168:171], v162 offset:18432
	ds_read_b128 v[172:175], v162 offset:19456
	ds_read_b128 v[176:179], v162 offset:20480
	ds_read_b128 v[180:183], v162 offset:21504
	ds_read_b128 v[184:187], v162 offset:22528
	ds_read_b128 v[188:191], v162 offset:23552
	global_load_lds_dwordx4 v[210:211], off
	s_mov_b32 m0, s8
	v_lshl_add_u64 v[212:213], s[36:37], 0, v[148:149]
	global_load_lds_dwordx4 v[212:213], off
	s_barrier
	s_waitcnt lgkmcnt(0)
	v_mfma_f32_16x16x32_bf16 v[62:65], v[70:73], v[154:157], v[62:65]
	v_mfma_f32_16x16x32_bf16 v[58:61], v[82:85], v[154:157], v[58:61]
	v_mfma_f32_16x16x32_bf16 v[46:49], v[70:73], v[168:171], v[46:49]
	v_mfma_f32_16x16x32_bf16 v[42:45], v[82:85], v[168:171], v[42:45]
	v_mfma_f32_16x16x32_bf16 v[30:33], v[70:73], v[176:179], v[30:33]
	v_mfma_f32_16x16x32_bf16 v[26:29], v[82:85], v[176:179], v[26:29]
	v_mfma_f32_16x16x32_bf16 v[22:25], v[70:73], v[184:187], v[22:25]
	v_mfma_f32_16x16x32_bf16 v[18:21], v[82:85], v[184:187], v[18:21]
	v_mfma_f32_16x16x32_bf16 v[62:65], v[78:81], v[164:167], v[62:65]
	v_mfma_f32_16x16x32_bf16 v[58:61], v[86:89], v[164:167], v[58:61]
	v_mfma_f32_16x16x32_bf16 v[46:49], v[78:81], v[172:175], v[46:49]
	v_mfma_f32_16x16x32_bf16 v[42:45], v[86:89], v[172:175], v[42:45]
	v_mfma_f32_16x16x32_bf16 v[30:33], v[78:81], v[180:183], v[30:33]
	v_mfma_f32_16x16x32_bf16 v[26:29], v[86:89], v[180:183], v[26:29]
	v_mfma_f32_16x16x32_bf16 v[22:25], v[78:81], v[188:191], v[22:25]
	v_mfma_f32_16x16x32_bf16 v[18:21], v[86:89], v[188:191], v[18:21]
	s_barrier
	s_add_u32 s46, s34, 0x80000
	s_addc_u32 s47, s35, 0
	s_add_i32 s48, s48, s4
	s_mov_b32 m0, s48
	v_lshl_add_u64 v[70:71], s[46:47], 0, v[98:99]
	global_load_lds_dwordx4 v[70:71], off
	s_add_i32 m0, s48, 0x2000
	v_lshl_add_u64 v[70:71], s[46:47], 0, v[148:149]
	global_load_lds_dwordx4 v[70:71], off
	s_waitcnt vmcnt(6)
	s_barrier
	v_mfma_f32_16x16x32_bf16 v[54:57], v[192:195], v[154:157], v[54:57]
	v_mfma_f32_16x16x32_bf16 v[50:53], v[200:203], v[154:157], v[50:53]
	v_mfma_f32_16x16x32_bf16 v[38:41], v[192:195], v[168:171], v[38:41]
	v_mfma_f32_16x16x32_bf16 v[34:37], v[200:203], v[168:171], v[34:37]
	v_mfma_f32_16x16x32_bf16 v[14:17], v[192:195], v[176:179], v[14:17]
	v_mfma_f32_16x16x32_bf16 v[10:13], v[200:203], v[176:179], v[10:13]
	v_mfma_f32_16x16x32_bf16 v[6:9], v[192:195], v[184:187], v[6:9]
	v_mfma_f32_16x16x32_bf16 v[2:5], v[200:203], v[184:187], v[2:5]
	v_mfma_f32_16x16x32_bf16 v[54:57], v[196:199], v[164:167], v[54:57]
	v_mfma_f32_16x16x32_bf16 v[50:53], v[204:207], v[164:167], v[50:53]
	v_mfma_f32_16x16x32_bf16 v[38:41], v[196:199], v[172:175], v[38:41]
	v_mfma_f32_16x16x32_bf16 v[34:37], v[204:207], v[172:175], v[34:37]
	v_mfma_f32_16x16x32_bf16 v[14:17], v[196:199], v[180:183], v[14:17]
	v_mfma_f32_16x16x32_bf16 v[10:13], v[204:207], v[180:183], v[10:13]
	v_mfma_f32_16x16x32_bf16 v[6:9], v[196:199], v[188:191], v[6:9]
	v_mfma_f32_16x16x32_bf16 v[2:5], v[204:207], v[188:191], v[2:5]
	s_add_i32 s46, 0, 0x18000
	v_add_u32_e32 v86, s46, v160
	s_barrier
	ds_read_b128 v[70:73], v86
	ds_read_b128 v[78:81], v86 offset:1024
	ds_read_b128 v[82:85], v86 offset:2048
	ds_read_b128 v[86:89], v86 offset:3072
	s_add_u32 s36, s36, 0x80000
	s_addc_u32 s37, s37, 0
	s_mov_b32 m0, s9
	v_lshl_add_u64 v[192:193], s[36:37], 0, v[98:99]
	ds_read_b128 v[154:157], v162 offset:32768
	ds_read_b128 v[164:167], v162 offset:33792
	ds_read_b128 v[168:171], v162 offset:34816
	ds_read_b128 v[172:175], v162 offset:35840
	ds_read_b128 v[176:179], v162 offset:36864
	ds_read_b128 v[180:183], v162 offset:37888
	ds_read_b128 v[184:187], v162 offset:38912
	ds_read_b128 v[188:191], v162 offset:39936
	global_load_lds_dwordx4 v[192:193], off
	s_mov_b32 m0, s20
	v_lshl_add_u64 v[192:193], s[36:37], 0, v[148:149]
	global_load_lds_dwordx4 v[192:193], off
	s_waitcnt lgkmcnt(8)
	s_barrier
	s_waitcnt lgkmcnt(0)
	v_mfma_f32_16x16x32_bf16 v[144:147], v[70:73], v[154:157], v[144:147]
	v_mfma_f32_16x16x32_bf16 v[140:143], v[82:85], v[154:157], v[140:143]
	v_mfma_f32_16x16x32_bf16 v[128:131], v[70:73], v[168:171], v[128:131]
	v_mfma_f32_16x16x32_bf16 v[124:127], v[82:85], v[168:171], v[124:127]
	v_mfma_f32_16x16x32_bf16 v[112:115], v[70:73], v[176:179], v[112:115]
	v_mfma_f32_16x16x32_bf16 v[108:111], v[82:85], v[176:179], v[108:111]
	v_mfma_f32_16x16x32_bf16 v[94:97], v[70:73], v[184:187], v[94:97]
	v_mfma_f32_16x16x32_bf16 v[90:93], v[82:85], v[184:187], v[90:93]
	v_mfma_f32_16x16x32_bf16 v[144:147], v[78:81], v[164:167], v[144:147]
	v_mfma_f32_16x16x32_bf16 v[140:143], v[86:89], v[164:167], v[140:143]
	v_mfma_f32_16x16x32_bf16 v[128:131], v[78:81], v[172:175], v[128:131]
	v_mfma_f32_16x16x32_bf16 v[124:127], v[86:89], v[172:175], v[124:127]
	v_mfma_f32_16x16x32_bf16 v[112:115], v[78:81], v[180:183], v[112:115]
	v_mfma_f32_16x16x32_bf16 v[108:111], v[86:89], v[180:183], v[108:111]
	v_mfma_f32_16x16x32_bf16 v[94:97], v[78:81], v[188:191], v[94:97]
	v_mfma_f32_16x16x32_bf16 v[90:93], v[86:89], v[188:191], v[90:93]
	s_barrier
	s_add_i32 s36, 0, 0x1c000
	s_add_i32 s37, s46, s4
	v_add_u32_e32 v163, s36, v160
	v_lshl_add_u64 v[158:159], v[158:159], 0, s[68:69]
	s_mov_b32 m0, s37
	ds_read_b128 v[192:195], v163
	ds_read_b128 v[196:199], v163 offset:1024
	ds_read_b128 v[200:203], v163 offset:2048
	ds_read_b128 v[204:207], v163 offset:3072
	global_load_lds_dwordx4 v[158:159], off
	s_add_i32 m0, s37, 0x2000
	v_lshl_add_u64 v[158:159], v[208:209], 0, s[68:69]
	global_load_lds_dwordx4 v[158:159], off
	s_barrier
	s_waitcnt lgkmcnt(0)
	v_mfma_f32_16x16x32_bf16 v[136:139], v[192:195], v[154:157], v[136:139]
	v_mfma_f32_16x16x32_bf16 v[132:135], v[200:203], v[154:157], v[132:135]
	v_mfma_f32_16x16x32_bf16 v[120:123], v[192:195], v[168:171], v[120:123]
	v_mfma_f32_16x16x32_bf16 v[116:119], v[200:203], v[168:171], v[116:119]
	v_mfma_f32_16x16x32_bf16 v[104:107], v[192:195], v[176:179], v[104:107]
	v_mfma_f32_16x16x32_bf16 v[100:103], v[200:203], v[176:179], v[100:103]
	v_mfma_f32_16x16x32_bf16 v[74:77], v[192:195], v[184:187], v[74:77]
	v_mfma_f32_16x16x32_bf16 v[66:69], v[200:203], v[184:187], v[66:69]
	v_mfma_f32_16x16x32_bf16 v[136:139], v[196:199], v[164:167], v[136:139]
	v_mfma_f32_16x16x32_bf16 v[132:135], v[204:207], v[164:167], v[132:135]
	v_mfma_f32_16x16x32_bf16 v[120:123], v[196:199], v[172:175], v[120:123]
	v_mfma_f32_16x16x32_bf16 v[116:119], v[204:207], v[172:175], v[116:119]
	v_mfma_f32_16x16x32_bf16 v[104:107], v[196:199], v[180:183], v[104:107]
	v_mfma_f32_16x16x32_bf16 v[100:103], v[204:207], v[180:183], v[100:103]
	v_mfma_f32_16x16x32_bf16 v[74:77], v[196:199], v[188:191], v[74:77]
	v_mfma_f32_16x16x32_bf16 v[66:69], v[204:207], v[188:191], v[66:69]
	s_mov_b32 m0, s21
	v_lshl_add_u64 v[158:159], v[210:211], 0, s[68:69]
	s_barrier
	ds_read_b128 v[154:157], v162 offset:49152
	ds_read_b128 v[164:167], v162 offset:50176
	ds_read_b128 v[168:171], v162 offset:51200
	ds_read_b128 v[172:175], v162 offset:52224
	ds_read_b128 v[176:179], v162 offset:53248
	ds_read_b128 v[180:183], v162 offset:54272
	ds_read_b128 v[184:187], v162 offset:55296
	ds_read_b128 v[188:191], v162 offset:56320
	global_load_lds_dwordx4 v[158:159], off
	s_mov_b32 m0, s33
	v_lshl_add_u64 v[158:159], v[212:213], 0, s[68:69]
	global_load_lds_dwordx4 v[158:159], off
	s_barrier
	s_waitcnt lgkmcnt(0)
	v_mfma_f32_16x16x32_bf16 v[62:65], v[70:73], v[154:157], v[62:65]
	v_mfma_f32_16x16x32_bf16 v[58:61], v[82:85], v[154:157], v[58:61]
	v_mfma_f32_16x16x32_bf16 v[46:49], v[70:73], v[168:171], v[46:49]
	v_mfma_f32_16x16x32_bf16 v[42:45], v[82:85], v[168:171], v[42:45]
	v_mfma_f32_16x16x32_bf16 v[30:33], v[70:73], v[176:179], v[30:33]
	v_mfma_f32_16x16x32_bf16 v[26:29], v[82:85], v[176:179], v[26:29]
	v_mfma_f32_16x16x32_bf16 v[22:25], v[70:73], v[184:187], v[22:25]
	v_mfma_f32_16x16x32_bf16 v[18:21], v[82:85], v[184:187], v[18:21]
	v_mfma_f32_16x16x32_bf16 v[62:65], v[78:81], v[164:167], v[62:65]
	v_mfma_f32_16x16x32_bf16 v[58:61], v[86:89], v[164:167], v[58:61]
	v_mfma_f32_16x16x32_bf16 v[46:49], v[78:81], v[172:175], v[46:49]
	v_mfma_f32_16x16x32_bf16 v[42:45], v[86:89], v[172:175], v[42:45]
	v_mfma_f32_16x16x32_bf16 v[30:33], v[78:81], v[180:183], v[30:33]
	v_mfma_f32_16x16x32_bf16 v[26:29], v[86:89], v[180:183], v[26:29]
	v_mfma_f32_16x16x32_bf16 v[22:25], v[78:81], v[188:191], v[22:25]
	v_mfma_f32_16x16x32_bf16 v[18:21], v[86:89], v[188:191], v[18:21]
	s_barrier
	s_add_u32 s34, s34, 0x80080
	s_addc_u32 s35, s35, 0
	s_add_i32 s36, s36, s4
	s_mov_b32 m0, s36
	v_lshl_add_u64 v[70:71], s[34:35], 0, v[98:99]
	global_load_lds_dwordx4 v[70:71], off
	s_add_i32 m0, s36, 0x2000
	v_lshl_add_u64 v[70:71], s[34:35], 0, v[148:149]
	global_load_lds_dwordx4 v[70:71], off
	s_waitcnt vmcnt(6)
	s_barrier
	v_mfma_f32_16x16x32_bf16 v[54:57], v[192:195], v[154:157], v[54:57]
	v_mfma_f32_16x16x32_bf16 v[50:53], v[200:203], v[154:157], v[50:53]
	v_mfma_f32_16x16x32_bf16 v[38:41], v[192:195], v[168:171], v[38:41]
	v_mfma_f32_16x16x32_bf16 v[34:37], v[200:203], v[168:171], v[34:37]
	v_mfma_f32_16x16x32_bf16 v[14:17], v[192:195], v[176:179], v[14:17]
	v_mfma_f32_16x16x32_bf16 v[10:13], v[200:203], v[176:179], v[10:13]
	v_mfma_f32_16x16x32_bf16 v[6:9], v[192:195], v[184:187], v[6:9]
	v_mfma_f32_16x16x32_bf16 v[2:5], v[200:203], v[184:187], v[2:5]
	v_mfma_f32_16x16x32_bf16 v[54:57], v[196:199], v[164:167], v[54:57]
	v_mfma_f32_16x16x32_bf16 v[50:53], v[204:207], v[164:167], v[50:53]
	v_mfma_f32_16x16x32_bf16 v[38:41], v[196:199], v[172:175], v[38:41]
	v_mfma_f32_16x16x32_bf16 v[34:37], v[204:207], v[172:175], v[34:37]
	v_mfma_f32_16x16x32_bf16 v[14:17], v[196:199], v[180:183], v[14:17]
	v_mfma_f32_16x16x32_bf16 v[10:13], v[204:207], v[180:183], v[10:13]
	v_mfma_f32_16x16x32_bf16 v[6:9], v[196:199], v[188:191], v[6:9]
	v_mfma_f32_16x16x32_bf16 v[2:5], v[204:207], v[188:191], v[2:5]
	s_add_i32 s45, s45, 2
	s_add_u32 s30, s30, 0x100
	s_addc_u32 s31, s31, 0
	s_add_u32 s43, s43, 0x100
	s_addc_u32 s44, s44, 0
	s_cmp_gt_u32 s45, 29
	s_barrier
	s_cbranch_scc0 .LBB0_1592
	v_lshl_or_b32 v70, s39, 8, v161
	v_lshl_add_u32 v154, s40, 8, v1
	v_ashrrev_i32_e32 v71, 31, v70
	v_readlane_b32 s30, v253, 28
	v_lshlrev_b64 v[156:157], 2, v[70:71]
	v_readlane_b32 s31, v253, 29
	v_ashrrev_i32_e32 v155, 31, v154
	v_lshlrev_b64 v[164:165], 13, v[154:155]
	v_lshl_add_u64 v[158:159], s[30:31], 0, v[156:157]
	v_lshl_add_u64 v[70:71], s[22:23], 0, v[156:157]
	v_lshl_add_u64 v[176:177], v[158:159], 0, v[164:165]
	global_load_dwordx4 v[86:89], v[70:71], off
	global_load_dwordx4 v[82:85], v[70:71], off offset:64
	global_load_dwordx4 v[78:81], v[70:71], off offset:512
	s_nop 0
	global_load_dwordx4 v[70:73], v[70:71], off offset:576
	s_nop 0
	global_load_dwordx4 v[164:167], v[176:177], off
	global_load_dwordx4 v[168:171], v[176:177], off offset:64
	global_load_dwordx4 v[172:175], v[176:177], off offset:512
	s_nop 0
	global_load_dwordx4 v[176:179], v[176:177], off offset:576
	v_or_b32_e32 v180, 16, v154
	v_ashrrev_i32_e32 v181, 31, v180
	v_lshlrev_b64 v[180:181], 13, v[180:181]
	v_lshl_add_u64 v[192:193], v[158:159], 0, v[180:181]
	global_load_dwordx4 v[180:183], v[192:193], off
	global_load_dwordx4 v[184:187], v[192:193], off offset:64
	global_load_dwordx4 v[188:191], v[192:193], off offset:512
	s_nop 0
	global_load_dwordx4 v[192:195], v[192:193], off offset:576
	v_add_u32_e32 v196, 0x100, v154
	v_ashrrev_i32_e32 v197, 31, v196
	v_lshlrev_b64 v[196:197], 13, v[196:197]
	v_lshl_add_u64 v[196:197], s[76:77], 0, v[196:197]
	v_lshl_add_u64 v[196:197], v[196:197], 0, v[156:157]
	s_and_b64 vcc, exec, s[0:1]
	s_mov_b32 s39, s18
	s_mov_b32 s40, s24
	s_mov_b64 s[34:35], s[28:29]
	s_mov_b64 s[30:31], s[26:27]
	s_waitcnt vmcnt(0)
	v_pk_fma_f32 v[146:147], v[146:147], v[88:89], v[166:167]
	v_pk_fma_f32 v[144:145], v[144:145], v[86:87], v[164:165]
	v_pk_fma_f32 v[142:143], v[142:143], v[84:85], v[170:171]
	v_pk_fma_f32 v[134:135], v[134:135], v[72:73], v[178:179]
	v_pk_fma_f32 v[132:133], v[132:133], v[70:71], v[176:177]
	global_store_dwordx4 v[196:197], v[132:135], off offset:576
	v_pk_fma_f32 v[140:141], v[140:141], v[82:83], v[168:169]
	v_pk_fma_f32 v[138:139], v[138:139], v[80:81], v[174:175]
	v_add_u32_e32 v132, 0x110, v154
	v_ashrrev_i32_e32 v133, 31, v132
	v_lshlrev_b64 v[132:133], 13, v[132:133]
	v_lshl_add_u64 v[132:133], s[76:77], 0, v[132:133]
	v_lshl_add_u64 v[132:133], v[132:133], 0, v[156:157]
	v_pk_fma_f32 v[118:119], v[118:119], v[72:73], v[194:195]
	v_pk_fma_f32 v[116:117], v[116:117], v[70:71], v[192:193]
	global_store_dwordx4 v[132:133], v[116:119], off offset:576
	v_pk_fma_f32 v[136:137], v[136:137], v[78:79], v[172:173]
	v_pk_fma_f32 v[130:131], v[130:131], v[88:89], v[182:183]
	v_or_b32_e32 v116, 32, v154
	v_ashrrev_i32_e32 v117, 31, v116
	v_pk_fma_f32 v[128:129], v[128:129], v[86:87], v[180:181]
	v_pk_fma_f32 v[126:127], v[126:127], v[84:85], v[186:187]
	v_pk_fma_f32 v[124:125], v[124:125], v[82:83], v[184:185]
	v_pk_fma_f32 v[122:123], v[122:123], v[80:81], v[190:191]
	v_pk_fma_f32 v[120:121], v[120:121], v[78:79], v[188:189]
	v_lshlrev_b64 v[116:117], 13, v[116:117]
	global_store_dwordx4 v[196:197], v[144:147], off
	global_store_dwordx4 v[196:197], v[140:143], off offset:64
	global_store_dwordx4 v[196:197], v[136:139], off offset:512
	global_store_dwordx4 v[132:133], v[128:131], off
	global_store_dwordx4 v[132:133], v[124:127], off offset:64
	global_store_dwordx4 v[132:133], v[120:123], off offset:512
	v_lshl_add_u64 v[128:129], v[158:159], 0, v[116:117]
	global_load_dwordx4 v[116:119], v[128:129], off
	global_load_dwordx4 v[120:123], v[128:129], off offset:64
	global_load_dwordx4 v[124:127], v[128:129], off offset:512
	s_nop 0
	global_load_dwordx4 v[128:131], v[128:129], off offset:576
	v_or_b32_e32 v132, 48, v154
	v_ashrrev_i32_e32 v133, 31, v132
	v_lshlrev_b64 v[132:133], 13, v[132:133]
	v_lshl_add_u64 v[144:145], v[158:159], 0, v[132:133]
	global_load_dwordx4 v[132:135], v[144:145], off
	global_load_dwordx4 v[136:139], v[144:145], off offset:64
	global_load_dwordx4 v[140:143], v[144:145], off offset:512
	s_nop 0
	global_load_dwordx4 v[144:147], v[144:145], off offset:576
	v_add_u32_e32 v164, 0x120, v154
	v_ashrrev_i32_e32 v165, 31, v164
	v_lshlrev_b64 v[164:165], 13, v[164:165]
	v_lshl_add_u64 v[164:165], s[76:77], 0, v[164:165]
	v_lshl_add_u64 v[164:165], v[164:165], 0, v[156:157]
	s_waitcnt vmcnt(0)
	v_pk_fma_f32 v[114:115], v[114:115], v[88:89], v[118:119]
	v_pk_fma_f32 v[112:113], v[112:113], v[86:87], v[116:117]
	v_pk_fma_f32 v[110:111], v[110:111], v[84:85], v[122:123]
	v_pk_fma_f32 v[102:103], v[102:103], v[72:73], v[130:131]
	v_pk_fma_f32 v[100:101], v[100:101], v[70:71], v[128:129]
	global_store_dwordx4 v[164:165], v[100:103], off offset:576
	v_pk_fma_f32 v[108:109], v[108:109], v[82:83], v[120:121]
	v_pk_fma_f32 v[106:107], v[106:107], v[80:81], v[126:127]
	v_add_u32_e32 v100, 0x130, v154
	v_ashrrev_i32_e32 v101, 31, v100
	v_lshlrev_b64 v[100:101], 13, v[100:101]
	v_lshl_add_u64 v[100:101], s[76:77], 0, v[100:101]
	v_lshl_add_u64 v[100:101], v[100:101], 0, v[156:157]
	v_pk_fma_f32 v[68:69], v[68:69], v[72:73], v[146:147]
	v_pk_fma_f32 v[66:67], v[66:67], v[70:71], v[144:145]
	global_store_dwordx4 v[100:101], v[66:69], off offset:576
	v_pk_fma_f32 v[104:105], v[104:105], v[78:79], v[124:125]
	v_pk_fma_f32 v[96:97], v[96:97], v[88:89], v[134:135]
	v_add_u32_e32 v66, 0x80, v154
	v_ashrrev_i32_e32 v67, 31, v66
	v_pk_fma_f32 v[94:95], v[94:95], v[86:87], v[132:133]
	v_pk_fma_f32 v[92:93], v[92:93], v[84:85], v[138:139]
	v_pk_fma_f32 v[90:91], v[90:91], v[82:83], v[136:137]
	v_pk_fma_f32 v[76:77], v[76:77], v[80:81], v[142:143]
	v_pk_fma_f32 v[74:75], v[74:75], v[78:79], v[140:141]
	v_lshlrev_b64 v[66:67], 13, v[66:67]
	global_store_dwordx4 v[164:165], v[112:115], off
	global_store_dwordx4 v[164:165], v[108:111], off offset:64
	global_store_dwordx4 v[164:165], v[104:107], off offset:512
	global_store_dwordx4 v[100:101], v[94:97], off
	global_store_dwordx4 v[100:101], v[90:93], off offset:64
	global_store_dwordx4 v[100:101], v[74:77], off offset:512
	v_lshl_add_u64 v[94:95], v[158:159], 0, v[66:67]
	global_load_dwordx4 v[66:69], v[94:95], off
	global_load_dwordx4 v[74:77], v[94:95], off offset:64
	global_load_dwordx4 v[90:93], v[94:95], off offset:512
	s_nop 0
	global_load_dwordx4 v[94:97], v[94:95], off offset:576
	v_add_u32_e32 v100, 0x90, v154
	v_ashrrev_i32_e32 v101, 31, v100
	v_lshlrev_b64 v[100:101], 13, v[100:101]
	v_lshl_add_u64 v[112:113], v[158:159], 0, v[100:101]
	global_load_dwordx4 v[100:103], v[112:113], off
	global_load_dwordx4 v[104:107], v[112:113], off offset:64
	global_load_dwordx4 v[108:111], v[112:113], off offset:512
	s_nop 0
	global_load_dwordx4 v[112:115], v[112:113], off offset:576
	v_add_u32_e32 v116, 0x180, v154
	v_ashrrev_i32_e32 v117, 31, v116
	v_lshlrev_b64 v[116:117], 13, v[116:117]
	v_lshl_add_u64 v[116:117], s[76:77], 0, v[116:117]
	v_lshl_add_u64 v[116:117], v[116:117], 0, v[156:157]
	s_waitcnt vmcnt(0)
	v_pk_fma_f32 v[64:65], v[64:65], v[88:89], v[68:69]
	v_pk_fma_f32 v[62:63], v[62:63], v[86:87], v[66:67]
	v_pk_fma_f32 v[60:61], v[60:61], v[84:85], v[76:77]
	v_pk_fma_f32 v[52:53], v[52:53], v[72:73], v[96:97]
	v_pk_fma_f32 v[50:51], v[50:51], v[70:71], v[94:95]
	global_store_dwordx4 v[116:117], v[50:53], off offset:576
	v_pk_fma_f32 v[58:59], v[58:59], v[82:83], v[74:75]
	v_pk_fma_f32 v[56:57], v[56:57], v[80:81], v[92:93]
	v_add_u32_e32 v50, 0x190, v154
	v_ashrrev_i32_e32 v51, 31, v50
	v_lshlrev_b64 v[50:51], 13, v[50:51]
	v_lshl_add_u64 v[50:51], s[76:77], 0, v[50:51]
	v_lshl_add_u64 v[50:51], v[50:51], 0, v[156:157]
	v_pk_fma_f32 v[36:37], v[36:37], v[72:73], v[114:115]
	v_pk_fma_f32 v[34:35], v[34:35], v[70:71], v[112:113]
	global_store_dwordx4 v[50:51], v[34:37], off offset:576
	v_pk_fma_f32 v[54:55], v[54:55], v[78:79], v[90:91]
	v_pk_fma_f32 v[48:49], v[48:49], v[88:89], v[102:103]
	v_add_u32_e32 v34, 0xa0, v154
	v_ashrrev_i32_e32 v35, 31, v34
	v_pk_fma_f32 v[46:47], v[46:47], v[86:87], v[100:101]
	v_pk_fma_f32 v[44:45], v[44:45], v[84:85], v[106:107]
	v_pk_fma_f32 v[42:43], v[42:43], v[82:83], v[104:105]
	v_pk_fma_f32 v[40:41], v[40:41], v[80:81], v[110:111]
	v_pk_fma_f32 v[38:39], v[38:39], v[78:79], v[108:109]
	v_lshlrev_b64 v[34:35], 13, v[34:35]
	global_store_dwordx4 v[116:117], v[62:65], off
	global_store_dwordx4 v[116:117], v[58:61], off offset:64
	global_store_dwordx4 v[116:117], v[54:57], off offset:512
	global_store_dwordx4 v[50:51], v[46:49], off
	global_store_dwordx4 v[50:51], v[42:45], off offset:64
	global_store_dwordx4 v[50:51], v[38:41], off offset:512
	v_lshl_add_u64 v[46:47], v[158:159], 0, v[34:35]
	global_load_dwordx4 v[34:37], v[46:47], off
	global_load_dwordx4 v[38:41], v[46:47], off offset:64
	global_load_dwordx4 v[42:45], v[46:47], off offset:512
	s_nop 0
	global_load_dwordx4 v[46:49], v[46:47], off offset:576
	v_add_u32_e32 v50, 0xb0, v154
	v_ashrrev_i32_e32 v51, 31, v50
	v_lshlrev_b64 v[50:51], 13, v[50:51]
	v_lshl_add_u64 v[62:63], v[158:159], 0, v[50:51]
	global_load_dwordx4 v[50:53], v[62:63], off
	global_load_dwordx4 v[54:57], v[62:63], off offset:64
	global_load_dwordx4 v[58:61], v[62:63], off offset:512
	s_nop 0
	global_load_dwordx4 v[62:65], v[62:63], off offset:576
	v_add_u32_e32 v66, 0x1a0, v154
	v_ashrrev_i32_e32 v67, 31, v66
	v_lshlrev_b64 v[66:67], 13, v[66:67]
	v_lshl_add_u64 v[66:67], s[76:77], 0, v[66:67]
	v_lshl_add_u64 v[66:67], v[66:67], 0, v[156:157]
	s_waitcnt vmcnt(0)
	v_pk_fma_f32 v[32:33], v[32:33], v[88:89], v[36:37]
	v_pk_fma_f32 v[30:31], v[30:31], v[86:87], v[34:35]
	v_pk_fma_f32 v[16:17], v[16:17], v[80:81], v[44:45]
	v_pk_fma_f32 v[12:13], v[12:13], v[72:73], v[48:49]
	v_pk_fma_f32 v[10:11], v[10:11], v[70:71], v[46:47]
	global_store_dwordx4 v[66:67], v[10:13], off offset:576
	v_pk_fma_f32 v[14:15], v[14:15], v[78:79], v[42:43]
	global_store_dwordx4 v[66:67], v[14:17], off offset:512
	v_add_u32_e32 v10, 0x1b0, v154
	v_ashrrev_i32_e32 v11, 31, v10
	v_lshlrev_b64 v[10:11], 13, v[10:11]
	v_lshl_add_u64 v[10:11], s[76:77], 0, v[10:11]
	v_lshl_add_u64 v[14:15], v[10:11], 0, v[156:157]
	v_pk_fma_f32 v[12:13], v[24:25], v[88:89], v[52:53]
	v_pk_fma_f32 v[10:11], v[22:23], v[86:87], v[50:51]
	v_pk_fma_f32 v[28:29], v[28:29], v[84:85], v[40:41]
	v_pk_fma_f32 v[26:27], v[26:27], v[82:83], v[38:39]
	global_store_dwordx4 v[14:15], v[10:13], off
	v_pk_fma_f32 v[8:9], v[8:9], v[80:81], v[60:61]
	v_pk_fma_f32 v[6:7], v[6:7], v[78:79], v[58:59]
	v_pk_fma_f32 v[12:13], v[20:21], v[84:85], v[56:57]
	v_pk_fma_f32 v[10:11], v[18:19], v[82:83], v[54:55]
	v_pk_fma_f32 v[4:5], v[4:5], v[72:73], v[64:65]
	v_pk_fma_f32 v[2:3], v[2:3], v[70:71], v[62:63]
	global_store_dwordx4 v[66:67], v[30:33], off
	global_store_dwordx4 v[66:67], v[26:29], off offset:64
	global_store_dwordx4 v[14:15], v[10:13], off offset:64
	global_store_dwordx4 v[14:15], v[6:9], off offset:512
	global_store_dwordx4 v[14:15], v[2:5], off offset:576
	s_cbranch_vccz .LBB0_1585
	s_waitcnt vmcnt(0)
	s_cmpk_gt_u32 s3, 0xff
	v_readlane_b32 s33, v255, 42
	s_cbranch_scc1 .LBB0_1596
	s_barrier

.LBB0_1616:
	s_add_i32 s50, s42, 2
	s_add_u32 s43, s40, 0xfff80080
	s_addc_u32 s44, s41, -1
	s_add_i32 s51, 0, 0x10000
	v_add_u32_e32 v144, s51, v1
	ds_read_b128 v[132:135], v144
	ds_read_b128 v[136:139], v144 offset:1024
	ds_read_b128 v[140:143], v144 offset:2048
	ds_read_b128 v[144:147], v144 offset:3072
	s_cmp_eq_u32 s47, s42
	s_cselect_b32 s42, s39, s48
	s_cselect_b32 s45, s1, s44
	s_cselect_b32 s44, s27, s43
	s_cselect_b32 s43, s25, s49
	v_lshl_add_u64 v[166:167], s[40:41], 0, v[154:155]
	s_add_i32 m0, s5, 0xc000
	ds_read_b128 v[158:161], v168
	ds_read_b128 v[162:165], v168 offset:1024
	ds_read_b128 v[170:173], v168 offset:2048
	ds_read_b128 v[174:177], v168 offset:3072
	ds_read_b128 v[178:181], v168 offset:4096
	ds_read_b128 v[182:185], v168 offset:5120
	ds_read_b128 v[186:189], v168 offset:6144
	ds_read_b128 v[190:193], v168 offset:7168
	global_load_lds_dwordx4 v[166:167], off
	s_add_i32 m0, s5, 0xe000
	v_lshl_add_u64 v[166:167], s[40:41], 0, v[156:157]
	global_load_lds_dwordx4 v[166:167], off
	s_waitcnt lgkmcnt(8)
	s_barrier
	s_waitcnt lgkmcnt(0)
	v_mfma_f32_16x16x32_bf16 v[128:131], v[132:135], v[158:161], v[128:131]
	v_mfma_f32_16x16x32_bf16 v[124:127], v[140:143], v[158:161], v[124:127]
	v_mfma_f32_16x16x32_bf16 v[120:123], v[132:135], v[170:173], v[120:123]
	v_mfma_f32_16x16x32_bf16 v[116:119], v[140:143], v[170:173], v[116:119]
	v_mfma_f32_16x16x32_bf16 v[108:111], v[132:135], v[178:181], v[108:111]
	v_mfma_f32_16x16x32_bf16 v[100:103], v[140:143], v[178:181], v[100:103]
	v_mfma_f32_16x16x32_bf16 v[90:93], v[132:135], v[186:189], v[90:93]
	v_mfma_f32_16x16x32_bf16 v[82:85], v[140:143], v[186:189], v[82:85]
	v_mfma_f32_16x16x32_bf16 v[128:131], v[136:139], v[162:165], v[128:131]
	v_mfma_f32_16x16x32_bf16 v[124:127], v[144:147], v[162:165], v[124:127]
	v_mfma_f32_16x16x32_bf16 v[120:123], v[136:139], v[174:177], v[120:123]
	v_mfma_f32_16x16x32_bf16 v[116:119], v[144:147], v[174:177], v[116:119]
	v_mfma_f32_16x16x32_bf16 v[108:111], v[136:139], v[182:185], v[108:111]
	v_mfma_f32_16x16x32_bf16 v[100:103], v[144:147], v[182:185], v[100:103]
	v_mfma_f32_16x16x32_bf16 v[90:93], v[136:139], v[190:193], v[90:93]
	v_mfma_f32_16x16x32_bf16 v[82:85], v[144:147], v[190:193], v[82:85]
	s_barrier
	s_add_i32 s64, 0, 0x14000
	v_add_u32_e32 v166, s64, v1
	s_add_i32 s51, s51, s4
	ds_read_b128 v[194:197], v166
	ds_read_b128 v[198:201], v166 offset:1024
	ds_read_b128 v[202:205], v166 offset:2048
	ds_read_b128 v[206:209], v166 offset:3072
	v_lshl_add_u64 v[166:167], s[42:43], 0, v[98:99]
	s_mov_b32 m0, s51
	v_lshl_add_u64 v[210:211], s[42:43], 0, v[148:149]
	global_load_lds_dwordx4 v[166:167], off
	s_add_i32 m0, s51, 0x2000
	s_nop 0
	global_load_lds_dwordx4 v[210:211], off
	s_barrier
	s_waitcnt lgkmcnt(0)
	v_mfma_f32_16x16x32_bf16 v[112:115], v[194:197], v[158:161], v[112:115]
	v_mfma_f32_16x16x32_bf16 v[104:107], v[202:205], v[158:161], v[104:107]
	v_mfma_f32_16x16x32_bf16 v[94:97], v[194:197], v[170:173], v[94:97]
	v_mfma_f32_16x16x32_bf16 v[86:89], v[202:205], v[170:173], v[86:89]
	v_mfma_f32_16x16x32_bf16 v[78:81], v[194:197], v[178:181], v[78:81]
	v_mfma_f32_16x16x32_bf16 v[74:77], v[202:205], v[178:181], v[74:77]
	v_mfma_f32_16x16x32_bf16 v[70:73], v[194:197], v[186:189], v[70:73]
	v_mfma_f32_16x16x32_bf16 v[66:69], v[202:205], v[186:189], v[66:69]
	v_mfma_f32_16x16x32_bf16 v[112:115], v[198:201], v[162:165], v[112:115]
	v_mfma_f32_16x16x32_bf16 v[104:107], v[206:209], v[162:165], v[104:107]
	v_mfma_f32_16x16x32_bf16 v[94:97], v[198:201], v[174:177], v[94:97]
	v_mfma_f32_16x16x32_bf16 v[86:89], v[206:209], v[174:177], v[86:89]
	v_mfma_f32_16x16x32_bf16 v[78:81], v[198:201], v[182:185], v[78:81]
	v_mfma_f32_16x16x32_bf16 v[74:77], v[206:209], v[182:185], v[74:77]
	v_mfma_f32_16x16x32_bf16 v[70:73], v[198:201], v[190:193], v[70:73]
	v_mfma_f32_16x16x32_bf16 v[66:69], v[206:209], v[190:193], v[66:69]
	s_mov_b32 m0, s5
	v_lshl_add_u64 v[212:213], s[44:45], 0, v[98:99]
	s_barrier
	ds_read_b128 v[158:161], v168 offset:16384
	ds_read_b128 v[162:165], v168 offset:17408
	ds_read_b128 v[170:173], v168 offset:18432
	ds_read_b128 v[174:177], v168 offset:19456
	ds_read_b128 v[178:181], v168 offset:20480
	ds_read_b128 v[182:185], v168 offset:21504
	ds_read_b128 v[186:189], v168 offset:22528
	ds_read_b128 v[190:193], v168 offset:23552
	global_load_lds_dwordx4 v[212:213], off
	s_mov_b32 m0, s8
	v_lshl_add_u64 v[214:215], s[44:45], 0, v[148:149]
	global_load_lds_dwordx4 v[214:215], off
	s_barrier
	s_waitcnt lgkmcnt(0)
	v_mfma_f32_16x16x32_bf16 v[62:65], v[132:135], v[158:161], v[62:65]
	v_mfma_f32_16x16x32_bf16 v[58:61], v[140:143], v[158:161], v[58:61]
	v_mfma_f32_16x16x32_bf16 v[54:57], v[132:135], v[170:173], v[54:57]
	v_mfma_f32_16x16x32_bf16 v[50:53], v[140:143], v[170:173], v[50:53]
	v_mfma_f32_16x16x32_bf16 v[42:45], v[132:135], v[178:181], v[42:45]
	v_mfma_f32_16x16x32_bf16 v[34:37], v[140:143], v[178:181], v[34:37]
	v_mfma_f32_16x16x32_bf16 v[26:29], v[132:135], v[186:189], v[26:29]
	v_mfma_f32_16x16x32_bf16 v[18:21], v[140:143], v[186:189], v[18:21]
	v_mfma_f32_16x16x32_bf16 v[62:65], v[136:139], v[162:165], v[62:65]
	v_mfma_f32_16x16x32_bf16 v[58:61], v[144:147], v[162:165], v[58:61]
	v_mfma_f32_16x16x32_bf16 v[54:57], v[136:139], v[174:177], v[54:57]
	v_mfma_f32_16x16x32_bf16 v[50:53], v[144:147], v[174:177], v[50:53]
	v_mfma_f32_16x16x32_bf16 v[42:45], v[136:139], v[182:185], v[42:45]
	v_mfma_f32_16x16x32_bf16 v[34:37], v[144:147], v[182:185], v[34:37]
	v_mfma_f32_16x16x32_bf16 v[26:29], v[136:139], v[190:193], v[26:29]
	v_mfma_f32_16x16x32_bf16 v[18:21], v[144:147], v[190:193], v[18:21]
	s_barrier
	s_add_u32 s52, s42, 0x80000
	s_addc_u32 s53, s43, 0
	s_add_i32 s51, s64, s4
	s_mov_b32 m0, s51
	v_lshl_add_u64 v[132:133], s[52:53], 0, v[98:99]
	global_load_lds_dwordx4 v[132:133], off
	s_add_i32 m0, s51, 0x2000
	v_lshl_add_u64 v[132:133], s[52:53], 0, v[148:149]
	global_load_lds_dwordx4 v[132:133], off
	s_waitcnt vmcnt(6)
	s_barrier
	v_mfma_f32_16x16x32_bf16 v[46:49], v[194:197], v[158:161], v[46:49]
	v_mfma_f32_16x16x32_bf16 v[38:41], v[202:205], v[158:161], v[38:41]
	v_mfma_f32_16x16x32_bf16 v[30:33], v[194:197], v[170:173], v[30:33]
	v_mfma_f32_16x16x32_bf16 v[22:25], v[202:205], v[170:173], v[22:25]
	v_mfma_f32_16x16x32_bf16 v[14:17], v[194:197], v[178:181], v[14:17]
	v_mfma_f32_16x16x32_bf16 v[10:13], v[202:205], v[178:181], v[10:13]
	v_mfma_f32_16x16x32_bf16 v[6:9], v[194:197], v[186:189], v[6:9]
	v_mfma_f32_16x16x32_bf16 v[2:5], v[202:205], v[186:189], v[2:5]
	v_mfma_f32_16x16x32_bf16 v[46:49], v[198:201], v[162:165], v[46:49]
	v_mfma_f32_16x16x32_bf16 v[38:41], v[206:209], v[162:165], v[38:41]
	v_mfma_f32_16x16x32_bf16 v[30:33], v[198:201], v[174:177], v[30:33]
	v_mfma_f32_16x16x32_bf16 v[22:25], v[206:209], v[174:177], v[22:25]
	v_mfma_f32_16x16x32_bf16 v[14:17], v[198:201], v[182:185], v[14:17]
	v_mfma_f32_16x16x32_bf16 v[10:13], v[206:209], v[182:185], v[10:13]
	v_mfma_f32_16x16x32_bf16 v[6:9], v[198:201], v[190:193], v[6:9]
	v_mfma_f32_16x16x32_bf16 v[2:5], v[206:209], v[190:193], v[2:5]
	s_add_i32 s51, 0, 0x18000
	v_add_u32_e32 v144, s51, v1
	s_barrier
	ds_read_b128 v[132:135], v144
	ds_read_b128 v[136:139], v144 offset:1024
	ds_read_b128 v[140:143], v144 offset:2048
	ds_read_b128 v[144:147], v144 offset:3072
	s_add_u32 s44, s44, 0x80000
	s_addc_u32 s45, s45, 0
	s_mov_b32 m0, s9
	v_lshl_add_u64 v[194:195], s[44:45], 0, v[98:99]
	ds_read_b128 v[158:161], v168 offset:32768
	ds_read_b128 v[162:165], v168 offset:33792
	ds_read_b128 v[170:173], v168 offset:34816
	ds_read_b128 v[174:177], v168 offset:35840
	ds_read_b128 v[178:181], v168 offset:36864
	ds_read_b128 v[182:185], v168 offset:37888
	ds_read_b128 v[186:189], v168 offset:38912
	ds_read_b128 v[190:193], v168 offset:39936
	global_load_lds_dwordx4 v[194:195], off
	s_mov_b32 m0, s18
	v_lshl_add_u64 v[194:195], s[44:45], 0, v[148:149]
	global_load_lds_dwordx4 v[194:195], off
	s_waitcnt lgkmcnt(8)
	s_barrier
	s_waitcnt lgkmcnt(0)
	v_mfma_f32_16x16x32_bf16 v[128:131], v[132:135], v[158:161], v[128:131]
	v_mfma_f32_16x16x32_bf16 v[124:127], v[140:143], v[158:161], v[124:127]
	v_mfma_f32_16x16x32_bf16 v[120:123], v[132:135], v[170:173], v[120:123]
	v_mfma_f32_16x16x32_bf16 v[116:119], v[140:143], v[170:173], v[116:119]
	v_mfma_f32_16x16x32_bf16 v[108:111], v[132:135], v[178:181], v[108:111]
	v_mfma_f32_16x16x32_bf16 v[100:103], v[140:143], v[178:181], v[100:103]
	v_mfma_f32_16x16x32_bf16 v[90:93], v[132:135], v[186:189], v[90:93]
	v_mfma_f32_16x16x32_bf16 v[82:85], v[140:143], v[186:189], v[82:85]
	v_mfma_f32_16x16x32_bf16 v[128:131], v[136:139], v[162:165], v[128:131]
	v_mfma_f32_16x16x32_bf16 v[124:127], v[144:147], v[162:165], v[124:127]
	v_mfma_f32_16x16x32_bf16 v[120:123], v[136:139], v[174:177], v[120:123]
	v_mfma_f32_16x16x32_bf16 v[116:119], v[144:147], v[174:177], v[116:119]
	v_mfma_f32_16x16x32_bf16 v[108:111], v[136:139], v[182:185], v[108:111]
	v_mfma_f32_16x16x32_bf16 v[100:103], v[144:147], v[182:185], v[100:103]
	v_mfma_f32_16x16x32_bf16 v[90:93], v[136:139], v[190:193], v[90:93]
	v_mfma_f32_16x16x32_bf16 v[82:85], v[144:147], v[190:193], v[82:85]
	s_barrier
	s_add_i32 s44, 0, 0x1c000
	s_add_i32 s45, s51, s4
	v_add_u32_e32 v169, s44, v1
	v_lshl_add_u64 v[166:167], v[166:167], 0, s[68:69]
	s_mov_b32 m0, s45
	ds_read_b128 v[194:197], v169
	ds_read_b128 v[198:201], v169 offset:1024
	ds_read_b128 v[202:205], v169 offset:2048
	ds_read_b128 v[206:209], v169 offset:3072
	global_load_lds_dwordx4 v[166:167], off
	s_add_i32 m0, s45, 0x2000
	v_lshl_add_u64 v[166:167], v[210:211], 0, s[68:69]
	global_load_lds_dwordx4 v[166:167], off
	s_barrier
	s_waitcnt lgkmcnt(0)
	v_mfma_f32_16x16x32_bf16 v[112:115], v[194:197], v[158:161], v[112:115]
	v_mfma_f32_16x16x32_bf16 v[104:107], v[202:205], v[158:161], v[104:107]
	v_mfma_f32_16x16x32_bf16 v[94:97], v[194:197], v[170:173], v[94:97]
	v_mfma_f32_16x16x32_bf16 v[86:89], v[202:205], v[170:173], v[86:89]
	v_mfma_f32_16x16x32_bf16 v[78:81], v[194:197], v[178:181], v[78:81]
	v_mfma_f32_16x16x32_bf16 v[74:77], v[202:205], v[178:181], v[74:77]
	v_mfma_f32_16x16x32_bf16 v[70:73], v[194:197], v[186:189], v[70:73]
	v_mfma_f32_16x16x32_bf16 v[66:69], v[202:205], v[186:189], v[66:69]
	v_mfma_f32_16x16x32_bf16 v[112:115], v[198:201], v[162:165], v[112:115]
	v_mfma_f32_16x16x32_bf16 v[104:107], v[206:209], v[162:165], v[104:107]
	v_mfma_f32_16x16x32_bf16 v[94:97], v[198:201], v[174:177], v[94:97]
	v_mfma_f32_16x16x32_bf16 v[86:89], v[206:209], v[174:177], v[86:89]
	v_mfma_f32_16x16x32_bf16 v[78:81], v[198:201], v[182:185], v[78:81]
	v_mfma_f32_16x16x32_bf16 v[74:77], v[206:209], v[182:185], v[74:77]
	v_mfma_f32_16x16x32_bf16 v[70:73], v[198:201], v[190:193], v[70:73]
	v_mfma_f32_16x16x32_bf16 v[66:69], v[206:209], v[190:193], v[66:69]
	s_mov_b32 m0, s19
	v_lshl_add_u64 v[166:167], v[212:213], 0, s[68:69]
	s_barrier
	ds_read_b128 v[158:161], v168 offset:49152
	ds_read_b128 v[162:165], v168 offset:50176
	ds_read_b128 v[170:173], v168 offset:51200
	ds_read_b128 v[174:177], v168 offset:52224
	ds_read_b128 v[178:181], v168 offset:53248
	ds_read_b128 v[182:185], v168 offset:54272
	ds_read_b128 v[186:189], v168 offset:55296
	ds_read_b128 v[190:193], v168 offset:56320
	global_load_lds_dwordx4 v[166:167], off
	s_mov_b32 m0, s20
	v_lshl_add_u64 v[166:167], v[214:215], 0, s[68:69]
	global_load_lds_dwordx4 v[166:167], off
	s_barrier
	s_waitcnt lgkmcnt(0)
	v_mfma_f32_16x16x32_bf16 v[62:65], v[132:135], v[158:161], v[62:65]
	v_mfma_f32_16x16x32_bf16 v[58:61], v[140:143], v[158:161], v[58:61]
	v_mfma_f32_16x16x32_bf16 v[54:57], v[132:135], v[170:173], v[54:57]
	v_mfma_f32_16x16x32_bf16 v[50:53], v[140:143], v[170:173], v[50:53]
	v_mfma_f32_16x16x32_bf16 v[42:45], v[132:135], v[178:181], v[42:45]
	v_mfma_f32_16x16x32_bf16 v[34:37], v[140:143], v[178:181], v[34:37]
	v_mfma_f32_16x16x32_bf16 v[26:29], v[132:135], v[186:189], v[26:29]
	v_mfma_f32_16x16x32_bf16 v[18:21], v[140:143], v[186:189], v[18:21]
	v_mfma_f32_16x16x32_bf16 v[62:65], v[136:139], v[162:165], v[62:65]
	v_mfma_f32_16x16x32_bf16 v[58:61], v[144:147], v[162:165], v[58:61]
	v_mfma_f32_16x16x32_bf16 v[54:57], v[136:139], v[174:177], v[54:57]
	v_mfma_f32_16x16x32_bf16 v[50:53], v[144:147], v[174:177], v[50:53]
	v_mfma_f32_16x16x32_bf16 v[42:45], v[136:139], v[182:185], v[42:45]
	v_mfma_f32_16x16x32_bf16 v[34:37], v[144:147], v[182:185], v[34:37]
	v_mfma_f32_16x16x32_bf16 v[26:29], v[136:139], v[190:193], v[26:29]
	v_mfma_f32_16x16x32_bf16 v[18:21], v[144:147], v[190:193], v[18:21]
	s_barrier
	s_add_u32 s42, s42, 0x80080
	s_addc_u32 s43, s43, 0
	s_add_i32 s44, s44, s4
	s_mov_b32 m0, s44
	v_lshl_add_u64 v[132:133], s[42:43], 0, v[98:99]
	global_load_lds_dwordx4 v[132:133], off
	s_add_i32 m0, s44, 0x2000
	v_lshl_add_u64 v[132:133], s[42:43], 0, v[148:149]
	global_load_lds_dwordx4 v[132:133], off
	s_waitcnt vmcnt(6)
	s_barrier
	v_mfma_f32_16x16x32_bf16 v[46:49], v[194:197], v[158:161], v[46:49]
	v_mfma_f32_16x16x32_bf16 v[38:41], v[202:205], v[158:161], v[38:41]
	v_mfma_f32_16x16x32_bf16 v[30:33], v[194:197], v[170:173], v[30:33]
	v_mfma_f32_16x16x32_bf16 v[22:25], v[202:205], v[170:173], v[22:25]
	v_mfma_f32_16x16x32_bf16 v[14:17], v[194:197], v[178:181], v[14:17]
	v_mfma_f32_16x16x32_bf16 v[10:13], v[202:205], v[178:181], v[10:13]
	v_mfma_f32_16x16x32_bf16 v[6:9], v[194:197], v[186:189], v[6:9]
	v_mfma_f32_16x16x32_bf16 v[2:5], v[202:205], v[186:189], v[2:5]
	v_mfma_f32_16x16x32_bf16 v[46:49], v[198:201], v[162:165], v[46:49]
	v_mfma_f32_16x16x32_bf16 v[38:41], v[206:209], v[162:165], v[38:41]
	v_mfma_f32_16x16x32_bf16 v[30:33], v[198:201], v[174:177], v[30:33]
	v_mfma_f32_16x16x32_bf16 v[22:25], v[206:209], v[174:177], v[22:25]
	v_mfma_f32_16x16x32_bf16 v[14:17], v[198:201], v[182:185], v[14:17]
	v_mfma_f32_16x16x32_bf16 v[10:13], v[206:209], v[182:185], v[10:13]
	v_mfma_f32_16x16x32_bf16 v[6:9], v[198:201], v[190:193], v[6:9]
	v_mfma_f32_16x16x32_bf16 v[2:5], v[206:209], v[190:193], v[2:5]
	s_add_u32 s40, s40, 0x100
	s_addc_u32 s41, s41, 0
	s_add_u32 s48, s48, 0x100
	s_addc_u32 s49, s49, 0
	s_cmp_ge_i32 s50, s46
	s_mov_b32 s42, s50
	s_barrier
	s_cbranch_scc0 .LBB0_1616
	v_lshl_or_b32 v158, s38, 8, v151
	v_ashrrev_i32_e32 v159, 31, v158
	s_cmp_lt_i32 s62, 0
	s_mov_b64 s[38:39], -1
	s_cbranch_scc0 .LBB0_1619
	v_lshl_add_u32 v162, s36, 8, v150
	v_add_u32_e32 v160, 0xffffff00, v162
	v_readlane_b32 s40, v251, 9
	v_lshlrev_b64 v[166:167], 2, v[158:159]
	v_readlane_b32 s41, v251, 10
	v_ashrrev_i32_e32 v161, 31, v160
	v_lshlrev_b64 v[160:161], 13, v[160:161]
	v_lshl_add_u64 v[164:165], s[40:41], 0, v[166:167]
	v_lshl_add_u64 v[132:133], s[22:23], 0, v[166:167]
	v_lshl_add_u64 v[160:161], v[164:165], 0, v[160:161]
	global_load_dwordx4 v[144:147], v[132:133], off
	global_load_dwordx4 v[140:143], v[132:133], off offset:64
	global_load_dwordx4 v[136:139], v[132:133], off offset:512
	s_nop 0
	global_load_dwordx4 v[132:135], v[132:133], off offset:576
	s_nop 0
	global_load_dwordx4 v[170:173], v[160:161], off
	global_load_dwordx4 v[174:177], v[160:161], off offset:64
	global_load_dwordx4 v[178:181], v[160:161], off offset:512
	global_load_dwordx4 v[182:185], v[160:161], off offset:576
	v_add_u32_e32 v160, 0xffffff10, v162
	v_ashrrev_i32_e32 v161, 31, v160
	v_lshlrev_b64 v[160:161], 13, v[160:161]
	v_lshl_add_u64 v[160:161], v[164:165], 0, v[160:161]
	global_load_dwordx4 v[186:189], v[160:161], off
	global_load_dwordx4 v[190:193], v[160:161], off offset:64
	global_load_dwordx4 v[194:197], v[160:161], off offset:512
	global_load_dwordx4 v[198:201], v[160:161], off offset:576
	v_ashrrev_i32_e32 v163, 31, v162
	v_lshlrev_b64 v[160:161], 13, v[162:163]
	v_lshl_add_u64 v[160:161], s[76:77], 0, v[160:161]
	v_lshl_add_u64 v[160:161], v[160:161], 0, v[166:167]
	v_or_b32_e32 v202, 32, v162
	v_ashrrev_i32_e32 v203, 31, v202
	v_lshlrev_b64 v[202:203], 13, v[202:203]
	v_lshl_add_u64 v[202:203], s[76:77], 0, v[202:203]
	v_lshl_add_u64 v[202:203], v[202:203], 0, v[166:167]
	s_mov_b32 s1, 0x100000
	s_mov_b64 s[38:39], 0x100000
	v_readlane_b32 s54, v251, 23
	v_readlane_b32 s55, v251, 24
	v_readlane_b32 s54, v255, 43
	v_readlane_b32 s42, v251, 11
	v_readlane_b32 s43, v251, 12
	v_readlane_b32 s44, v251, 13
	v_readlane_b32 s45, v251, 14
	v_readlane_b32 s46, v251, 15
	v_readlane_b32 s47, v251, 16
	v_readlane_b32 s48, v251, 17
	v_readlane_b32 s49, v251, 18
	v_readlane_b32 s50, v251, 19
	v_readlane_b32 s51, v251, 20
	v_readlane_b32 s52, v251, 21
	v_readlane_b32 s53, v251, 22
	v_readlane_b32 s55, v255, 44
	s_waitcnt vmcnt(0)
	v_pk_fma_f32 v[172:173], v[130:131], v[146:147], v[172:173]
	v_pk_fma_f32 v[170:171], v[128:129], v[144:145], v[170:171]
	global_store_dwordx4 v[160:161], v[170:173], off
	s_nop 1
	v_pk_fma_f32 v[172:173], v[126:127], v[142:143], v[176:177]
	v_pk_fma_f32 v[170:171], v[124:125], v[140:141], v[174:175]
	global_store_dwordx4 v[160:161], v[170:173], off offset:64
	s_nop 1
	v_pk_fma_f32 v[172:173], v[114:115], v[138:139], v[180:181]
	v_pk_fma_f32 v[170:171], v[112:113], v[136:137], v[178:179]
	global_store_dwordx4 v[160:161], v[170:173], off offset:512
	s_nop 1
	v_pk_fma_f32 v[172:173], v[106:107], v[134:135], v[184:185]
	v_pk_fma_f32 v[170:171], v[104:105], v[132:133], v[182:183]
	global_store_dwordx4 v[160:161], v[170:173], off offset:576
	s_nop 1
	v_or_b32_e32 v170, 16, v162
	v_ashrrev_i32_e32 v171, 31, v170
	v_lshlrev_b64 v[170:171], 13, v[170:171]
	v_lshl_add_u64 v[170:171], s[76:77], 0, v[170:171]
	v_lshl_add_u64 v[174:175], v[170:171], 0, v[166:167]
	v_pk_fma_f32 v[172:173], v[122:123], v[146:147], v[188:189]
	v_pk_fma_f32 v[170:171], v[120:121], v[144:145], v[186:187]
	global_store_dwordx4 v[174:175], v[170:173], off
	v_add_u32_e32 v186, 0xffffff30, v162
	v_ashrrev_i32_e32 v187, 31, v186
	v_pk_fma_f32 v[172:173], v[118:119], v[142:143], v[192:193]
	v_pk_fma_f32 v[170:171], v[116:117], v[140:141], v[190:191]
	global_store_dwordx4 v[174:175], v[170:173], off offset:64
	v_lshlrev_b64 v[186:187], 13, v[186:187]
	s_nop 0
	v_pk_fma_f32 v[172:173], v[96:97], v[138:139], v[196:197]
	v_pk_fma_f32 v[170:171], v[94:95], v[136:137], v[194:195]
	global_store_dwordx4 v[174:175], v[170:173], off offset:512
	s_nop 1
	v_pk_fma_f32 v[172:173], v[88:89], v[134:135], v[200:201]
	v_pk_fma_f32 v[170:171], v[86:87], v[132:133], v[198:199]
	global_store_dwordx4 v[174:175], v[170:173], off offset:576
	v_lshl_add_u64 v[198:199], v[164:165], 0, v[186:187]
	s_nop 0
	v_add_u32_e32 v170, 0xffffff20, v162
	v_ashrrev_i32_e32 v171, 31, v170
	v_lshlrev_b64 v[170:171], 13, v[170:171]
	v_lshl_add_u64 v[182:183], v[164:165], 0, v[170:171]
	global_load_dwordx4 v[170:173], v[182:183], off
	global_load_dwordx4 v[174:177], v[182:183], off offset:64
	global_load_dwordx4 v[178:181], v[182:183], off offset:512
	s_nop 0
	global_load_dwordx4 v[182:185], v[182:183], off offset:576
	s_nop 0
	global_load_dwordx4 v[186:189], v[198:199], off
	global_load_dwordx4 v[190:193], v[198:199], off offset:64
	global_load_dwordx4 v[194:197], v[198:199], off offset:512
	s_nop 0
	global_load_dwordx4 v[198:201], v[198:199], off offset:576
	s_waitcnt vmcnt(0)
	v_pk_fma_f32 v[172:173], v[110:111], v[146:147], v[172:173]
	v_pk_fma_f32 v[170:171], v[108:109], v[144:145], v[170:171]
	global_store_dwordx4 v[202:203], v[170:173], off
	s_nop 1
	v_pk_fma_f32 v[172:173], v[102:103], v[142:143], v[176:177]
	v_pk_fma_f32 v[170:171], v[100:101], v[140:141], v[174:175]
	global_store_dwordx4 v[202:203], v[170:173], off offset:64
	s_nop 1
	v_pk_fma_f32 v[172:173], v[80:81], v[138:139], v[180:181]
	v_pk_fma_f32 v[170:171], v[78:79], v[136:137], v[178:179]
	global_store_dwordx4 v[202:203], v[170:173], off offset:512
	s_nop 1
	v_pk_fma_f32 v[172:173], v[76:77], v[134:135], v[184:185]
	v_pk_fma_f32 v[170:171], v[74:75], v[132:133], v[182:183]
	global_store_dwordx4 v[202:203], v[170:173], off offset:576
	v_add_co_u32_e32 v202, vcc, s1, v160
	s_nop 0
	v_or_b32_e32 v170, 48, v162
	v_ashrrev_i32_e32 v171, 31, v170
	v_lshlrev_b64 v[170:171], 13, v[170:171]
	v_lshl_add_u64 v[170:171], s[76:77], 0, v[170:171]
	v_lshl_add_u64 v[166:167], v[170:171], 0, v[166:167]
	v_pk_fma_f32 v[172:173], v[92:93], v[146:147], v[188:189]
	v_pk_fma_f32 v[170:171], v[90:91], v[144:145], v[186:187]
	global_store_dwordx4 v[166:167], v[170:173], off
	v_addc_co_u32_e32 v203, vcc, 0, v161, vcc
	s_nop 0
	v_pk_fma_f32 v[172:173], v[84:85], v[142:143], v[192:193]
	v_pk_fma_f32 v[170:171], v[82:83], v[140:141], v[190:191]
	global_store_dwordx4 v[166:167], v[170:173], off offset:64
	s_mov_b32 s1, 0x120000
	s_nop 0
	v_pk_fma_f32 v[172:173], v[72:73], v[138:139], v[196:197]
	v_pk_fma_f32 v[170:171], v[70:71], v[136:137], v[194:195]
	global_store_dwordx4 v[166:167], v[170:173], off offset:512
	s_nop 1
	v_pk_fma_f32 v[172:173], v[68:69], v[134:135], v[200:201]
	v_pk_fma_f32 v[170:171], v[66:67], v[132:133], v[198:199]
	global_store_dwordx4 v[166:167], v[170:173], off offset:576
	v_add_u32_e32 v166, 0xffffff80, v162
	v_ashrrev_i32_e32 v167, 31, v166
	v_lshlrev_b64 v[166:167], 13, v[166:167]
	v_lshl_add_u64 v[166:167], v[164:165], 0, v[166:167]
	global_load_dwordx4 v[170:173], v[166:167], off
	global_load_dwordx4 v[174:177], v[166:167], off offset:64
	global_load_dwordx4 v[178:181], v[166:167], off offset:512
	global_load_dwordx4 v[182:185], v[166:167], off offset:576
	v_add_u32_e32 v166, 0xffffff90, v162
	v_ashrrev_i32_e32 v167, 31, v166
	v_lshlrev_b64 v[166:167], 13, v[166:167]
	v_lshl_add_u64 v[166:167], v[164:165], 0, v[166:167]
	global_load_dwordx4 v[186:189], v[166:167], off
	global_load_dwordx4 v[190:193], v[166:167], off offset:64
	global_load_dwordx4 v[194:197], v[166:167], off offset:512
	global_load_dwordx4 v[198:201], v[166:167], off offset:576
	v_lshl_add_u64 v[166:167], v[160:161], 0, s[38:39]
	s_mov_b64 s[38:39], 0x120000
	s_waitcnt vmcnt(0)
	v_pk_fma_f32 v[172:173], v[64:65], v[146:147], v[172:173]
	v_pk_fma_f32 v[170:171], v[62:63], v[144:145], v[170:171]
	global_store_dwordx4 v[202:203], v[170:173], off
	s_nop 1
	v_pk_fma_f32 v[172:173], v[60:61], v[142:143], v[176:177]
	v_pk_fma_f32 v[170:171], v[58:59], v[140:141], v[174:175]
	global_store_dwordx4 v[166:167], v[170:173], off offset:64
	v_add_co_u32_e32 v174, vcc, s1, v160
	s_nop 0
	v_pk_fma_f32 v[172:173], v[48:49], v[138:139], v[180:181]
	v_pk_fma_f32 v[170:171], v[46:47], v[136:137], v[178:179]
	global_store_dwordx4 v[166:167], v[170:173], off offset:512
	v_addc_co_u32_e32 v175, vcc, 0, v161, vcc
	s_nop 0
	v_pk_fma_f32 v[172:173], v[40:41], v[134:135], v[184:185]
	v_pk_fma_f32 v[170:171], v[38:39], v[132:133], v[182:183]
	global_store_dwordx4 v[166:167], v[170:173], off offset:576
	v_lshl_add_u64 v[166:167], v[160:161], 0, s[38:39]
	s_mov_b32 s1, 0x140000
	v_pk_fma_f32 v[172:173], v[56:57], v[146:147], v[188:189]
	v_pk_fma_f32 v[170:171], v[54:55], v[144:145], v[186:187]
	global_store_dwordx4 v[174:175], v[170:173], off
	s_mov_b64 s[38:39], 0x140000
	s_nop 0
	v_pk_fma_f32 v[172:173], v[52:53], v[142:143], v[192:193]
	v_pk_fma_f32 v[170:171], v[50:51], v[140:141], v[190:191]
	global_store_dwordx4 v[166:167], v[170:173], off offset:64
	s_nop 1
	v_pk_fma_f32 v[172:173], v[32:33], v[138:139], v[196:197]
	v_pk_fma_f32 v[170:171], v[30:31], v[136:137], v[194:195]
	global_store_dwordx4 v[166:167], v[170:173], off offset:512
	s_nop 1
	v_pk_fma_f32 v[172:173], v[24:25], v[134:135], v[200:201]
	v_pk_fma_f32 v[170:171], v[22:23], v[132:133], v[198:199]
	global_store_dwordx4 v[166:167], v[170:173], off offset:576
	v_add_u32_e32 v166, 0xffffffa0, v162
	v_ashrrev_i32_e32 v167, 31, v166
	v_lshlrev_b64 v[166:167], 13, v[166:167]
	v_add_u32_e32 v162, 0xffffffb0, v162
	v_lshl_add_u64 v[166:167], v[164:165], 0, v[166:167]
	v_ashrrev_i32_e32 v163, 31, v162
	global_load_dwordx4 v[170:173], v[166:167], off
	global_load_dwordx4 v[174:177], v[166:167], off offset:64
	global_load_dwordx4 v[178:181], v[166:167], off offset:512
	global_load_dwordx4 v[182:185], v[166:167], off offset:576
	v_lshlrev_b64 v[162:163], 13, v[162:163]
	v_lshl_add_u64 v[166:167], v[164:165], 0, v[162:163]
	global_load_dwordx4 v[162:165], v[166:167], off
	global_load_dwordx4 v[186:189], v[166:167], off offset:64
	global_load_dwordx4 v[190:193], v[166:167], off offset:512
	global_load_dwordx4 v[194:197], v[166:167], off offset:576
	v_add_co_u32_e32 v198, vcc, s1, v160
	v_lshl_add_u64 v[166:167], v[160:161], 0, s[38:39]
	s_nop 0
	v_addc_co_u32_e32 v199, vcc, 0, v161, vcc
	s_mov_b64 s[38:39], 0x160000
	s_mov_b32 s1, 0x160000
	s_waitcnt vmcnt(0)
	v_pk_fma_f32 v[172:173], v[44:45], v[146:147], v[172:173]
	v_pk_fma_f32 v[170:171], v[42:43], v[144:145], v[170:171]
	global_store_dwordx4 v[198:199], v[170:173], off
	v_pk_fma_f32 v[146:147], v[28:29], v[146:147], v[164:165]
	v_pk_fma_f32 v[144:145], v[26:27], v[144:145], v[162:163]
	v_pk_fma_f32 v[172:173], v[36:37], v[142:143], v[176:177]
	v_pk_fma_f32 v[170:171], v[34:35], v[140:141], v[174:175]
	global_store_dwordx4 v[166:167], v[170:173], off offset:64
	v_pk_fma_f32 v[142:143], v[20:21], v[142:143], v[188:189]
	v_pk_fma_f32 v[140:141], v[18:19], v[140:141], v[186:187]
	v_pk_fma_f32 v[172:173], v[16:17], v[138:139], v[180:181]
	v_pk_fma_f32 v[170:171], v[14:15], v[136:137], v[178:179]
	global_store_dwordx4 v[166:167], v[170:173], off offset:512
	v_pk_fma_f32 v[138:139], v[8:9], v[138:139], v[192:193]
	v_pk_fma_f32 v[136:137], v[6:7], v[136:137], v[190:191]
	v_pk_fma_f32 v[172:173], v[12:13], v[134:135], v[184:185]
	v_pk_fma_f32 v[170:171], v[10:11], v[132:133], v[182:183]
	global_store_dwordx4 v[166:167], v[170:173], off offset:576
	v_lshl_add_u64 v[166:167], v[160:161], 0, s[38:39]
	v_add_co_u32_e32 v160, vcc, s1, v160
	v_pk_fma_f32 v[134:135], v[4:5], v[134:135], v[196:197]
	s_nop 0
	v_addc_co_u32_e32 v161, vcc, 0, v161, vcc
	v_pk_fma_f32 v[132:133], v[2:3], v[132:133], v[194:195]
	global_store_dwordx4 v[160:161], v[144:147], off
	global_store_dwordx4 v[166:167], v[140:143], off offset:64
	global_store_dwordx4 v[166:167], v[136:139], off offset:512
	global_store_dwordx4 v[166:167], v[132:135], off offset:576
	s_mov_b64 s[38:39], 0

.LBB0_1870:
	s_add_u32 s36, s26, 0x100
	s_addc_u32 s37, s27, 0
	s_add_u32 s40, s31, s26
	s_addc_u32 s41, s20, s27
	s_cmpk_eq_i32 s26, 0x700
	s_cselect_b64 vcc, -1, 0
	s_and_b64 s[38:39], vcc, exec
	s_cselect_b32 s48, 0, s36
	s_cselect_b32 s45, 0, s37
	s_cselect_b32 s38, s24, s40
	s_cselect_b32 s39, s25, s41
	s_add_u32 s40, s94, s48
	s_addc_u32 s41, s95, s45
	s_add_i32 s45, 0, 0x10000
	v_add_u32_e32 v98, s45, v165
	ds_read_b128 v[148:151], v98
	ds_read_b128 v[154:157], v98 offset:1024
	ds_read_b128 v[176:179], v98 offset:2048
	ds_read_b128 v[182:185], v98 offset:3072
	v_lshl_add_u64 v[170:171], v[144:145], 0, s[26:27]
	s_add_i32 m0, s35, 0xc000
	ds_read_b128 v[186:189], v169
	ds_read_b128 v[190:193], v169 offset:1024
	ds_read_b128 v[194:197], v169 offset:2048
	ds_read_b128 v[198:201], v169 offset:3072
	ds_read_b128 v[202:205], v169 offset:4096
	ds_read_b128 v[206:209], v169 offset:5120
	ds_read_b128 v[210:213], v169 offset:6144
	ds_read_b128 v[214:217], v169 offset:7168
	global_load_lds_dwordx4 v[170:171], off
	s_add_i32 m0, s35, 0xe000
	v_lshl_add_u64 v[170:171], v[146:147], 0, s[26:27]
	global_load_lds_dwordx4 v[170:171], off
	s_waitcnt lgkmcnt(8)
	s_barrier
	s_waitcnt lgkmcnt(0)
	v_mfma_i32_16x16x64_i8 v[128:131], v[148:151], v[186:189], v[128:131]
	v_mfma_i32_16x16x64_i8 v[120:123], v[176:179], v[186:189], v[120:123]
	v_mfma_i32_16x16x64_i8 v[112:115], v[148:151], v[194:197], v[112:115]
	v_mfma_i32_16x16x64_i8 v[108:111], v[176:179], v[194:197], v[108:111]
	v_mfma_i32_16x16x64_i8 v[94:97], v[148:151], v[202:205], v[94:97]
	v_mfma_i32_16x16x64_i8 v[90:93], v[176:179], v[202:205], v[90:93]
	v_mfma_i32_16x16x64_i8 v[78:81], v[148:151], v[210:213], v[78:81]
	v_mfma_i32_16x16x64_i8 v[74:77], v[176:179], v[210:213], v[74:77]
	v_mfma_i32_16x16x64_i8 v[128:131], v[154:157], v[190:193], v[128:131]
	v_mfma_i32_16x16x64_i8 v[120:123], v[182:185], v[190:193], v[120:123]
	v_mfma_i32_16x16x64_i8 v[112:115], v[154:157], v[198:201], v[112:115]
	v_mfma_i32_16x16x64_i8 v[108:111], v[182:185], v[198:201], v[108:111]
	v_mfma_i32_16x16x64_i8 v[94:97], v[154:157], v[206:209], v[94:97]
	v_mfma_i32_16x16x64_i8 v[90:93], v[182:185], v[206:209], v[90:93]
	v_mfma_i32_16x16x64_i8 v[78:81], v[154:157], v[214:217], v[78:81]
	v_mfma_i32_16x16x64_i8 v[74:77], v[182:185], v[214:217], v[74:77]
	s_barrier
	s_add_i32 s48, 0, 0x14000
	s_add_i32 s26, s45, s93
	v_add_u32_e32 v98, s48, v165
	v_lshl_add_u64 v[170:171], s[38:39], 0, v[132:133]
	s_mov_b32 m0, s26
	ds_read_b128 v[222:225], v98
	ds_read_b128 v[230:233], v98 offset:1024
	ds_read_b128 v[236:239], v98 offset:2048
	ds_read_b128 v[240:243], v98 offset:3072
	global_load_lds_dwordx4 v[170:171], off
	s_add_i32 m0, s26, 0x2000
	v_lshl_add_u64 v[218:219], s[38:39], 0, v[134:135]
	global_load_lds_dwordx4 v[218:219], off
	s_barrier
	s_waitcnt lgkmcnt(0)
	v_mfma_i32_16x16x64_i8 v[124:127], v[222:225], v[186:189], v[124:127]
	v_mfma_i32_16x16x64_i8 v[116:119], v[236:239], v[186:189], v[116:119]
	v_mfma_i32_16x16x64_i8 v[104:107], v[222:225], v[194:197], v[104:107]
	v_mfma_i32_16x16x64_i8 v[100:103], v[236:239], v[194:197], v[100:103]
	v_mfma_i32_16x16x64_i8 v[86:89], v[222:225], v[202:205], v[86:89]
	v_mfma_i32_16x16x64_i8 v[82:85], v[236:239], v[202:205], v[82:85]
	v_mfma_i32_16x16x64_i8 v[70:73], v[222:225], v[210:213], v[70:73]
	v_mfma_i32_16x16x64_i8 v[66:69], v[236:239], v[210:213], v[66:69]
	v_mfma_i32_16x16x64_i8 v[124:127], v[230:233], v[190:193], v[124:127]
	v_mfma_i32_16x16x64_i8 v[116:119], v[240:243], v[190:193], v[116:119]
	v_mfma_i32_16x16x64_i8 v[104:107], v[230:233], v[198:201], v[104:107]
	v_mfma_i32_16x16x64_i8 v[100:103], v[240:243], v[198:201], v[100:103]
	v_mfma_i32_16x16x64_i8 v[86:89], v[230:233], v[206:209], v[86:89]
	v_mfma_i32_16x16x64_i8 v[82:85], v[240:243], v[206:209], v[82:85]
	v_mfma_i32_16x16x64_i8 v[70:73], v[230:233], v[214:217], v[70:73]
	v_mfma_i32_16x16x64_i8 v[66:69], v[240:243], v[214:217], v[66:69]
	s_mov_b32 m0, s35
	v_cndmask_b32_e32 v98, v136, v173, vcc
	s_barrier
	ds_read_b128 v[186:189], v169 offset:16384
	ds_read_b128 v[190:193], v169 offset:17408
	ds_read_b128 v[194:197], v169 offset:18432
	ds_read_b128 v[198:201], v169 offset:19456
	ds_read_b128 v[202:205], v169 offset:20480
	ds_read_b128 v[206:209], v169 offset:21504
	ds_read_b128 v[210:213], v169 offset:22528
	ds_read_b128 v[214:217], v169 offset:23552
	v_lshl_add_u64 v[244:245], s[40:41], 0, v[98:99]
	global_load_lds_dwordx4 v98, s[40:41]
	v_cndmask_b32_e32 v98, v138, v174, vcc
	s_mov_b32 m0, s18
	v_lshl_add_u64 v[246:247], s[40:41], 0, v[98:99]
	global_load_lds_dwordx4 v98, s[40:41]
	s_barrier
	s_waitcnt lgkmcnt(0)
	v_mfma_i32_16x16x64_i8 v[62:65], v[148:151], v[186:189], v[62:65]
	v_mfma_i32_16x16x64_i8 v[58:61], v[176:179], v[186:189], v[58:61]
	v_mfma_i32_16x16x64_i8 v[46:49], v[148:151], v[194:197], v[46:49]
	v_mfma_i32_16x16x64_i8 v[42:45], v[176:179], v[194:197], v[42:45]
	v_mfma_i32_16x16x64_i8 v[30:33], v[148:151], v[202:205], v[30:33]
	v_mfma_i32_16x16x64_i8 v[26:29], v[176:179], v[202:205], v[26:29]
	v_mfma_i32_16x16x64_i8 v[14:17], v[148:151], v[210:213], v[14:17]
	v_mfma_i32_16x16x64_i8 v[10:13], v[176:179], v[210:213], v[10:13]
	v_mfma_i32_16x16x64_i8 v[62:65], v[154:157], v[190:193], v[62:65]
	v_mfma_i32_16x16x64_i8 v[58:61], v[182:185], v[190:193], v[58:61]
	v_mfma_i32_16x16x64_i8 v[46:49], v[154:157], v[198:201], v[46:49]
	v_mfma_i32_16x16x64_i8 v[42:45], v[182:185], v[198:201], v[42:45]
	v_mfma_i32_16x16x64_i8 v[30:33], v[154:157], v[206:209], v[30:33]
	v_mfma_i32_16x16x64_i8 v[26:29], v[182:185], v[206:209], v[26:29]
	v_mfma_i32_16x16x64_i8 v[14:17], v[154:157], v[214:217], v[14:17]
	v_mfma_i32_16x16x64_i8 v[10:13], v[182:185], v[214:217], v[10:13]
	s_barrier
	s_add_u32 s26, s38, 0x40000
	s_addc_u32 s27, s39, 0
	s_add_i32 s45, s48, s93
	s_mov_b32 m0, s45
	v_lshl_add_u64 v[148:149], s[26:27], 0, v[132:133]
	global_load_lds_dwordx4 v[148:149], off
	s_add_i32 m0, s45, 0x2000
	v_lshl_add_u64 v[148:149], s[26:27], 0, v[134:135]
	global_load_lds_dwordx4 v[148:149], off
	s_waitcnt vmcnt(6)
	s_barrier
	v_mfma_i32_16x16x64_i8 v[54:57], v[222:225], v[186:189], v[54:57]
	v_mfma_i32_16x16x64_i8 v[50:53], v[236:239], v[186:189], v[50:53]
	v_mfma_i32_16x16x64_i8 v[38:41], v[222:225], v[194:197], v[38:41]
	v_mfma_i32_16x16x64_i8 v[34:37], v[236:239], v[194:197], v[34:37]
	v_mfma_i32_16x16x64_i8 v[22:25], v[222:225], v[202:205], v[22:25]
	v_mfma_i32_16x16x64_i8 v[18:21], v[236:239], v[202:205], v[18:21]
	v_mfma_i32_16x16x64_i8 v[6:9], v[222:225], v[210:213], v[6:9]
	v_mfma_i32_16x16x64_i8 v[2:5], v[236:239], v[210:213], v[2:5]
	v_mfma_i32_16x16x64_i8 v[54:57], v[230:233], v[190:193], v[54:57]
	v_mfma_i32_16x16x64_i8 v[50:53], v[240:243], v[190:193], v[50:53]
	v_mfma_i32_16x16x64_i8 v[38:41], v[230:233], v[198:201], v[38:41]
	v_mfma_i32_16x16x64_i8 v[34:37], v[240:243], v[198:201], v[34:37]
	v_mfma_i32_16x16x64_i8 v[22:25], v[230:233], v[206:209], v[22:25]
	v_mfma_i32_16x16x64_i8 v[18:21], v[240:243], v[206:209], v[18:21]
	v_mfma_i32_16x16x64_i8 v[6:9], v[230:233], v[214:217], v[6:9]
	v_mfma_i32_16x16x64_i8 v[2:5], v[240:243], v[214:217], v[2:5]
	s_add_i32 s26, 0, 0x18000
	v_add_u32_e32 v98, s26, v165
	s_barrier
	ds_read_b128 v[148:151], v98
	ds_read_b128 v[154:157], v98 offset:1024
	ds_read_b128 v[176:179], v98 offset:2048
	ds_read_b128 v[182:185], v98 offset:3072
	s_mov_b32 m0, s19
	v_cndmask_b32_e32 v98, v140, v175, vcc
	ds_read_b128 v[186:189], v169 offset:32768
	ds_read_b128 v[190:193], v169 offset:33792
	ds_read_b128 v[194:197], v169 offset:34816
	ds_read_b128 v[198:201], v169 offset:35840
	ds_read_b128 v[202:205], v169 offset:36864
	ds_read_b128 v[206:209], v169 offset:37888
	ds_read_b128 v[210:213], v169 offset:38912
	ds_read_b128 v[214:217], v169 offset:39936
	global_load_lds_dwordx4 v98, s[40:41]
	v_cndmask_b32_e32 v98, v142, v180, vcc
	s_mov_b32 m0, s92
	s_nop 0
	global_load_lds_dwordx4 v98, s[40:41]
	s_waitcnt lgkmcnt(8)
	s_barrier
	s_waitcnt lgkmcnt(0)
	v_mfma_i32_16x16x64_i8 v[128:131], v[148:151], v[186:189], v[128:131]
	v_mfma_i32_16x16x64_i8 v[120:123], v[176:179], v[186:189], v[120:123]
	v_mfma_i32_16x16x64_i8 v[112:115], v[148:151], v[194:197], v[112:115]
	v_mfma_i32_16x16x64_i8 v[108:111], v[176:179], v[194:197], v[108:111]
	v_mfma_i32_16x16x64_i8 v[94:97], v[148:151], v[202:205], v[94:97]
	v_mfma_i32_16x16x64_i8 v[90:93], v[176:179], v[202:205], v[90:93]
	v_mfma_i32_16x16x64_i8 v[78:81], v[148:151], v[210:213], v[78:81]
	v_mfma_i32_16x16x64_i8 v[74:77], v[176:179], v[210:213], v[74:77]
	v_mfma_i32_16x16x64_i8 v[128:131], v[154:157], v[190:193], v[128:131]
	v_mfma_i32_16x16x64_i8 v[120:123], v[182:185], v[190:193], v[120:123]
	v_mfma_i32_16x16x64_i8 v[112:115], v[154:157], v[198:201], v[112:115]
	v_mfma_i32_16x16x64_i8 v[108:111], v[182:185], v[198:201], v[108:111]
	v_mfma_i32_16x16x64_i8 v[94:97], v[154:157], v[206:209], v[94:97]
	v_mfma_i32_16x16x64_i8 v[90:93], v[182:185], v[206:209], v[90:93]
	v_mfma_i32_16x16x64_i8 v[78:81], v[154:157], v[214:217], v[78:81]
	v_mfma_i32_16x16x64_i8 v[74:77], v[182:185], v[214:217], v[74:77]
	s_barrier
	s_add_i32 s40, 0, 0x1c000
	s_add_i32 s26, s26, s93
	v_add_u32_e32 v98, s40, v165
	v_lshl_add_u64 v[170:171], v[170:171], 0, s[68:69]
	s_mov_b32 m0, s26
	ds_read_b128 v[222:225], v98
	ds_read_b128 v[230:233], v98 offset:1024
	ds_read_b128 v[236:239], v98 offset:2048
	ds_read_b128 v[240:243], v98 offset:3072
	global_load_lds_dwordx4 v[170:171], off
	s_add_i32 m0, s26, 0x2000
	v_lshl_add_u64 v[170:171], v[218:219], 0, s[68:69]
	global_load_lds_dwordx4 v[170:171], off
	s_barrier
	s_waitcnt lgkmcnt(0)
	v_mfma_i32_16x16x64_i8 v[124:127], v[222:225], v[186:189], v[124:127]
	v_mfma_i32_16x16x64_i8 v[116:119], v[236:239], v[186:189], v[116:119]
	v_mfma_i32_16x16x64_i8 v[104:107], v[222:225], v[194:197], v[104:107]
	v_mfma_i32_16x16x64_i8 v[100:103], v[236:239], v[194:197], v[100:103]
	v_mfma_i32_16x16x64_i8 v[86:89], v[222:225], v[202:205], v[86:89]
	v_mfma_i32_16x16x64_i8 v[82:85], v[236:239], v[202:205], v[82:85]
	v_mfma_i32_16x16x64_i8 v[70:73], v[222:225], v[210:213], v[70:73]
	v_mfma_i32_16x16x64_i8 v[66:69], v[236:239], v[210:213], v[66:69]
	v_mfma_i32_16x16x64_i8 v[124:127], v[230:233], v[190:193], v[124:127]
	v_mfma_i32_16x16x64_i8 v[116:119], v[240:243], v[190:193], v[116:119]
	v_mfma_i32_16x16x64_i8 v[104:107], v[230:233], v[198:201], v[104:107]
	v_mfma_i32_16x16x64_i8 v[100:103], v[240:243], v[198:201], v[100:103]
	v_mfma_i32_16x16x64_i8 v[86:89], v[230:233], v[206:209], v[86:89]
	v_mfma_i32_16x16x64_i8 v[82:85], v[240:243], v[206:209], v[82:85]
	v_mfma_i32_16x16x64_i8 v[70:73], v[230:233], v[214:217], v[70:73]
	v_mfma_i32_16x16x64_i8 v[66:69], v[240:243], v[214:217], v[66:69]
	s_mov_b32 m0, s3
	v_lshl_add_u64 v[170:171], v[244:245], 0, s[68:69]
	s_barrier
	ds_read_b128 v[186:189], v169 offset:49152
	ds_read_b128 v[190:193], v169 offset:50176
	ds_read_b128 v[194:197], v169 offset:51200
	ds_read_b128 v[198:201], v169 offset:52224
	ds_read_b128 v[202:205], v169 offset:53248
	ds_read_b128 v[206:209], v169 offset:54272
	ds_read_b128 v[210:213], v169 offset:55296
	ds_read_b128 v[214:217], v169 offset:56320
	global_load_lds_dwordx4 v[170:171], off
	s_mov_b32 m0, s74
	v_lshl_add_u64 v[170:171], v[246:247], 0, s[68:69]
	global_load_lds_dwordx4 v[170:171], off
	s_barrier
	s_waitcnt lgkmcnt(0)
	v_mfma_i32_16x16x64_i8 v[62:65], v[148:151], v[186:189], v[62:65]
	v_mfma_i32_16x16x64_i8 v[58:61], v[176:179], v[186:189], v[58:61]
	v_mfma_i32_16x16x64_i8 v[46:49], v[148:151], v[194:197], v[46:49]
	v_mfma_i32_16x16x64_i8 v[42:45], v[176:179], v[194:197], v[42:45]
	v_mfma_i32_16x16x64_i8 v[30:33], v[148:151], v[202:205], v[30:33]
	v_mfma_i32_16x16x64_i8 v[26:29], v[176:179], v[202:205], v[26:29]
	v_mfma_i32_16x16x64_i8 v[14:17], v[148:151], v[210:213], v[14:17]
	v_mfma_i32_16x16x64_i8 v[10:13], v[176:179], v[210:213], v[10:13]
	v_mfma_i32_16x16x64_i8 v[62:65], v[154:157], v[190:193], v[62:65]
	v_mfma_i32_16x16x64_i8 v[58:61], v[182:185], v[190:193], v[58:61]
	v_mfma_i32_16x16x64_i8 v[46:49], v[154:157], v[198:201], v[46:49]
	v_mfma_i32_16x16x64_i8 v[42:45], v[182:185], v[198:201], v[42:45]
	v_mfma_i32_16x16x64_i8 v[30:33], v[154:157], v[206:209], v[30:33]
	v_mfma_i32_16x16x64_i8 v[26:29], v[182:185], v[206:209], v[26:29]
	v_mfma_i32_16x16x64_i8 v[14:17], v[154:157], v[214:217], v[14:17]
	v_mfma_i32_16x16x64_i8 v[10:13], v[182:185], v[214:217], v[10:13]
	s_barrier
	s_add_u32 s26, s38, 0x40080
	s_addc_u32 s27, s39, 0
	s_add_i32 s38, s40, s93
	s_mov_b32 m0, s38
	v_lshl_add_u64 v[148:149], s[26:27], 0, v[132:133]
	global_load_lds_dwordx4 v[148:149], off
	s_add_i32 m0, s38, 0x2000
	v_lshl_add_u64 v[148:149], s[26:27], 0, v[134:135]
	global_load_lds_dwordx4 v[148:149], off
	s_waitcnt vmcnt(6)
	s_barrier
	v_mfma_i32_16x16x64_i8 v[54:57], v[222:225], v[186:189], v[54:57]
	v_mfma_i32_16x16x64_i8 v[50:53], v[236:239], v[186:189], v[50:53]
	v_mfma_i32_16x16x64_i8 v[38:41], v[222:225], v[194:197], v[38:41]
	v_mfma_i32_16x16x64_i8 v[34:37], v[236:239], v[194:197], v[34:37]
	v_mfma_i32_16x16x64_i8 v[22:25], v[222:225], v[202:205], v[22:25]
	v_mfma_i32_16x16x64_i8 v[18:21], v[236:239], v[202:205], v[18:21]
	v_mfma_i32_16x16x64_i8 v[6:9], v[222:225], v[210:213], v[6:9]
	v_mfma_i32_16x16x64_i8 v[2:5], v[236:239], v[210:213], v[2:5]
	v_mfma_i32_16x16x64_i8 v[54:57], v[230:233], v[190:193], v[54:57]
	v_mfma_i32_16x16x64_i8 v[50:53], v[240:243], v[190:193], v[50:53]
	v_mfma_i32_16x16x64_i8 v[38:41], v[230:233], v[198:201], v[38:41]
	v_mfma_i32_16x16x64_i8 v[34:37], v[240:243], v[198:201], v[34:37]
	v_mfma_i32_16x16x64_i8 v[22:25], v[230:233], v[206:209], v[22:25]
	v_mfma_i32_16x16x64_i8 v[18:21], v[240:243], v[206:209], v[18:21]
	v_mfma_i32_16x16x64_i8 v[6:9], v[230:233], v[214:217], v[6:9]
	v_mfma_i32_16x16x64_i8 v[2:5], v[240:243], v[214:217], v[2:5]
	s_add_i32 s42, s42, 2
	s_cmp_gt_u32 s42, 13
	s_mov_b64 s[26:27], s[36:37]
	s_barrier
	s_cbranch_scc0 .LBB0_1870
	v_lshl_add_u32 v136, s71, 8, v163
	v_readlane_b32 s26, v253, 52
	v_ashrrev_i32_e32 v137, 31, v136
	v_readlane_b32 s27, v253, 53
	s_mul_hi_i32 s20, s9, 0xb000
	s_mul_i32 s9, s9, 0xb000
	v_lshl_add_u64 v[138:139], v[136:137], 2, s[26:27]
	v_readlane_b32 s26, v254, 15
	s_add_u32 s9, s26, s9
	v_readlane_b32 s26, v254, 16
	s_addc_u32 s20, s26, s20
	s_lshl_b32 s26, s34, 8
	s_ashr_i32 s27, s26, 31
	s_lshl_b64 s[26:27], s[26:27], 2
	s_add_u32 s9, s9, s26
	s_addc_u32 s20, s20, s27
	s_add_u32 s26, s9, s85
	s_addc_u32 s27, s20, 0
	global_load_dword v168, v[138:139], off
	global_load_dword v166, v[138:139], off offset:64
	global_load_dword v164, v[138:139], off offset:128
	global_load_dword v162, v[138:139], off offset:192
	global_load_dword v160, v[138:139], off offset:512
	global_load_dword v158, v[138:139], off offset:576
	global_load_dword v152, v[138:139], off offset:640
	global_load_dword v98, v[138:139], off offset:704
	global_load_dwordx4 v[176:179], v172, s[26:27] offset:16
	global_load_dwordx4 v[140:143], v172, s[26:27]
	global_load_dwordx4 v[182:185], v172, s[26:27] offset:528
	global_load_dwordx4 v[144:147], v172, s[26:27] offset:512
	v_cvt_f32_i32_e32 v129, v129
	v_cvt_f32_i32_e32 v121, v121
	v_readlane_b32 s26, v254, 13
	v_readlane_b32 s27, v254, 14
	v_lshl_or_b32 v138, s34, 7, v167
	s_movk_i32 s9, 0x2c00
	v_mov_b64_e32 v[170:171], s[26:27]
	v_ashrrev_i32_e32 v139, 31, v138
	v_mad_i64_i32 v[170:171], s[26:27], v136, s9, v[170:171]
	s_waitcnt vmcnt(0)
	v_mov_b32_e32 v149, v140
	v_mov_b32_e32 v140, v145
	v_pk_mul_f32 v[154:155], v[140:141], s[58:59] op_sel_hi:[1,0]
	v_mov_b32_e32 v140, v146
	v_mov_b32_e32 v141, v142
	v_pk_mul_f32 v[150:151], v[140:141], s[58:59] op_sel_hi:[1,0]
	v_mov_b32_e32 v141, v176
	v_mov_b32_e32 v176, v183
	v_mov_b32_e32 v148, v144
	v_pk_mul_f32 v[144:145], v[176:177], s[58:59] op_sel_hi:[1,0]
	v_cvt_f32_i32_e32 v177, v128
	v_cvt_f32_i32_e32 v176, v124
	v_mov_b32_e32 v140, v182
	v_pk_mul_f32 v[156:157], v[148:149], s[58:59] op_sel_hi:[1,0]
	v_mov_b32_e32 v142, v147
	v_pk_mul_f32 v[146:147], v[140:141], s[58:59] op_sel_hi:[1,0]
	v_mov_b32_e32 v140, v184
	v_mov_b32_e32 v141, v178
	v_mov_b32_e32 v178, v185
	v_pk_mul_f32 v[148:149], v[142:143], s[58:59] op_sel_hi:[1,0]
	v_pk_mul_f32 v[142:143], v[140:141], s[58:59] op_sel_hi:[1,0]
	v_pk_mul_f32 v[140:141], v[178:179], s[58:59] op_sel_hi:[1,0]
	v_pk_mul_f32 v[178:179], v[168:169], v[156:157] op_sel_hi:[0,1]
	v_pk_mul_f32 v[176:177], v[178:179], v[176:177]
	v_cvt_f32_i32_e32 v128, v125
	v_mul_f32_e32 v124, 0xbfb8aa3b, v177
	v_exp_f32_e32 v124, v124
	s_nop 0
	v_add_f32_e32 v124, 1.0, v124
	v_rcp_f32_e32 v124, v124
	s_nop 0
	v_mul_f32_e32 v124, v177, v124
	v_mul_f32_e32 v124, v176, v124
	v_pk_mul_f32 v[176:177], v[168:169], v[154:155] op_sel_hi:[0,1]
	v_pk_mul_f32 v[128:129], v[176:177], v[128:129]
	v_pk_mul_f32 v[176:177], v[168:169], v[150:151] op_sel_hi:[0,1]
	v_mul_f32_e32 v125, 0xbfb8aa3b, v129
	v_exp_f32_e32 v125, v125
	s_nop 0
	v_add_f32_e32 v125, 1.0, v125
	v_rcp_f32_e32 v125, v125
	s_nop 0
	v_mul_f32_e32 v125, v129, v125
	v_mul_f32_e32 v125, v128, v125
	v_cvt_f32_i32_e32 v129, v130
	v_cvt_f32_i32_e32 v128, v126
	v_pk_mul_f32 v[128:129], v[176:177], v[128:129]
	s_nop 0
	v_mul_f32_e32 v126, 0xbfb8aa3b, v129
	v_exp_f32_e32 v126, v126
	s_nop 0
	v_add_f32_e32 v126, 1.0, v126
	v_rcp_f32_e32 v126, v126
	s_nop 0
	v_mul_f32_e32 v126, v129, v126
	v_mul_f32_e32 v126, v128, v126
	v_cvt_f32_i32_e32 v129, v131
	v_cvt_f32_i32_e32 v128, v127
	v_pk_mul_f32 v[130:131], v[168:169], v[148:149] op_sel_hi:[0,1]
	v_pk_mul_f32 v[128:129], v[130:131], v[128:129]
	s_nop 0
	v_mul_f32_e32 v127, 0xbfb8aa3b, v129
	v_exp_f32_e32 v127, v127
	v_pk_mul_f32 v[130:131], v[168:169], v[146:147] op_sel_hi:[0,1]
	v_add_f32_e32 v127, 1.0, v127
	v_rcp_f32_e32 v127, v127
	s_nop 0
	v_mul_f32_e32 v127, v129, v127
	v_mul_f32_e32 v127, v128, v127
	v_cvt_f32_i32_e32 v129, v120
	v_cvt_f32_i32_e32 v128, v116
	v_cvt_f32_i32_e32 v120, v117
	v_pk_mul_f32 v[128:129], v[130:131], v[128:129]
	s_nop 0
	v_mul_f32_e32 v116, 0xbfb8aa3b, v129
	v_exp_f32_e32 v116, v116
	s_nop 0
	v_add_f32_e32 v116, 1.0, v116
	v_rcp_f32_e32 v116, v116
	s_nop 0
	v_mul_f32_e32 v116, v129, v116
	v_mul_f32_e32 v128, v128, v116
	v_pk_mul_f32 v[116:117], v[168:169], v[144:145] op_sel_hi:[0,1]
	v_pk_mul_f32 v[116:117], v[116:117], v[120:121]
	s_nop 0
	v_mul_f32_e32 v120, 0xbfb8aa3b, v117
	v_exp_f32_e32 v120, v120
	s_nop 0
	v_add_f32_e32 v120, 1.0, v120
	v_rcp_f32_e32 v120, v120
	s_nop 0
	v_mul_f32_e32 v117, v117, v120
	v_mul_f32_e32 v129, v116, v117
	v_cvt_f32_i32_e32 v117, v122
	v_cvt_f32_i32_e32 v116, v118
	v_pk_mul_f32 v[120:121], v[168:169], v[142:143] op_sel_hi:[0,1]
	v_pk_mul_f32 v[116:117], v[120:121], v[116:117]
	s_nop 0
	v_mul_f32_e32 v118, 0xbfb8aa3b, v117
	v_exp_f32_e32 v118, v118
	v_lshl_add_u64 v[120:121], v[138:139], 1, v[170:171]
	v_add_f32_e32 v118, 1.0, v118
	v_rcp_f32_e32 v118, v118
	s_nop 0
	v_mul_f32_e32 v117, v117, v118
	v_mul_f32_e32 v122, v116, v117
	v_cvt_f32_i32_e32 v117, v123
	v_cvt_f32_i32_e32 v116, v119
	v_pk_mul_f32 v[118:119], v[168:169], v[140:141] op_sel_hi:[0,1]
	v_pk_mul_f32 v[116:117], v[118:119], v[116:117]
	s_nop 0
	v_mul_f32_e32 v118, 0xbfb8aa3b, v117
	v_exp_f32_e32 v118, v118
	s_nop 0
	v_add_f32_e32 v118, 1.0, v118
	v_rcp_f32_e32 v118, v118
	s_nop 0
	v_mul_f32_e32 v117, v117, v118
	v_mul_f32_e32 v123, v116, v117
	v_cvt_pk_bf16_f32 v116, v124, v125
	v_cvt_pk_bf16_f32 v117, v126, v127
	v_cvt_pk_bf16_f32 v118, v128, v129
	v_cvt_pk_bf16_f32 v119, v122, v123
	global_store_dwordx4 v[120:121], v[116:119], off
	s_nop 1
	v_max_f32_e64 v118, |v122|, |v123|
	v_max_f32_e64 v116, |v124|, |v125|
	v_max_f32_e64 v117, |v126|, |v127|
	v_max3_f32 v118, |v128|, |v129|, v118
	v_max3_f32 v116, v116, v117, v118
	v_mov_b32_e32 v117, v0
	s_nop 0
	v_lshlrev_b32_e32 v117, 2, v117
	v_bitop3_b32 v118, v117, 64, v220 bitop3:0x6c
	ds_bpermute_b32 v118, v118, v116
	v_bitop3_b32 v117, v117, s59, v220 bitop3:0x6c
	s_waitcnt lgkmcnt(0)
	v_max_f32_e32 v118, v118, v118
	v_max_f32_e32 v116, v116, v118
	ds_bpermute_b32 v117, v117, v116
	s_and_saveexec_b64 s[26:27], s[0:1]
	s_cbranch_execz .LBB0_1873
	v_readlane_b32 s36, v253, 57
	s_waitcnt lgkmcnt(0)
	v_max_f32_e32 v117, v117, v117
	v_max_f32_e32 v116, v116, v116
	v_readlane_b32 s37, v253, 58
	v_max_f32_e32 v118, v116, v117
	s_nop 0
	v_lshl_add_u64 v[116:117], v[136:137], 2, s[36:37]
	global_atomic_umax v[116:117], v118, off

.LBB0_2010:
	s_add_u32 s34, s30, 0x100
	s_addc_u32 s35, s31, 0
	s_add_i32 vcc_hi, 0, 0x10000
	v_add_u32_e32 v146, vcc_hi, v147
	ds_read_b128 v[132:135], v146
	ds_read_b128 v[150:153], v146 offset:1024
	ds_read_b128 v[154:157], v146 offset:2048
	ds_read_b128 v[158:161], v146 offset:3072
	s_cmp_eq_u32 vcc_lo, 40
	s_cselect_b32 s39, s23, s35
	s_cselect_b32 s38, s22, s34
	s_cselect_b32 s37, s25, s93
	s_cselect_b32 s36, s24, s71
	v_lshl_add_u64 v[196:197], s[30:31], 0, v[142:143]
	s_add_i32 m0, s8, 0xc000
	ds_read_b128 v[164:167], v163
	ds_read_b128 v[168:171], v163 offset:1024
	ds_read_b128 v[172:175], v163 offset:2048
	ds_read_b128 v[176:179], v163 offset:3072
	ds_read_b128 v[180:183], v163 offset:4096
	ds_read_b128 v[184:187], v163 offset:5120
	ds_read_b128 v[188:191], v163 offset:6144
	ds_read_b128 v[192:195], v163 offset:7168
	global_load_lds_dwordx4 v[196:197], off
	s_add_i32 m0, s8, 0xe000
	v_lshl_add_u64 v[196:197], s[30:31], 0, v[144:145]
	global_load_lds_dwordx4 v[196:197], off
	s_waitcnt lgkmcnt(8)
	s_barrier
	s_waitcnt lgkmcnt(0)
	v_mfma_i32_16x16x64_i8 v[128:131], v[132:135], v[164:167], v[128:131]
	v_mfma_i32_16x16x64_i8 v[124:127], v[154:157], v[164:167], v[124:127]
	v_mfma_i32_16x16x64_i8 v[120:123], v[132:135], v[172:175], v[120:123]
	v_mfma_i32_16x16x64_i8 v[116:119], v[154:157], v[172:175], v[116:119]
	v_mfma_i32_16x16x64_i8 v[112:115], v[132:135], v[180:183], v[112:115]
	v_mfma_i32_16x16x64_i8 v[108:111], v[154:157], v[180:183], v[108:111]
	v_mfma_i32_16x16x64_i8 v[104:107], v[132:135], v[188:191], v[104:107]
	v_mfma_i32_16x16x64_i8 v[100:103], v[154:157], v[188:191], v[100:103]
	v_mfma_i32_16x16x64_i8 v[128:131], v[150:153], v[168:171], v[128:131]
	v_mfma_i32_16x16x64_i8 v[124:127], v[158:161], v[168:171], v[124:127]
	v_mfma_i32_16x16x64_i8 v[120:123], v[150:153], v[176:179], v[120:123]
	v_mfma_i32_16x16x64_i8 v[116:119], v[158:161], v[176:179], v[116:119]
	v_mfma_i32_16x16x64_i8 v[112:115], v[150:153], v[184:187], v[112:115]
	v_mfma_i32_16x16x64_i8 v[108:111], v[158:161], v[184:187], v[108:111]
	v_mfma_i32_16x16x64_i8 v[104:107], v[150:153], v[192:195], v[104:107]
	v_mfma_i32_16x16x64_i8 v[100:103], v[158:161], v[192:195], v[100:103]
	s_barrier
	s_add_i32 s3, 0, 0x14000
	s_add_i32 s30, vcc_hi, s62
	v_add_u32_e32 v146, s3, v147
	v_lshl_add_u64 v[212:213], s[36:37], 0, v[98:99]
	s_mov_b32 m0, s30
	ds_read_b128 v[196:199], v146
	ds_read_b128 v[200:203], v146 offset:1024
	ds_read_b128 v[204:207], v146 offset:2048
	ds_read_b128 v[208:211], v146 offset:3072
	global_load_lds_dwordx4 v[212:213], off
	s_add_i32 m0, s30, 0x2000
	v_lshl_add_u64 v[214:215], s[36:37], 0, v[136:137]
	global_load_lds_dwordx4 v[214:215], off
	s_barrier
	s_waitcnt lgkmcnt(0)
	v_mfma_i32_16x16x64_i8 v[94:97], v[196:199], v[164:167], v[94:97]
	v_mfma_i32_16x16x64_i8 v[90:93], v[204:207], v[164:167], v[90:93]
	v_mfma_i32_16x16x64_i8 v[86:89], v[196:199], v[172:175], v[86:89]
	v_mfma_i32_16x16x64_i8 v[82:85], v[204:207], v[172:175], v[82:85]
	v_mfma_i32_16x16x64_i8 v[78:81], v[196:199], v[180:183], v[78:81]
	v_mfma_i32_16x16x64_i8 v[74:77], v[204:207], v[180:183], v[74:77]
	v_mfma_i32_16x16x64_i8 v[70:73], v[196:199], v[188:191], v[70:73]
	v_mfma_i32_16x16x64_i8 v[66:69], v[204:207], v[188:191], v[66:69]
	v_mfma_i32_16x16x64_i8 v[94:97], v[200:203], v[168:171], v[94:97]
	v_mfma_i32_16x16x64_i8 v[90:93], v[208:211], v[168:171], v[90:93]
	v_mfma_i32_16x16x64_i8 v[86:89], v[200:203], v[176:179], v[86:89]
	v_mfma_i32_16x16x64_i8 v[82:85], v[208:211], v[176:179], v[82:85]
	v_mfma_i32_16x16x64_i8 v[78:81], v[200:203], v[184:187], v[78:81]
	v_mfma_i32_16x16x64_i8 v[74:77], v[208:211], v[184:187], v[74:77]
	v_mfma_i32_16x16x64_i8 v[70:73], v[200:203], v[192:195], v[70:73]
	v_mfma_i32_16x16x64_i8 v[66:69], v[208:211], v[192:195], v[66:69]
	s_mov_b32 m0, s8
	v_lshl_add_u64 v[216:217], s[38:39], 0, v[140:141]
	s_barrier
	ds_read_b128 v[164:167], v163 offset:16384
	ds_read_b128 v[168:171], v163 offset:17408
	ds_read_b128 v[172:175], v163 offset:18432
	ds_read_b128 v[176:179], v163 offset:19456
	ds_read_b128 v[180:183], v163 offset:20480
	ds_read_b128 v[184:187], v163 offset:21504
	ds_read_b128 v[188:191], v163 offset:22528
	ds_read_b128 v[192:195], v163 offset:23552
	global_load_lds_dwordx4 v[216:217], off
	s_mov_b32 m0, s64
	v_lshl_add_u64 v[218:219], s[38:39], 0, v[138:139]
	global_load_lds_dwordx4 v[218:219], off
	s_barrier
	s_waitcnt lgkmcnt(0)
	v_mfma_i32_16x16x64_i8 v[62:65], v[132:135], v[164:167], v[62:65]
	v_mfma_i32_16x16x64_i8 v[58:61], v[154:157], v[164:167], v[58:61]
	v_mfma_i32_16x16x64_i8 v[54:57], v[132:135], v[172:175], v[54:57]
	v_mfma_i32_16x16x64_i8 v[50:53], v[154:157], v[172:175], v[50:53]
	v_mfma_i32_16x16x64_i8 v[46:49], v[132:135], v[180:183], v[46:49]
	v_mfma_i32_16x16x64_i8 v[42:45], v[154:157], v[180:183], v[42:45]
	v_mfma_i32_16x16x64_i8 v[38:41], v[132:135], v[188:191], v[38:41]
	v_mfma_i32_16x16x64_i8 v[34:37], v[154:157], v[188:191], v[34:37]
	v_mfma_i32_16x16x64_i8 v[62:65], v[150:153], v[168:171], v[62:65]
	v_mfma_i32_16x16x64_i8 v[58:61], v[158:161], v[168:171], v[58:61]
	v_mfma_i32_16x16x64_i8 v[54:57], v[150:153], v[176:179], v[54:57]
	v_mfma_i32_16x16x64_i8 v[50:53], v[158:161], v[176:179], v[50:53]
	v_mfma_i32_16x16x64_i8 v[46:49], v[150:153], v[184:187], v[46:49]
	v_mfma_i32_16x16x64_i8 v[42:45], v[158:161], v[184:187], v[42:45]
	v_mfma_i32_16x16x64_i8 v[38:41], v[150:153], v[192:195], v[38:41]
	v_mfma_i32_16x16x64_i8 v[34:37], v[158:161], v[192:195], v[34:37]
	s_barrier
	s_add_u32 s30, s36, 0xb0000
	s_addc_u32 s31, s37, 0
	s_add_i32 s3, s3, s62
	s_mov_b32 m0, s3
	v_lshl_add_u64 v[132:133], s[30:31], 0, v[98:99]
	global_load_lds_dwordx4 v[132:133], off
	s_add_i32 m0, s3, 0x2000
	v_lshl_add_u64 v[132:133], s[30:31], 0, v[136:137]
	global_load_lds_dwordx4 v[132:133], off
	s_waitcnt vmcnt(6)
	s_barrier
	v_mfma_i32_16x16x64_i8 v[30:33], v[196:199], v[164:167], v[30:33]
	v_mfma_i32_16x16x64_i8 v[26:29], v[204:207], v[164:167], v[26:29]
	v_mfma_i32_16x16x64_i8 v[22:25], v[196:199], v[172:175], v[22:25]
	v_mfma_i32_16x16x64_i8 v[18:21], v[204:207], v[172:175], v[18:21]
	v_mfma_i32_16x16x64_i8 v[14:17], v[196:199], v[180:183], v[14:17]
	v_mfma_i32_16x16x64_i8 v[10:13], v[204:207], v[180:183], v[10:13]
	v_mfma_i32_16x16x64_i8 v[6:9], v[196:199], v[188:191], v[6:9]
	v_mfma_i32_16x16x64_i8 v[2:5], v[204:207], v[188:191], v[2:5]
	v_mfma_i32_16x16x64_i8 v[30:33], v[200:203], v[168:171], v[30:33]
	v_mfma_i32_16x16x64_i8 v[26:29], v[208:211], v[168:171], v[26:29]
	v_mfma_i32_16x16x64_i8 v[22:25], v[200:203], v[176:179], v[22:25]
	v_mfma_i32_16x16x64_i8 v[18:21], v[208:211], v[176:179], v[18:21]
	v_mfma_i32_16x16x64_i8 v[14:17], v[200:203], v[184:187], v[14:17]
	v_mfma_i32_16x16x64_i8 v[10:13], v[208:211], v[184:187], v[10:13]
	v_mfma_i32_16x16x64_i8 v[6:9], v[200:203], v[192:195], v[6:9]
	v_mfma_i32_16x16x64_i8 v[2:5], v[208:211], v[192:195], v[2:5]
	s_add_i32 s3, 0, 0x18000
	v_add_u32_e32 v146, s3, v147
	s_barrier
	ds_read_b128 v[132:135], v146
	ds_read_b128 v[150:153], v146 offset:1024
	ds_read_b128 v[154:157], v146 offset:2048
	ds_read_b128 v[158:161], v146 offset:3072
	s_add_u32 s30, s38, 0xb0000
	s_addc_u32 s31, s39, 0
	s_mov_b32 m0, s65
	v_lshl_add_u64 v[196:197], s[30:31], 0, v[140:141]
	ds_read_b128 v[164:167], v163 offset:32768
	ds_read_b128 v[168:171], v163 offset:33792
	ds_read_b128 v[172:175], v163 offset:34816
	ds_read_b128 v[176:179], v163 offset:35840
	ds_read_b128 v[180:183], v163 offset:36864
	ds_read_b128 v[184:187], v163 offset:37888
	ds_read_b128 v[188:191], v163 offset:38912
	ds_read_b128 v[192:195], v163 offset:39936
	global_load_lds_dwordx4 v[196:197], off
	s_mov_b32 m0, s66
	v_lshl_add_u64 v[196:197], s[30:31], 0, v[138:139]
	global_load_lds_dwordx4 v[196:197], off
	s_waitcnt lgkmcnt(8)
	s_barrier
	s_waitcnt lgkmcnt(0)
	v_mfma_i32_16x16x64_i8 v[128:131], v[132:135], v[164:167], v[128:131]
	v_mfma_i32_16x16x64_i8 v[124:127], v[154:157], v[164:167], v[124:127]
	v_mfma_i32_16x16x64_i8 v[120:123], v[132:135], v[172:175], v[120:123]
	v_mfma_i32_16x16x64_i8 v[116:119], v[154:157], v[172:175], v[116:119]
	v_mfma_i32_16x16x64_i8 v[112:115], v[132:135], v[180:183], v[112:115]
	v_mfma_i32_16x16x64_i8 v[108:111], v[154:157], v[180:183], v[108:111]
	v_mfma_i32_16x16x64_i8 v[104:107], v[132:135], v[188:191], v[104:107]
	v_mfma_i32_16x16x64_i8 v[100:103], v[154:157], v[188:191], v[100:103]
	v_mfma_i32_16x16x64_i8 v[128:131], v[150:153], v[168:171], v[128:131]
	v_mfma_i32_16x16x64_i8 v[124:127], v[158:161], v[168:171], v[124:127]
	v_mfma_i32_16x16x64_i8 v[120:123], v[150:153], v[176:179], v[120:123]
	v_mfma_i32_16x16x64_i8 v[116:119], v[158:161], v[176:179], v[116:119]
	v_mfma_i32_16x16x64_i8 v[112:115], v[150:153], v[184:187], v[112:115]
	v_mfma_i32_16x16x64_i8 v[108:111], v[158:161], v[184:187], v[108:111]
	v_mfma_i32_16x16x64_i8 v[104:107], v[150:153], v[192:195], v[104:107]
	v_mfma_i32_16x16x64_i8 v[100:103], v[158:161], v[192:195], v[100:103]
	s_barrier
	s_add_i32 s38, 0, 0x1c000
	s_add_i32 s3, s3, s62
	v_add_u32_e32 v146, s38, v147
	v_lshl_add_u64 v[212:213], v[212:213], 0, s[68:69]
	s_mov_b32 m0, s3
	ds_read_b128 v[196:199], v146
	ds_read_b128 v[200:203], v146 offset:1024
	ds_read_b128 v[204:207], v146 offset:2048
	ds_read_b128 v[208:211], v146 offset:3072
	global_load_lds_dwordx4 v[212:213], off
	s_add_i32 m0, s3, 0x2000
	v_lshl_add_u64 v[212:213], v[214:215], 0, s[68:69]
	global_load_lds_dwordx4 v[212:213], off
	s_barrier
	s_waitcnt lgkmcnt(0)
	v_mfma_i32_16x16x64_i8 v[94:97], v[196:199], v[164:167], v[94:97]
	v_mfma_i32_16x16x64_i8 v[90:93], v[204:207], v[164:167], v[90:93]
	v_mfma_i32_16x16x64_i8 v[86:89], v[196:199], v[172:175], v[86:89]
	v_mfma_i32_16x16x64_i8 v[82:85], v[204:207], v[172:175], v[82:85]
	v_mfma_i32_16x16x64_i8 v[78:81], v[196:199], v[180:183], v[78:81]
	v_mfma_i32_16x16x64_i8 v[74:77], v[204:207], v[180:183], v[74:77]
	v_mfma_i32_16x16x64_i8 v[70:73], v[196:199], v[188:191], v[70:73]
	v_mfma_i32_16x16x64_i8 v[66:69], v[204:207], v[188:191], v[66:69]
	v_mfma_i32_16x16x64_i8 v[94:97], v[200:203], v[168:171], v[94:97]
	v_mfma_i32_16x16x64_i8 v[90:93], v[208:211], v[168:171], v[90:93]
	v_mfma_i32_16x16x64_i8 v[86:89], v[200:203], v[176:179], v[86:89]
	v_mfma_i32_16x16x64_i8 v[82:85], v[208:211], v[176:179], v[82:85]
	v_mfma_i32_16x16x64_i8 v[78:81], v[200:203], v[184:187], v[78:81]
	v_mfma_i32_16x16x64_i8 v[74:77], v[208:211], v[184:187], v[74:77]
	v_mfma_i32_16x16x64_i8 v[70:73], v[200:203], v[192:195], v[70:73]
	v_mfma_i32_16x16x64_i8 v[66:69], v[208:211], v[192:195], v[66:69]
	s_mov_b32 m0, s67
	v_lshl_add_u64 v[212:213], v[216:217], 0, s[68:69]
	s_barrier
	ds_read_b128 v[164:167], v163 offset:49152
	ds_read_b128 v[168:171], v163 offset:50176
	ds_read_b128 v[172:175], v163 offset:51200
	ds_read_b128 v[176:179], v163 offset:52224
	ds_read_b128 v[180:183], v163 offset:53248
	ds_read_b128 v[184:187], v163 offset:54272
	ds_read_b128 v[188:191], v163 offset:55296
	ds_read_b128 v[192:195], v163 offset:56320
	global_load_lds_dwordx4 v[212:213], off
	s_mov_b32 m0, s74
	v_lshl_add_u64 v[212:213], v[218:219], 0, s[68:69]
	global_load_lds_dwordx4 v[212:213], off
	s_barrier
	s_waitcnt lgkmcnt(0)
	v_mfma_i32_16x16x64_i8 v[62:65], v[132:135], v[164:167], v[62:65]
	v_mfma_i32_16x16x64_i8 v[58:61], v[154:157], v[164:167], v[58:61]
	v_mfma_i32_16x16x64_i8 v[54:57], v[132:135], v[172:175], v[54:57]
	v_mfma_i32_16x16x64_i8 v[50:53], v[154:157], v[172:175], v[50:53]
	v_mfma_i32_16x16x64_i8 v[46:49], v[132:135], v[180:183], v[46:49]
	v_mfma_i32_16x16x64_i8 v[42:45], v[154:157], v[180:183], v[42:45]
	v_mfma_i32_16x16x64_i8 v[38:41], v[132:135], v[188:191], v[38:41]
	v_mfma_i32_16x16x64_i8 v[34:37], v[154:157], v[188:191], v[34:37]
	v_mfma_i32_16x16x64_i8 v[62:65], v[150:153], v[168:171], v[62:65]
	v_mfma_i32_16x16x64_i8 v[58:61], v[158:161], v[168:171], v[58:61]
	v_mfma_i32_16x16x64_i8 v[54:57], v[150:153], v[176:179], v[54:57]
	v_mfma_i32_16x16x64_i8 v[50:53], v[158:161], v[176:179], v[50:53]
	v_mfma_i32_16x16x64_i8 v[46:49], v[150:153], v[184:187], v[46:49]
	v_mfma_i32_16x16x64_i8 v[42:45], v[158:161], v[184:187], v[42:45]
	v_mfma_i32_16x16x64_i8 v[38:41], v[150:153], v[192:195], v[38:41]
	v_mfma_i32_16x16x64_i8 v[34:37], v[158:161], v[192:195], v[34:37]
	s_barrier
	s_add_u32 s30, s36, 0xb0080
	s_addc_u32 s31, s37, 0
	s_add_i32 s3, s38, s62
	s_mov_b32 m0, s3
	v_lshl_add_u64 v[132:133], s[30:31], 0, v[98:99]
	global_load_lds_dwordx4 v[132:133], off
	s_add_i32 m0, s3, 0x2000
	v_lshl_add_u64 v[132:133], s[30:31], 0, v[136:137]
	global_load_lds_dwordx4 v[132:133], off
	s_waitcnt vmcnt(6)
	s_barrier
	v_mfma_i32_16x16x64_i8 v[30:33], v[196:199], v[164:167], v[30:33]
	v_mfma_i32_16x16x64_i8 v[26:29], v[204:207], v[164:167], v[26:29]
	v_mfma_i32_16x16x64_i8 v[22:25], v[196:199], v[172:175], v[22:25]
	v_mfma_i32_16x16x64_i8 v[18:21], v[204:207], v[172:175], v[18:21]
	v_mfma_i32_16x16x64_i8 v[14:17], v[196:199], v[180:183], v[14:17]
	v_mfma_i32_16x16x64_i8 v[10:13], v[204:207], v[180:183], v[10:13]
	v_mfma_i32_16x16x64_i8 v[6:9], v[196:199], v[188:191], v[6:9]
	v_mfma_i32_16x16x64_i8 v[2:5], v[204:207], v[188:191], v[2:5]
	v_mfma_i32_16x16x64_i8 v[30:33], v[200:203], v[168:171], v[30:33]
	v_mfma_i32_16x16x64_i8 v[26:29], v[208:211], v[168:171], v[26:29]
	v_mfma_i32_16x16x64_i8 v[22:25], v[200:203], v[176:179], v[22:25]
	v_mfma_i32_16x16x64_i8 v[18:21], v[208:211], v[176:179], v[18:21]
	v_mfma_i32_16x16x64_i8 v[14:17], v[200:203], v[184:187], v[14:17]
	v_mfma_i32_16x16x64_i8 v[10:13], v[208:211], v[184:187], v[10:13]
	v_mfma_i32_16x16x64_i8 v[6:9], v[200:203], v[192:195], v[6:9]
	v_mfma_i32_16x16x64_i8 v[2:5], v[208:211], v[192:195], v[2:5]
	s_add_i32 vcc_lo, vcc_lo, 2
	s_add_u32 s71, s71, 0x100
	s_addc_u32 s93, s93, 0
	s_cmp_gt_u32 vcc_lo, 41
	s_mov_b64 s[30:31], s[34:35]
	s_barrier
	s_cbranch_scc0 .LBB0_2010
	v_lshl_add_u32 v208, s70, 8, v1
	v_readlane_b32 s30, v253, 57
	v_or_b32_e32 v204, 16, v208
	v_lshl_or_b32 v210, s29, 8, v149
	s_ashr_i32 s29, s28, 31
	v_ashrrev_i32_e32 v209, 31, v208
	v_readlane_b32 s31, v253, 58
	v_ashrrev_i32_e32 v205, 31, v204
	v_or_b32_e32 v200, 32, v208
	s_lshl_b64 s[28:29], s[28:29], 13
	v_readlane_b32 s3, v254, 21
	v_lshl_add_u64 v[132:133], v[208:209], 2, s[30:31]
	v_lshl_add_u64 v[134:135], v[204:205], 2, s[30:31]
	v_ashrrev_i32_e32 v201, 31, v200
	v_or_b32_e32 v188, 48, v208
	s_add_u32 s28, s3, s28
	v_readlane_b32 s3, v254, 22
	global_load_dword v206, v[132:133], off
	global_load_dword v202, v[134:135], off
	v_lshl_add_u64 v[134:135], v[200:201], 2, s[30:31]
	v_ashrrev_i32_e32 v189, 31, v188
	v_ashrrev_i32_e32 v211, 31, v210
	s_addc_u32 s29, s3, s29
	global_load_dword v190, v[134:135], off
	v_lshl_add_u64 v[134:135], v[188:189], 2, s[30:31]
	v_lshl_add_u64 v[212:213], v[210:211], 2, s[28:29]
	global_load_dword v174, v[134:135], off
	global_load_dword v168, v[132:133], off offset:512
	global_load_dword v162, v[132:133], off offset:576
	global_load_dword v148, v[132:133], off offset:640
	global_load_dword v146, v[132:133], off offset:704
	s_nop 0
	global_load_dwordx4 v[132:135], v[212:213], off offset:16
	global_load_dwordx4 v[150:153], v[212:213], off
	v_cvt_f32_i32_e32 v155, v9
	v_cvt_f32_i32_e32 v154, v8
	v_cvt_f32_i32_e32 v161, v7
	v_cvt_f32_i32_e32 v160, v6
	v_cvt_f32_i32_e32 v195, v27
	v_cvt_f32_i32_e32 v194, v26
	v_cvt_f32_i32_e32 v197, v33
	v_cvt_f32_i32_e32 v196, v32
	v_cvt_f32_i32_e32 v27, v53
	v_cvt_f32_i32_e32 v26, v52
	v_cvt_f32_i32_e32 v33, v55
	v_cvt_f32_i32_e32 v32, v54
	v_cvt_f32_i32_e32 v53, v101
	v_cvt_f32_i32_e32 v52, v100
	v_cvt_f32_i32_e32 v55, v107
	v_cvt_f32_i32_e32 v54, v106
	v_cvt_f32_i32_e32 v101, v127
	v_cvt_f32_i32_e32 v100, v126
	v_cvt_f32_i32_e32 v107, v129
	v_cvt_f32_i32_e32 v106, v128
	v_cvt_f32_i32_e32 v167, v11
	v_cvt_f32_i32_e32 v166, v10
	v_cvt_f32_i32_e32 v171, v17
	v_cvt_f32_i32_e32 v170, v16
	v_cvt_f32_i32_e32 v193, v29
	v_cvt_f32_i32_e32 v192, v28
	v_cvt_f32_i32_e32 v11, v37
	v_cvt_f32_i32_e32 v10, v36
	v_cvt_f32_i32_e32 v17, v39
	v_cvt_f32_i32_e32 v16, v38
	v_cvt_f32_i32_e32 v29, v51
	v_cvt_f32_i32_e32 v28, v50
	v_cvt_f32_i32_e32 v37, v59
	v_cvt_f32_i32_e32 v36, v58
	v_cvt_f32_i32_e32 v39, v65
	v_cvt_f32_i32_e32 v38, v64
	v_cvt_f32_i32_e32 v65, v79
	v_cvt_f32_i32_e32 v64, v78
	v_cvt_f32_i32_e32 v79, v89
	v_cvt_f32_i32_e32 v78, v88
	v_cvt_f32_i32_e32 v89, v93
	v_cvt_f32_i32_e32 v88, v92
	v_cvt_f32_i32_e32 v95, v95
	v_cvt_f32_i32_e32 v94, v94
	v_cvt_f32_i32_e32 v51, v103
	v_cvt_f32_i32_e32 v50, v102
	v_cvt_f32_i32_e32 v59, v105
	v_cvt_f32_i32_e32 v58, v104
	v_cvt_f32_i32_e32 v103, v125
	v_cvt_f32_i32_e32 v102, v124
	v_cvt_f32_i32_e32 v105, v131
	v_cvt_f32_i32_e32 v104, v130
	v_cvt_f32_i32_e32 v93, v91
	v_cvt_f32_i32_e32 v92, v90
	v_cvt_f32_i32_e32 v97, v97
	v_cvt_f32_i32_e32 v96, v96
	v_cvt_f32_i32_e32 v199, v31
	v_cvt_f32_i32_e32 v198, v30
	v_cvt_f32_i32_e32 v31, v57
	v_cvt_f32_i32_e32 v30, v56
	v_cvt_f32_i32_e32 v57, v77
	v_cvt_f32_i32_e32 v56, v76
	v_cvt_f32_i32_e32 v77, v83
	v_cvt_f32_i32_e32 v76, v82
	v_cvt_f32_i32_e32 v83, v119
	v_cvt_f32_i32_e32 v82, v118
	v_cvt_f32_i32_e32 v91, v121
	v_cvt_f32_i32_e32 v90, v120
	v_readlane_b32 s28, v252, 15
	v_cvt_f32_i32_e32 v173, v15
	v_cvt_f32_i32_e32 v172, v14
	v_cvt_f32_i32_e32 v181, v21
	v_cvt_f32_i32_e32 v180, v20
	v_cvt_f32_i32_e32 v183, v19
	v_cvt_f32_i32_e32 v182, v18
	v_cvt_f32_i32_e32 v185, v25
	v_cvt_f32_i32_e32 v184, v24
	v_cvt_f32_i32_e32 v15, v41
	v_cvt_f32_i32_e32 v14, v40
	s_waitcnt vmcnt(0)
	v_pk_mul_f32 v[156:157], v[152:153], s[58:59] op_sel_hi:[1,0]
	v_pk_mul_f32 v[158:159], v[150:151], s[58:59] op_sel_hi:[1,0]
	v_cvt_f32_i32_e32 v151, v5
	v_cvt_f32_i32_e32 v150, v4
	v_cvt_f32_i32_e32 v153, v3
	v_cvt_f32_i32_e32 v152, v2
	global_load_dwordx4 v[2:5], v[212:213], off offset:512
	global_load_dwordx4 v[6:9], v[212:213], off offset:528
	v_cvt_f32_i32_e32 v19, v45
	v_cvt_f32_i32_e32 v18, v44
	v_cvt_f32_i32_e32 v21, v43
	v_cvt_f32_i32_e32 v20, v42
	v_cvt_f32_i32_e32 v25, v47
	v_cvt_f32_i32_e32 v24, v46
	v_cvt_f32_i32_e32 v41, v63
	v_cvt_f32_i32_e32 v40, v62
	v_cvt_f32_i32_e32 v43, v69
	v_cvt_f32_i32_e32 v42, v68
	v_cvt_f32_i32_e32 v45, v67
	v_cvt_f32_i32_e32 v44, v66
	v_cvt_f32_i32_e32 v47, v73
	v_cvt_f32_i32_e32 v46, v72
	v_cvt_f32_i32_e32 v63, v81
	v_cvt_f32_i32_e32 v62, v80
	v_cvt_f32_i32_e32 v73, v85
	v_cvt_f32_i32_e32 v72, v84
	v_cvt_f32_i32_e32 v81, v87
	v_cvt_f32_i32_e32 v80, v86
	v_cvt_f32_i32_e32 v67, v111
	v_cvt_f32_i32_e32 v66, v110
	v_cvt_f32_i32_e32 v69, v109
	v_cvt_f32_i32_e32 v68, v108
	v_cvt_f32_i32_e32 v85, v117
	v_cvt_f32_i32_e32 v84, v116
	v_cvt_f32_i32_e32 v87, v123
	v_cvt_f32_i32_e32 v86, v122
	v_pk_mul_f32 v[110:111], v[134:135], s[58:59] op_sel_hi:[1,0]
	v_lshlrev_b64 v[108:109], 12, v[208:209]
	v_readlane_b32 s29, v252, 16
	v_pk_mul_f32 v[106:107], v[206:207], v[106:107] op_sel_hi:[0,1]
	v_pk_mul_f32 v[100:101], v[206:207], v[100:101] op_sel_hi:[0,1]
	v_cvt_f32_i32_e32 v165, v13
	v_cvt_f32_i32_e32 v164, v12
	v_cvt_f32_i32_e32 v187, v23
	v_cvt_f32_i32_e32 v186, v22
	v_cvt_f32_i32_e32 v13, v35
	v_cvt_f32_i32_e32 v12, v34
	v_cvt_f32_i32_e32 v23, v49
	v_cvt_f32_i32_e32 v22, v48
	v_cvt_f32_i32_e32 v35, v61
	v_cvt_f32_i32_e32 v34, v60
	v_cvt_f32_i32_e32 v49, v71
	v_cvt_f32_i32_e32 v48, v70
	v_cvt_f32_i32_e32 v61, v75
	v_cvt_f32_i32_e32 v60, v74
	v_cvt_f32_i32_e32 v71, v115
	v_cvt_f32_i32_e32 v70, v114
	v_cvt_f32_i32_e32 v75, v113
	v_cvt_f32_i32_e32 v74, v112
	v_pk_mul_f32 v[112:113], v[132:133], s[58:59] op_sel_hi:[1,0]
	v_lshl_add_u64 v[108:109], s[28:29], 0, v[108:109]
	v_lshlrev_b64 v[114:115], 1, v[210:211]
	v_pk_mul_f32 v[104:105], v[206:207], v[104:105] op_sel_hi:[0,1]
	v_pk_mul_f32 v[102:103], v[206:207], v[102:103] op_sel_hi:[0,1]
	v_pk_mul_f32 v[116:117], v[110:111], v[100:101]
	v_pk_mul_f32 v[100:101], v[158:159], v[106:107]
	v_pk_mul_f32 v[94:95], v[206:207], v[94:95] op_sel_hi:[0,1]
	v_pk_mul_f32 v[88:89], v[206:207], v[88:89] op_sel_hi:[0,1]
	v_lshl_add_u64 v[108:109], v[108:109], 0, v[114:115]
	v_pk_mul_f32 v[102:103], v[112:113], v[102:103]
	v_pk_mul_f32 v[104:105], v[156:157], v[104:105]
	v_cvt_pk_bf16_f32 v100, v100, v101
	v_pk_mul_f32 v[96:97], v[206:207], v[96:97] op_sel_hi:[0,1]
	v_cvt_pk_bf16_f32 v101, v104, v105
	v_pk_mul_f32 v[92:93], v[206:207], v[92:93] op_sel_hi:[0,1]
	v_cvt_pk_bf16_f32 v102, v102, v103
	v_cvt_pk_bf16_f32 v103, v116, v117
	global_store_dwordx4 v[108:109], v[100:103], off
	v_pk_mul_f32 v[90:91], v[202:203], v[90:91] op_sel_hi:[0,1]
	v_pk_mul_f32 v[82:83], v[202:203], v[82:83] op_sel_hi:[0,1]
	v_pk_mul_f32 v[86:87], v[202:203], v[86:87] op_sel_hi:[0,1]
	v_pk_mul_f32 v[84:85], v[202:203], v[84:85] op_sel_hi:[0,1]
	v_pk_mul_f32 v[78:79], v[202:203], v[78:79] op_sel_hi:[0,1]
	v_pk_mul_f32 v[72:73], v[202:203], v[72:73] op_sel_hi:[0,1]
	v_pk_mul_f32 v[84:85], v[112:113], v[84:85]
	v_pk_mul_f32 v[86:87], v[156:157], v[86:87]
	s_waitcnt vmcnt(0)
	v_pk_mul_f32 v[2:3], v[2:3], s[58:59] op_sel_hi:[1,0]
	v_pk_mul_f32 v[8:9], v[8:9], s[58:59] op_sel_hi:[1,0]
	v_pk_mul_f32 v[6:7], v[6:7], s[58:59] op_sel_hi:[1,0]
	v_pk_mul_f32 v[4:5], v[4:5], s[58:59] op_sel_hi:[1,0]
	v_pk_mul_f32 v[94:95], v[2:3], v[94:95]
	v_pk_mul_f32 v[88:89], v[8:9], v[88:89]
	v_pk_mul_f32 v[96:97], v[4:5], v[96:97]
	v_pk_mul_f32 v[100:101], v[6:7], v[92:93]
	v_cvt_pk_bf16_f32 v92, v94, v95
	v_cvt_pk_bf16_f32 v93, v96, v97
	v_pk_mul_f32 v[80:81], v[202:203], v[80:81] op_sel_hi:[0,1]
	v_cvt_pk_bf16_f32 v94, v100, v101
	v_cvt_pk_bf16_f32 v95, v88, v89
	v_lshlrev_b64 v[88:89], 12, v[204:205]
	global_store_dwordx4 v[108:109], v[92:95], off offset:256
	v_lshl_add_u64 v[88:89], s[28:29], 0, v[88:89]
	v_lshl_add_u64 v[88:89], v[88:89], 0, v[114:115]
	v_pk_mul_f32 v[92:93], v[110:111], v[82:83]
	v_pk_mul_f32 v[82:83], v[158:159], v[90:91]
	v_pk_mul_f32 v[76:77], v[202:203], v[76:77] op_sel_hi:[0,1]
	v_cvt_pk_bf16_f32 v82, v82, v83
	v_cvt_pk_bf16_f32 v83, v86, v87
	v_pk_mul_f32 v[78:79], v[4:5], v[78:79]
	v_pk_mul_f32 v[72:73], v[8:9], v[72:73]
	v_cvt_pk_bf16_f32 v84, v84, v85
	v_cvt_pk_bf16_f32 v85, v92, v93
	global_store_dwordx4 v[88:89], v[82:85], off
	v_pk_mul_f32 v[80:81], v[2:3], v[80:81]
	v_pk_mul_f32 v[74:75], v[190:191], v[74:75] op_sel_hi:[0,1]
	v_pk_mul_f32 v[82:83], v[6:7], v[76:77]
	v_cvt_pk_bf16_f32 v76, v80, v81
	v_cvt_pk_bf16_f32 v77, v78, v79
	v_pk_mul_f32 v[66:67], v[190:191], v[66:67] op_sel_hi:[0,1]
	v_cvt_pk_bf16_f32 v78, v82, v83
	v_cvt_pk_bf16_f32 v79, v72, v73
	v_lshlrev_b64 v[72:73], 12, v[200:201]
	global_store_dwordx4 v[88:89], v[76:79], off offset:256
	v_lshl_add_u64 v[72:73], s[28:29], 0, v[72:73]
	v_pk_mul_f32 v[70:71], v[190:191], v[70:71] op_sel_hi:[0,1]
	v_pk_mul_f32 v[68:69], v[190:191], v[68:69] op_sel_hi:[0,1]
	v_pk_mul_f32 v[76:77], v[110:111], v[66:67]
	v_pk_mul_f32 v[66:67], v[158:159], v[74:75]
	v_pk_mul_f32 v[62:63], v[190:191], v[62:63] op_sel_hi:[0,1]
	v_pk_mul_f32 v[56:57], v[190:191], v[56:57] op_sel_hi:[0,1]
	v_lshl_add_u64 v[72:73], v[72:73], 0, v[114:115]
	v_pk_mul_f32 v[68:69], v[112:113], v[68:69]
	v_pk_mul_f32 v[70:71], v[156:157], v[70:71]
	v_cvt_pk_bf16_f32 v66, v66, v67
	v_pk_mul_f32 v[64:65], v[190:191], v[64:65] op_sel_hi:[0,1]
	v_cvt_pk_bf16_f32 v67, v70, v71
	v_pk_mul_f32 v[60:61], v[190:191], v[60:61] op_sel_hi:[0,1]
	v_pk_mul_f32 v[62:63], v[4:5], v[62:63]
	v_pk_mul_f32 v[56:57], v[8:9], v[56:57]
	v_cvt_pk_bf16_f32 v68, v68, v69
	v_cvt_pk_bf16_f32 v69, v76, v77
	global_store_dwordx4 v[72:73], v[66:69], off
	v_pk_mul_f32 v[64:65], v[2:3], v[64:65]
	v_pk_mul_f32 v[58:59], v[174:175], v[58:59] op_sel_hi:[0,1]
	v_pk_mul_f32 v[66:67], v[6:7], v[60:61]
	v_cvt_pk_bf16_f32 v60, v64, v65
	v_cvt_pk_bf16_f32 v61, v62, v63
	v_pk_mul_f32 v[50:51], v[174:175], v[50:51] op_sel_hi:[0,1]
	v_cvt_pk_bf16_f32 v62, v66, v67
	v_cvt_pk_bf16_f32 v63, v56, v57
	v_lshlrev_b64 v[56:57], 12, v[188:189]
	global_store_dwordx4 v[72:73], v[60:63], off offset:256
	v_lshl_add_u64 v[56:57], s[28:29], 0, v[56:57]
	v_pk_mul_f32 v[54:55], v[174:175], v[54:55] op_sel_hi:[0,1]
	v_pk_mul_f32 v[52:53], v[174:175], v[52:53] op_sel_hi:[0,1]
	v_pk_mul_f32 v[60:61], v[110:111], v[50:51]
	v_pk_mul_f32 v[50:51], v[158:159], v[58:59]
	v_pk_mul_f32 v[44:45], v[174:175], v[44:45] op_sel_hi:[0,1]
	v_lshl_add_u64 v[56:57], v[56:57], 0, v[114:115]
	v_pk_mul_f32 v[52:53], v[112:113], v[52:53]
	v_pk_mul_f32 v[54:55], v[156:157], v[54:55]
	v_cvt_pk_bf16_f32 v50, v50, v51
	v_pk_mul_f32 v[48:49], v[174:175], v[48:49] op_sel_hi:[0,1]
	v_cvt_pk_bf16_f32 v51, v54, v55
	v_pk_mul_f32 v[46:47], v[174:175], v[46:47] op_sel_hi:[0,1]
	v_pk_mul_f32 v[42:43], v[174:175], v[42:43] op_sel_hi:[0,1]
	v_pk_mul_f32 v[44:45], v[6:7], v[44:45]
	v_cvt_pk_bf16_f32 v52, v52, v53
	v_cvt_pk_bf16_f32 v53, v60, v61
	global_store_dwordx4 v[56:57], v[50:53], off
	v_pk_mul_f32 v[46:47], v[4:5], v[46:47]
	v_pk_mul_f32 v[48:49], v[2:3], v[48:49]
	v_pk_mul_f32 v[50:51], v[8:9], v[42:43]
	v_cvt_pk_bf16_f32 v42, v48, v49
	v_cvt_pk_bf16_f32 v43, v46, v47
	v_cvt_pk_bf16_f32 v44, v44, v45
	s_mov_b64 s[28:29], 0x80000
	v_cvt_pk_bf16_f32 v45, v50, v51
	v_pk_mul_f32 v[40:41], v[168:169], v[40:41] op_sel_hi:[0,1]
	v_pk_mul_f32 v[38:39], v[168:169], v[38:39] op_sel_hi:[0,1]
	v_pk_mul_f32 v[34:35], v[168:169], v[34:35] op_sel_hi:[0,1]
	global_store_dwordx4 v[56:57], v[42:45], off offset:256
	v_pk_mul_f32 v[36:37], v[168:169], v[36:37] op_sel_hi:[0,1]
	v_pk_mul_f32 v[38:39], v[156:157], v[38:39]
	v_lshl_add_u64 v[42:43], v[108:109], 0, s[28:29]
	v_pk_mul_f32 v[44:45], v[110:111], v[34:35]
	v_pk_mul_f32 v[34:35], v[158:159], v[40:41]
	s_mov_b32 s28, 0x80000
	v_pk_mul_f32 v[36:37], v[112:113], v[36:37]
	v_cvt_pk_bf16_f32 v34, v34, v35
	v_cvt_pk_bf16_f32 v35, v38, v39
	v_add_co_u32_e32 v38, vcc, s28, v108
	v_cvt_pk_bf16_f32 v36, v36, v37
	v_cvt_pk_bf16_f32 v37, v44, v45
	v_pk_mul_f32 v[40:41], v[168:169], v[192:193] op_sel_hi:[0,1]
	s_nop 0
	v_addc_co_u32_e32 v39, vcc, 0, v109, vcc
	global_store_dwordx4 v[38:39], v[34:37], off
	v_pk_mul_f32 v[38:39], v[168:169], v[194:195] op_sel_hi:[0,1]
	v_pk_mul_f32 v[40:41], v[8:9], v[40:41]
	v_pk_mul_f32 v[34:35], v[168:169], v[198:199] op_sel_hi:[0,1]
	v_pk_mul_f32 v[36:37], v[168:169], v[196:197] op_sel_hi:[0,1]
	v_pk_mul_f32 v[36:37], v[4:5], v[36:37]
	v_pk_mul_f32 v[34:35], v[2:3], v[34:35]
	v_pk_mul_f32 v[38:39], v[6:7], v[38:39]
	v_cvt_pk_bf16_f32 v34, v34, v35
	v_cvt_pk_bf16_f32 v35, v36, v37
	s_mov_b64 s[28:29], 0x90000
	v_cvt_pk_bf16_f32 v36, v38, v39
	v_cvt_pk_bf16_f32 v37, v40, v41
	v_pk_mul_f32 v[32:33], v[162:163], v[32:33] op_sel_hi:[0,1]
	v_pk_mul_f32 v[30:31], v[162:163], v[30:31] op_sel_hi:[0,1]
	v_pk_mul_f32 v[26:27], v[162:163], v[26:27] op_sel_hi:[0,1]
	global_store_dwordx4 v[42:43], v[34:37], off offset:256
	v_pk_mul_f32 v[28:29], v[162:163], v[28:29] op_sel_hi:[0,1]
	v_pk_mul_f32 v[30:31], v[156:157], v[30:31]
	v_lshl_add_u64 v[34:35], v[108:109], 0, s[28:29]
	v_pk_mul_f32 v[36:37], v[110:111], v[26:27]
	v_pk_mul_f32 v[26:27], v[158:159], v[32:33]
	s_mov_b32 s28, 0x90000
	v_pk_mul_f32 v[28:29], v[112:113], v[28:29]
	v_cvt_pk_bf16_f32 v26, v26, v27
	v_cvt_pk_bf16_f32 v27, v30, v31
	v_add_co_u32_e32 v30, vcc, s28, v108
	v_cvt_pk_bf16_f32 v28, v28, v29
	v_cvt_pk_bf16_f32 v29, v36, v37
	v_pk_mul_f32 v[32:33], v[162:163], v[180:181] op_sel_hi:[0,1]
	s_nop 0
	v_addc_co_u32_e32 v31, vcc, 0, v109, vcc
	global_store_dwordx4 v[30:31], v[26:29], off
	v_pk_mul_f32 v[30:31], v[162:163], v[182:183] op_sel_hi:[0,1]
	v_pk_mul_f32 v[32:33], v[8:9], v[32:33]
	v_pk_mul_f32 v[26:27], v[162:163], v[186:187] op_sel_hi:[0,1]
	v_pk_mul_f32 v[28:29], v[162:163], v[184:185] op_sel_hi:[0,1]
	v_pk_mul_f32 v[28:29], v[4:5], v[28:29]
	v_pk_mul_f32 v[26:27], v[2:3], v[26:27]
	v_pk_mul_f32 v[30:31], v[6:7], v[30:31]
	v_cvt_pk_bf16_f32 v26, v26, v27
	v_cvt_pk_bf16_f32 v27, v28, v29
	s_mov_b64 s[28:29], 0xa0000
	v_cvt_pk_bf16_f32 v28, v30, v31
	v_cvt_pk_bf16_f32 v29, v32, v33
	v_pk_mul_f32 v[24:25], v[148:149], v[24:25] op_sel_hi:[0,1]
	v_pk_mul_f32 v[22:23], v[148:149], v[22:23] op_sel_hi:[0,1]
	v_pk_mul_f32 v[18:19], v[148:149], v[18:19] op_sel_hi:[0,1]
	global_store_dwordx4 v[34:35], v[26:29], off offset:256
	v_pk_mul_f32 v[20:21], v[148:149], v[20:21] op_sel_hi:[0,1]
	v_pk_mul_f32 v[22:23], v[156:157], v[22:23]
	v_lshl_add_u64 v[26:27], v[108:109], 0, s[28:29]
	v_pk_mul_f32 v[28:29], v[110:111], v[18:19]
	v_pk_mul_f32 v[18:19], v[158:159], v[24:25]
	s_mov_b32 s28, 0xa0000
	v_pk_mul_f32 v[20:21], v[112:113], v[20:21]
	v_cvt_pk_bf16_f32 v18, v18, v19
	v_cvt_pk_bf16_f32 v19, v22, v23
	v_add_co_u32_e32 v22, vcc, s28, v108
	v_cvt_pk_bf16_f32 v20, v20, v21
	v_cvt_pk_bf16_f32 v21, v28, v29
	v_pk_mul_f32 v[24:25], v[148:149], v[164:165] op_sel_hi:[0,1]
	s_nop 0
	v_addc_co_u32_e32 v23, vcc, 0, v109, vcc
	global_store_dwordx4 v[22:23], v[18:21], off
	v_pk_mul_f32 v[22:23], v[148:149], v[166:167] op_sel_hi:[0,1]
	v_pk_mul_f32 v[24:25], v[8:9], v[24:25]
	v_pk_mul_f32 v[18:19], v[148:149], v[172:173] op_sel_hi:[0,1]
	v_pk_mul_f32 v[20:21], v[148:149], v[170:171] op_sel_hi:[0,1]
	v_pk_mul_f32 v[20:21], v[4:5], v[20:21]
	v_pk_mul_f32 v[18:19], v[2:3], v[18:19]
	v_pk_mul_f32 v[22:23], v[6:7], v[22:23]
	v_cvt_pk_bf16_f32 v18, v18, v19
	v_cvt_pk_bf16_f32 v19, v20, v21
	s_mov_b64 s[28:29], 0xb0000
	v_cvt_pk_bf16_f32 v20, v22, v23
	v_cvt_pk_bf16_f32 v21, v24, v25
	v_pk_mul_f32 v[16:17], v[146:147], v[16:17] op_sel_hi:[0,1]
	v_pk_mul_f32 v[14:15], v[146:147], v[14:15] op_sel_hi:[0,1]
	v_pk_mul_f32 v[10:11], v[146:147], v[10:11] op_sel_hi:[0,1]
	global_store_dwordx4 v[26:27], v[18:21], off offset:256
	v_pk_mul_f32 v[12:13], v[146:147], v[12:13] op_sel_hi:[0,1]
	v_pk_mul_f32 v[14:15], v[156:157], v[14:15]
	v_lshl_add_u64 v[18:19], v[108:109], 0, s[28:29]
	v_pk_mul_f32 v[20:21], v[110:111], v[10:11]
	v_pk_mul_f32 v[10:11], v[158:159], v[16:17]
	s_mov_b32 s28, 0xb0000
	v_pk_mul_f32 v[12:13], v[112:113], v[12:13]
	v_cvt_pk_bf16_f32 v10, v10, v11
	v_cvt_pk_bf16_f32 v11, v14, v15
	v_add_co_u32_e32 v14, vcc, s28, v108
	v_cvt_pk_bf16_f32 v12, v12, v13
	v_cvt_pk_bf16_f32 v13, v20, v21
	v_pk_mul_f32 v[16:17], v[146:147], v[150:151] op_sel_hi:[0,1]
	s_nop 0
	v_addc_co_u32_e32 v15, vcc, 0, v109, vcc
	global_store_dwordx4 v[14:15], v[10:13], off
	v_pk_mul_f32 v[14:15], v[146:147], v[152:153] op_sel_hi:[0,1]
	s_and_b64 vcc, exec, s[0:1]
	v_pk_mul_f32 v[10:11], v[146:147], v[160:161] op_sel_hi:[0,1]
	v_pk_mul_f32 v[12:13], v[146:147], v[154:155] op_sel_hi:[0,1]
	v_pk_mul_f32 v[4:5], v[4:5], v[12:13]
	v_pk_mul_f32 v[2:3], v[2:3], v[10:11]
	s_mov_b32 s28, s84
	s_mov_b32 s29, s85
	s_mov_b32 s70, s92
	s_mov_b64 s[34:35], s[24:25]
	s_mov_b64 s[30:31], s[22:23]
	v_pk_mul_f32 v[8:9], v[8:9], v[16:17]
	v_pk_mul_f32 v[6:7], v[6:7], v[14:15]
	v_cvt_pk_bf16_f32 v2, v2, v3
	v_cvt_pk_bf16_f32 v3, v4, v5
	s_nop 0
	v_cvt_pk_bf16_f32 v4, v6, v7
	v_cvt_pk_bf16_f32 v5, v8, v9
	global_store_dwordx4 v[18:19], v[2:5], off offset:256
	s_cbranch_vccz .LBB0_2003
	s_waitcnt vmcnt(0)
	v_readlane_b32 s0, v255, 48
	v_readlane_b32 s84, v252, 13
	v_readlane_b32 s70, v252, 21
	v_readlane_b32 s74, v255, 49
	s_cmpk_gt_u32 s0, 0xff
	v_readlane_b32 s85, v252, 14
	v_readlane_b32 s71, v252, 22
	v_readlane_b32 s75, v255, 50
	s_cbranch_scc1 .LBB0_2014
	s_barrier

.LBB0_2088:
	s_add_u32 s40, s38, 0xfffc0080
	s_addc_u32 s41, s39, -1
	s_add_i32 s46, 0, 0x10000
	v_add_u32_e32 v144, s46, v145
	ds_read_b128 v[146:149], v144
	ds_read_b128 v[150:153], v144 offset:1024
	ds_read_b128 v[154:157], v144 offset:2048
	ds_read_b128 v[158:161], v144 offset:3072
	s_cmp_eq_u32 s45, 12
	s_cselect_b32 s43, s8, s41
	s_cselect_b32 s42, s27, s40
	s_cselect_b32 s41, s25, s44
	s_cselect_b32 s40, s35, s37
	v_lshl_add_u64 v[198:199], s[38:39], 0, v[140:141]
	s_add_i32 m0, s5, 0xc000
	ds_read_b128 v[164:167], v169
	ds_read_b128 v[170:173], v169 offset:1024
	ds_read_b128 v[174:177], v169 offset:2048
	ds_read_b128 v[178:181], v169 offset:3072
	ds_read_b128 v[182:185], v169 offset:4096
	ds_read_b128 v[186:189], v169 offset:5120
	ds_read_b128 v[190:193], v169 offset:6144
	ds_read_b128 v[194:197], v169 offset:7168
	global_load_lds_dwordx4 v[198:199], off
	s_add_i32 m0, s5, 0xe000
	v_lshl_add_u64 v[198:199], s[38:39], 0, v[142:143]
	global_load_lds_dwordx4 v[198:199], off
	s_waitcnt lgkmcnt(8)
	s_barrier
	s_waitcnt lgkmcnt(0)
	v_mfma_i32_16x16x64_i8 v[128:131], v[146:149], v[164:167], v[128:131]
	v_mfma_i32_16x16x64_i8 v[120:123], v[154:157], v[164:167], v[120:123]
	v_mfma_i32_16x16x64_i8 v[112:115], v[146:149], v[174:177], v[112:115]
	v_mfma_i32_16x16x64_i8 v[108:111], v[154:157], v[174:177], v[108:111]
	v_mfma_i32_16x16x64_i8 v[94:97], v[146:149], v[182:185], v[94:97]
	v_mfma_i32_16x16x64_i8 v[90:93], v[154:157], v[182:185], v[90:93]
	v_mfma_i32_16x16x64_i8 v[78:81], v[146:149], v[190:193], v[78:81]
	v_mfma_i32_16x16x64_i8 v[74:77], v[154:157], v[190:193], v[74:77]
	v_mfma_i32_16x16x64_i8 v[128:131], v[150:153], v[170:173], v[128:131]
	v_mfma_i32_16x16x64_i8 v[120:123], v[158:161], v[170:173], v[120:123]
	v_mfma_i32_16x16x64_i8 v[112:115], v[150:153], v[178:181], v[112:115]
	v_mfma_i32_16x16x64_i8 v[108:111], v[158:161], v[178:181], v[108:111]
	v_mfma_i32_16x16x64_i8 v[94:97], v[150:153], v[186:189], v[94:97]
	v_mfma_i32_16x16x64_i8 v[90:93], v[158:161], v[186:189], v[90:93]
	v_mfma_i32_16x16x64_i8 v[78:81], v[150:153], v[194:197], v[78:81]
	v_mfma_i32_16x16x64_i8 v[74:77], v[158:161], v[194:197], v[74:77]
	s_barrier
	s_add_i32 s48, 0, 0x14000
	s_add_i32 s46, s46, s3
	v_add_u32_e32 v144, s48, v145
	v_lshl_add_u64 v[214:215], s[40:41], 0, v[98:99]
	s_mov_b32 m0, s46
	ds_read_b128 v[198:201], v144
	ds_read_b128 v[202:205], v144 offset:1024
	ds_read_b128 v[206:209], v144 offset:2048
	ds_read_b128 v[210:213], v144 offset:3072
	global_load_lds_dwordx4 v[214:215], off
	s_add_i32 m0, s46, 0x2000
	v_lshl_add_u64 v[216:217], s[40:41], 0, v[136:137]
	global_load_lds_dwordx4 v[216:217], off
	s_barrier
	s_waitcnt lgkmcnt(0)
	v_mfma_i32_16x16x64_i8 v[124:127], v[198:201], v[164:167], v[124:127]
	v_mfma_i32_16x16x64_i8 v[116:119], v[206:209], v[164:167], v[116:119]
	v_mfma_i32_16x16x64_i8 v[104:107], v[198:201], v[174:177], v[104:107]
	v_mfma_i32_16x16x64_i8 v[100:103], v[206:209], v[174:177], v[100:103]
	v_mfma_i32_16x16x64_i8 v[86:89], v[198:201], v[182:185], v[86:89]
	v_mfma_i32_16x16x64_i8 v[82:85], v[206:209], v[182:185], v[82:85]
	v_mfma_i32_16x16x64_i8 v[70:73], v[198:201], v[190:193], v[70:73]
	v_mfma_i32_16x16x64_i8 v[66:69], v[206:209], v[190:193], v[66:69]
	v_mfma_i32_16x16x64_i8 v[124:127], v[202:205], v[170:173], v[124:127]
	v_mfma_i32_16x16x64_i8 v[116:119], v[210:213], v[170:173], v[116:119]
	v_mfma_i32_16x16x64_i8 v[104:107], v[202:205], v[178:181], v[104:107]
	v_mfma_i32_16x16x64_i8 v[100:103], v[210:213], v[178:181], v[100:103]
	v_mfma_i32_16x16x64_i8 v[86:89], v[202:205], v[186:189], v[86:89]
	v_mfma_i32_16x16x64_i8 v[82:85], v[210:213], v[186:189], v[82:85]
	v_mfma_i32_16x16x64_i8 v[70:73], v[202:205], v[194:197], v[70:73]
	v_mfma_i32_16x16x64_i8 v[66:69], v[210:213], v[194:197], v[66:69]
	s_mov_b32 m0, s5
	v_lshl_add_u64 v[218:219], s[42:43], 0, v[132:133]
	s_barrier
	ds_read_b128 v[164:167], v169 offset:16384
	ds_read_b128 v[170:173], v169 offset:17408
	ds_read_b128 v[174:177], v169 offset:18432
	ds_read_b128 v[178:181], v169 offset:19456
	ds_read_b128 v[182:185], v169 offset:20480
	ds_read_b128 v[186:189], v169 offset:21504
	ds_read_b128 v[190:193], v169 offset:22528
	ds_read_b128 v[194:197], v169 offset:23552
	global_load_lds_dwordx4 v[218:219], off
	s_mov_b32 m0, s18
	v_lshl_add_u64 v[222:223], s[42:43], 0, v[134:135]
	global_load_lds_dwordx4 v[222:223], off
	s_barrier
	s_waitcnt lgkmcnt(0)
	v_mfma_i32_16x16x64_i8 v[62:65], v[146:149], v[164:167], v[62:65]
	v_mfma_i32_16x16x64_i8 v[58:61], v[154:157], v[164:167], v[58:61]
	v_mfma_i32_16x16x64_i8 v[46:49], v[146:149], v[174:177], v[46:49]
	v_mfma_i32_16x16x64_i8 v[42:45], v[154:157], v[174:177], v[42:45]
	v_mfma_i32_16x16x64_i8 v[30:33], v[146:149], v[182:185], v[30:33]
	v_mfma_i32_16x16x64_i8 v[26:29], v[154:157], v[182:185], v[26:29]
	v_mfma_i32_16x16x64_i8 v[14:17], v[146:149], v[190:193], v[14:17]
	v_mfma_i32_16x16x64_i8 v[10:13], v[154:157], v[190:193], v[10:13]
	v_mfma_i32_16x16x64_i8 v[62:65], v[150:153], v[170:173], v[62:65]
	v_mfma_i32_16x16x64_i8 v[58:61], v[158:161], v[170:173], v[58:61]
	v_mfma_i32_16x16x64_i8 v[46:49], v[150:153], v[178:181], v[46:49]
	v_mfma_i32_16x16x64_i8 v[42:45], v[158:161], v[178:181], v[42:45]
	v_mfma_i32_16x16x64_i8 v[30:33], v[150:153], v[186:189], v[30:33]
	v_mfma_i32_16x16x64_i8 v[26:29], v[158:161], v[186:189], v[26:29]
	v_mfma_i32_16x16x64_i8 v[14:17], v[150:153], v[194:197], v[14:17]
	v_mfma_i32_16x16x64_i8 v[10:13], v[158:161], v[194:197], v[10:13]
	s_barrier
	s_add_u32 s46, s40, 0x40000
	s_addc_u32 s47, s41, 0
	s_add_i32 s48, s48, s3
	s_mov_b32 m0, s48
	v_lshl_add_u64 v[146:147], s[46:47], 0, v[98:99]
	global_load_lds_dwordx4 v[146:147], off
	s_add_i32 m0, s48, 0x2000
	v_lshl_add_u64 v[146:147], s[46:47], 0, v[136:137]
	global_load_lds_dwordx4 v[146:147], off
	s_waitcnt vmcnt(6)
	s_barrier
	v_mfma_i32_16x16x64_i8 v[54:57], v[198:201], v[164:167], v[54:57]
	v_mfma_i32_16x16x64_i8 v[50:53], v[206:209], v[164:167], v[50:53]
	v_mfma_i32_16x16x64_i8 v[38:41], v[198:201], v[174:177], v[38:41]
	v_mfma_i32_16x16x64_i8 v[34:37], v[206:209], v[174:177], v[34:37]
	v_mfma_i32_16x16x64_i8 v[22:25], v[198:201], v[182:185], v[22:25]
	v_mfma_i32_16x16x64_i8 v[18:21], v[206:209], v[182:185], v[18:21]
	v_mfma_i32_16x16x64_i8 v[6:9], v[198:201], v[190:193], v[6:9]
	v_mfma_i32_16x16x64_i8 v[2:5], v[206:209], v[190:193], v[2:5]
	v_mfma_i32_16x16x64_i8 v[54:57], v[202:205], v[170:173], v[54:57]
	v_mfma_i32_16x16x64_i8 v[50:53], v[210:213], v[170:173], v[50:53]
	v_mfma_i32_16x16x64_i8 v[38:41], v[202:205], v[178:181], v[38:41]
	v_mfma_i32_16x16x64_i8 v[34:37], v[210:213], v[178:181], v[34:37]
	v_mfma_i32_16x16x64_i8 v[22:25], v[202:205], v[186:189], v[22:25]
	v_mfma_i32_16x16x64_i8 v[18:21], v[210:213], v[186:189], v[18:21]
	v_mfma_i32_16x16x64_i8 v[6:9], v[202:205], v[194:197], v[6:9]
	v_mfma_i32_16x16x64_i8 v[2:5], v[210:213], v[194:197], v[2:5]
	s_add_i32 s46, 0, 0x18000
	v_add_u32_e32 v144, s46, v145
	s_barrier
	ds_read_b128 v[146:149], v144
	ds_read_b128 v[150:153], v144 offset:1024
	ds_read_b128 v[154:157], v144 offset:2048
	ds_read_b128 v[158:161], v144 offset:3072
	s_add_u32 s42, s42, 0x40000
	s_addc_u32 s43, s43, 0
	s_mov_b32 m0, s19
	v_lshl_add_u64 v[198:199], s[42:43], 0, v[132:133]
	ds_read_b128 v[164:167], v169 offset:32768
	ds_read_b128 v[170:173], v169 offset:33792
	ds_read_b128 v[174:177], v169 offset:34816
	ds_read_b128 v[178:181], v169 offset:35840
	ds_read_b128 v[182:185], v169 offset:36864
	ds_read_b128 v[186:189], v169 offset:37888
	ds_read_b128 v[190:193], v169 offset:38912
	ds_read_b128 v[194:197], v169 offset:39936
	global_load_lds_dwordx4 v[198:199], off
	s_mov_b32 m0, s20
	v_lshl_add_u64 v[198:199], s[42:43], 0, v[134:135]
	global_load_lds_dwordx4 v[198:199], off
	s_waitcnt lgkmcnt(8)
	s_barrier
	s_waitcnt lgkmcnt(0)
	v_mfma_i32_16x16x64_i8 v[128:131], v[146:149], v[164:167], v[128:131]
	v_mfma_i32_16x16x64_i8 v[120:123], v[154:157], v[164:167], v[120:123]
	v_mfma_i32_16x16x64_i8 v[112:115], v[146:149], v[174:177], v[112:115]
	v_mfma_i32_16x16x64_i8 v[108:111], v[154:157], v[174:177], v[108:111]
	v_mfma_i32_16x16x64_i8 v[94:97], v[146:149], v[182:185], v[94:97]
	v_mfma_i32_16x16x64_i8 v[90:93], v[154:157], v[182:185], v[90:93]
	v_mfma_i32_16x16x64_i8 v[78:81], v[146:149], v[190:193], v[78:81]
	v_mfma_i32_16x16x64_i8 v[74:77], v[154:157], v[190:193], v[74:77]
	v_mfma_i32_16x16x64_i8 v[128:131], v[150:153], v[170:173], v[128:131]
	v_mfma_i32_16x16x64_i8 v[120:123], v[158:161], v[170:173], v[120:123]
	v_mfma_i32_16x16x64_i8 v[112:115], v[150:153], v[178:181], v[112:115]
	v_mfma_i32_16x16x64_i8 v[108:111], v[158:161], v[178:181], v[108:111]
	v_mfma_i32_16x16x64_i8 v[94:97], v[150:153], v[186:189], v[94:97]
	v_mfma_i32_16x16x64_i8 v[90:93], v[158:161], v[186:189], v[90:93]
	v_mfma_i32_16x16x64_i8 v[78:81], v[150:153], v[194:197], v[78:81]
	v_mfma_i32_16x16x64_i8 v[74:77], v[158:161], v[194:197], v[74:77]
	s_barrier
	s_add_i32 s42, 0, 0x1c000
	s_add_i32 s43, s46, s3
	v_add_u32_e32 v144, s42, v145
	v_lshl_add_u64 v[214:215], v[214:215], 0, s[68:69]
	s_mov_b32 m0, s43
	ds_read_b128 v[198:201], v144
	ds_read_b128 v[202:205], v144 offset:1024
	ds_read_b128 v[206:209], v144 offset:2048
	ds_read_b128 v[210:213], v144 offset:3072
	global_load_lds_dwordx4 v[214:215], off
	s_add_i32 m0, s43, 0x2000
	v_lshl_add_u64 v[214:215], v[216:217], 0, s[68:69]
	global_load_lds_dwordx4 v[214:215], off
	s_barrier
	s_waitcnt lgkmcnt(0)
	v_mfma_i32_16x16x64_i8 v[124:127], v[198:201], v[164:167], v[124:127]
	v_mfma_i32_16x16x64_i8 v[116:119], v[206:209], v[164:167], v[116:119]
	v_mfma_i32_16x16x64_i8 v[104:107], v[198:201], v[174:177], v[104:107]
	v_mfma_i32_16x16x64_i8 v[100:103], v[206:209], v[174:177], v[100:103]
	v_mfma_i32_16x16x64_i8 v[86:89], v[198:201], v[182:185], v[86:89]
	v_mfma_i32_16x16x64_i8 v[82:85], v[206:209], v[182:185], v[82:85]
	v_mfma_i32_16x16x64_i8 v[70:73], v[198:201], v[190:193], v[70:73]
	v_mfma_i32_16x16x64_i8 v[66:69], v[206:209], v[190:193], v[66:69]
	v_mfma_i32_16x16x64_i8 v[124:127], v[202:205], v[170:173], v[124:127]
	v_mfma_i32_16x16x64_i8 v[116:119], v[210:213], v[170:173], v[116:119]
	v_mfma_i32_16x16x64_i8 v[104:107], v[202:205], v[178:181], v[104:107]
	v_mfma_i32_16x16x64_i8 v[100:103], v[210:213], v[178:181], v[100:103]
	v_mfma_i32_16x16x64_i8 v[86:89], v[202:205], v[186:189], v[86:89]
	v_mfma_i32_16x16x64_i8 v[82:85], v[210:213], v[186:189], v[82:85]
	v_mfma_i32_16x16x64_i8 v[70:73], v[202:205], v[194:197], v[70:73]
	v_mfma_i32_16x16x64_i8 v[66:69], v[210:213], v[194:197], v[66:69]
	s_mov_b32 m0, s9
	v_lshl_add_u64 v[214:215], v[218:219], 0, s[68:69]
	s_barrier
	ds_read_b128 v[164:167], v169 offset:49152
	ds_read_b128 v[170:173], v169 offset:50176
	ds_read_b128 v[174:177], v169 offset:51200
	ds_read_b128 v[178:181], v169 offset:52224
	ds_read_b128 v[182:185], v169 offset:53248
	ds_read_b128 v[186:189], v169 offset:54272
	ds_read_b128 v[190:193], v169 offset:55296
	ds_read_b128 v[194:197], v169 offset:56320
	global_load_lds_dwordx4 v[214:215], off
	s_mov_b32 m0, s21
	v_lshl_add_u64 v[214:215], v[222:223], 0, s[68:69]
	global_load_lds_dwordx4 v[214:215], off
	s_barrier
	s_waitcnt lgkmcnt(0)
	v_mfma_i32_16x16x64_i8 v[62:65], v[146:149], v[164:167], v[62:65]
	v_mfma_i32_16x16x64_i8 v[58:61], v[154:157], v[164:167], v[58:61]
	v_mfma_i32_16x16x64_i8 v[46:49], v[146:149], v[174:177], v[46:49]
	v_mfma_i32_16x16x64_i8 v[42:45], v[154:157], v[174:177], v[42:45]
	v_mfma_i32_16x16x64_i8 v[30:33], v[146:149], v[182:185], v[30:33]
	v_mfma_i32_16x16x64_i8 v[26:29], v[154:157], v[182:185], v[26:29]
	v_mfma_i32_16x16x64_i8 v[14:17], v[146:149], v[190:193], v[14:17]
	v_mfma_i32_16x16x64_i8 v[10:13], v[154:157], v[190:193], v[10:13]
	v_mfma_i32_16x16x64_i8 v[62:65], v[150:153], v[170:173], v[62:65]
	v_mfma_i32_16x16x64_i8 v[58:61], v[158:161], v[170:173], v[58:61]
	v_mfma_i32_16x16x64_i8 v[46:49], v[150:153], v[178:181], v[46:49]
	v_mfma_i32_16x16x64_i8 v[42:45], v[158:161], v[178:181], v[42:45]
	v_mfma_i32_16x16x64_i8 v[30:33], v[150:153], v[186:189], v[30:33]
	v_mfma_i32_16x16x64_i8 v[26:29], v[158:161], v[186:189], v[26:29]
	v_mfma_i32_16x16x64_i8 v[14:17], v[150:153], v[194:197], v[14:17]
	v_mfma_i32_16x16x64_i8 v[10:13], v[158:161], v[194:197], v[10:13]
	s_barrier
	s_add_u32 s40, s40, 0x40080
	s_addc_u32 s41, s41, 0
	s_add_i32 s42, s42, s3
	s_mov_b32 m0, s42
	v_lshl_add_u64 v[146:147], s[40:41], 0, v[98:99]
	global_load_lds_dwordx4 v[146:147], off
	s_add_i32 m0, s42, 0x2000
	v_lshl_add_u64 v[146:147], s[40:41], 0, v[136:137]
	global_load_lds_dwordx4 v[146:147], off
	s_waitcnt vmcnt(6)
	s_barrier
	v_mfma_i32_16x16x64_i8 v[54:57], v[198:201], v[164:167], v[54:57]
	v_mfma_i32_16x16x64_i8 v[50:53], v[206:209], v[164:167], v[50:53]
	v_mfma_i32_16x16x64_i8 v[38:41], v[198:201], v[174:177], v[38:41]
	v_mfma_i32_16x16x64_i8 v[34:37], v[206:209], v[174:177], v[34:37]
	v_mfma_i32_16x16x64_i8 v[22:25], v[198:201], v[182:185], v[22:25]
	v_mfma_i32_16x16x64_i8 v[18:21], v[206:209], v[182:185], v[18:21]
	v_mfma_i32_16x16x64_i8 v[6:9], v[198:201], v[190:193], v[6:9]
	v_mfma_i32_16x16x64_i8 v[2:5], v[206:209], v[190:193], v[2:5]
	v_mfma_i32_16x16x64_i8 v[54:57], v[202:205], v[170:173], v[54:57]
	v_mfma_i32_16x16x64_i8 v[50:53], v[210:213], v[170:173], v[50:53]
	v_mfma_i32_16x16x64_i8 v[38:41], v[202:205], v[178:181], v[38:41]
	v_mfma_i32_16x16x64_i8 v[34:37], v[210:213], v[178:181], v[34:37]
	v_mfma_i32_16x16x64_i8 v[22:25], v[202:205], v[186:189], v[22:25]
	v_mfma_i32_16x16x64_i8 v[18:21], v[210:213], v[186:189], v[18:21]
	v_mfma_i32_16x16x64_i8 v[6:9], v[202:205], v[194:197], v[6:9]
	v_mfma_i32_16x16x64_i8 v[2:5], v[210:213], v[194:197], v[2:5]
	s_add_i32 s45, s45, 2
	s_add_u32 s38, s38, 0x100
	s_addc_u32 s39, s39, 0
	s_add_u32 s37, s37, 0x100
	s_addc_u32 s44, s44, 0
	s_cmp_gt_u32 s45, 13
	s_barrier
	s_cbranch_scc0 .LBB0_2088
	v_lshl_add_u32 v146, s36, 8, v1
	v_ashrrev_i32_e32 v147, 31, v146
	s_lshl_b32 s36, s34, 8
	v_lshl_add_u64 v[148:149], v[146:147], 2, s[54:55]
	s_ashr_i32 s37, s36, 31
	global_load_dword v182, v[148:149], off
	global_load_dword v180, v[148:149], off offset:64
	global_load_dword v174, v[148:149], off offset:128
	global_load_dword v172, v[148:149], off offset:192
	global_load_dword v170, v[148:149], off offset:512
	global_load_dword v168, v[148:149], off offset:576
	global_load_dword v162, v[148:149], off offset:640
	global_load_dword v144, v[148:149], off offset:704
	v_lshl_add_u64 v[148:149], s[36:37], 2, v[138:139]
	global_load_dwordx4 v[176:179], v[148:149], off offset:16
	global_load_dwordx4 v[150:153], v[148:149], off
	global_load_dwordx4 v[184:187], v[148:149], off offset:528
	global_load_dwordx4 v[154:157], v[148:149], off offset:512
	v_lshl_or_b32 v148, s34, 7, v163
	v_readlane_b32 s34, v252, 59
	v_readlane_b32 s35, v252, 60
	s_movk_i32 s8, 0x2c00
	v_cvt_f32_i32_e32 v129, v129
	v_cvt_f32_i32_e32 v121, v121
	v_ashrrev_i32_e32 v149, 31, v148
	s_waitcnt vmcnt(0)
	v_mov_b32_e32 v159, v150
	v_mov_b32_e32 v150, v155
	v_pk_mul_f32 v[164:165], v[150:151], s[58:59] op_sel_hi:[1,0]
	v_mov_b32_e32 v150, v156
	v_mov_b32_e32 v151, v152
	v_pk_mul_f32 v[160:161], v[150:151], s[58:59] op_sel_hi:[1,0]
	v_mov_b32_e32 v151, v176
	v_mov_b32_e32 v176, v185
	v_mov_b32_e32 v158, v154
	v_pk_mul_f32 v[154:155], v[176:177], s[58:59] op_sel_hi:[1,0]
	v_mov_b64_e32 v[176:177], s[34:35]
	v_mov_b32_e32 v150, v184
	v_mad_i64_i32 v[184:185], s[34:35], v146, s8, v[176:177]
	v_cvt_f32_i32_e32 v177, v128
	v_cvt_f32_i32_e32 v176, v124
	v_pk_mul_f32 v[166:167], v[158:159], s[58:59] op_sel_hi:[1,0]
	v_mov_b32_e32 v152, v157
	v_pk_mul_f32 v[156:157], v[150:151], s[58:59] op_sel_hi:[1,0]
	v_mov_b32_e32 v150, v186
	v_mov_b32_e32 v151, v178
	v_mov_b32_e32 v178, v187
	v_pk_mul_f32 v[158:159], v[152:153], s[58:59] op_sel_hi:[1,0]
	v_pk_mul_f32 v[152:153], v[150:151], s[58:59] op_sel_hi:[1,0]
	v_pk_mul_f32 v[150:151], v[178:179], s[58:59] op_sel_hi:[1,0]
	v_pk_mul_f32 v[178:179], v[182:183], v[166:167] op_sel_hi:[0,1]
	v_pk_mul_f32 v[176:177], v[178:179], v[176:177]
	v_cvt_f32_i32_e32 v128, v125
	v_mul_f32_e32 v124, 0xbfb8aa3b, v177
	v_exp_f32_e32 v124, v124
	s_nop 0
	v_add_f32_e32 v124, 1.0, v124
	v_rcp_f32_e32 v124, v124
	s_nop 0
	v_mul_f32_e32 v124, v177, v124
	v_mul_f32_e32 v124, v176, v124
	v_pk_mul_f32 v[176:177], v[182:183], v[164:165] op_sel_hi:[0,1]
	v_pk_mul_f32 v[128:129], v[176:177], v[128:129]
	v_pk_mul_f32 v[176:177], v[182:183], v[160:161] op_sel_hi:[0,1]
	v_mul_f32_e32 v125, 0xbfb8aa3b, v129
	v_exp_f32_e32 v125, v125
	s_nop 0
	v_add_f32_e32 v125, 1.0, v125
	v_rcp_f32_e32 v125, v125
	s_nop 0
	v_mul_f32_e32 v125, v129, v125
	v_mul_f32_e32 v125, v128, v125
	v_cvt_f32_i32_e32 v129, v130
	v_cvt_f32_i32_e32 v128, v126
	v_pk_mul_f32 v[128:129], v[176:177], v[128:129]
	s_nop 0
	v_mul_f32_e32 v126, 0xbfb8aa3b, v129
	v_exp_f32_e32 v126, v126
	s_nop 0
	v_add_f32_e32 v126, 1.0, v126
	v_rcp_f32_e32 v126, v126
	s_nop 0
	v_mul_f32_e32 v126, v129, v126
	v_mul_f32_e32 v126, v128, v126
	v_cvt_f32_i32_e32 v129, v131
	v_cvt_f32_i32_e32 v128, v127
	v_pk_mul_f32 v[130:131], v[182:183], v[158:159] op_sel_hi:[0,1]
	v_pk_mul_f32 v[128:129], v[130:131], v[128:129]
	s_nop 0
	v_mul_f32_e32 v127, 0xbfb8aa3b, v129
	v_exp_f32_e32 v127, v127
	v_pk_mul_f32 v[130:131], v[182:183], v[156:157] op_sel_hi:[0,1]
	v_add_f32_e32 v127, 1.0, v127
	v_rcp_f32_e32 v127, v127
	s_nop 0
	v_mul_f32_e32 v127, v129, v127
	v_mul_f32_e32 v127, v128, v127
	v_cvt_f32_i32_e32 v129, v120
	v_cvt_f32_i32_e32 v128, v116
	v_cvt_f32_i32_e32 v120, v117
	v_pk_mul_f32 v[128:129], v[130:131], v[128:129]
	s_nop 0
	v_mul_f32_e32 v116, 0xbfb8aa3b, v129
	v_exp_f32_e32 v116, v116
	s_nop 0
	v_add_f32_e32 v116, 1.0, v116
	v_rcp_f32_e32 v116, v116
	s_nop 0
	v_mul_f32_e32 v116, v129, v116
	v_mul_f32_e32 v128, v128, v116
	v_pk_mul_f32 v[116:117], v[182:183], v[154:155] op_sel_hi:[0,1]
	v_pk_mul_f32 v[116:117], v[116:117], v[120:121]
	s_nop 0
	v_mul_f32_e32 v120, 0xbfb8aa3b, v117
	v_exp_f32_e32 v120, v120
	s_nop 0
	v_add_f32_e32 v120, 1.0, v120
	v_rcp_f32_e32 v120, v120
	s_nop 0
	v_mul_f32_e32 v117, v117, v120
	v_mul_f32_e32 v129, v116, v117
	v_cvt_f32_i32_e32 v117, v122
	v_cvt_f32_i32_e32 v116, v118
	v_pk_mul_f32 v[120:121], v[182:183], v[152:153] op_sel_hi:[0,1]
	v_pk_mul_f32 v[116:117], v[120:121], v[116:117]
	s_nop 0
	v_mul_f32_e32 v118, 0xbfb8aa3b, v117
	v_exp_f32_e32 v118, v118
	v_lshl_add_u64 v[120:121], v[148:149], 1, v[184:185]
	v_add_f32_e32 v118, 1.0, v118
	v_rcp_f32_e32 v118, v118
	s_nop 0
	v_mul_f32_e32 v117, v117, v118
	v_mul_f32_e32 v122, v116, v117
	v_cvt_f32_i32_e32 v117, v123
	v_cvt_f32_i32_e32 v116, v119
	v_pk_mul_f32 v[118:119], v[182:183], v[150:151] op_sel_hi:[0,1]
	v_pk_mul_f32 v[116:117], v[118:119], v[116:117]
	s_nop 0
	v_mul_f32_e32 v118, 0xbfb8aa3b, v117
	v_exp_f32_e32 v118, v118
	s_nop 0
	v_add_f32_e32 v118, 1.0, v118
	v_rcp_f32_e32 v118, v118
	s_nop 0
	v_mul_f32_e32 v117, v117, v118
	v_mul_f32_e32 v123, v116, v117
	v_cvt_pk_bf16_f32 v116, v124, v125
	v_cvt_pk_bf16_f32 v117, v126, v127
	v_cvt_pk_bf16_f32 v118, v128, v129
	v_cvt_pk_bf16_f32 v119, v122, v123
	global_store_dwordx4 v[120:121], v[116:119], off
	s_nop 1
	v_max_f32_e64 v118, |v122|, |v123|
	v_max_f32_e64 v116, |v124|, |v125|
	v_max_f32_e64 v117, |v126|, |v127|
	v_max3_f32 v118, |v128|, |v129|, v118
	v_max3_f32 v116, v116, v117, v118
	v_mov_b32_e32 v117, v0
	s_nop 0
	v_lshlrev_b32_e32 v117, 2, v117
	v_bitop3_b32 v118, v117, 64, v220 bitop3:0x6c
	ds_bpermute_b32 v118, v118, v116
	v_bitop3_b32 v117, v117, s59, v220 bitop3:0x6c
	s_waitcnt lgkmcnt(0)
	v_max_f32_e32 v118, v118, v118
	v_max_f32_e32 v116, v116, v118
	ds_bpermute_b32 v117, v117, v116
	s_and_saveexec_b64 s[34:35], s[0:1]
	s_cbranch_execz .LBB0_2091
	v_readlane_b32 s36, v253, 57
	s_waitcnt lgkmcnt(0)
	v_max_f32_e32 v117, v117, v117
	v_max_f32_e32 v116, v116, v116
	v_readlane_b32 s37, v253, 58
	v_max_f32_e32 v118, v116, v117
	s_nop 0
	v_lshl_add_u64 v[116:117], v[146:147], 2, s[36:37]
	global_atomic_umax v[116:117], v118, off

.LBB0_2238:
	s_add_i32 s46, s30, 2
	s_add_u32 s28, s26, 0x100
	s_addc_u32 s29, s27, 0
	s_add_i32 s47, 0, 0x10000
	v_add_u32_e32 v142, s47, v1
	ds_read_b128 v[144:147], v142
	ds_read_b128 v[148:151], v142 offset:1024
	ds_read_b128 v[152:155], v142 offset:2048
	ds_read_b128 v[156:159], v142 offset:3072
	s_cmp_eq_u32 s19, s30
	s_cselect_b32 s30, s0, s33
	s_cselect_b32 s35, s25, s29
	s_cselect_b32 s34, s24, s28
	s_cselect_b32 s31, s1, s45
	v_lshl_add_u64 v[192:193], s[26:27], 0, v[138:139]
	s_add_i32 m0, s20, 0xc000
	ds_read_b128 v[160:163], v143
	ds_read_b128 v[164:167], v143 offset:1024
	ds_read_b128 v[168:171], v143 offset:2048
	ds_read_b128 v[172:175], v143 offset:3072
	ds_read_b128 v[176:179], v143 offset:4096
	ds_read_b128 v[180:183], v143 offset:5120
	ds_read_b128 v[184:187], v143 offset:6144
	ds_read_b128 v[188:191], v143 offset:7168
	global_load_lds_dwordx4 v[192:193], off
	s_add_i32 m0, s20, 0xe000
	v_lshl_add_u64 v[192:193], s[26:27], 0, v[140:141]
	global_load_lds_dwordx4 v[192:193], off
	s_waitcnt lgkmcnt(8)
	s_barrier
	s_waitcnt lgkmcnt(0)
	v_mfma_i32_16x16x64_i8 v[128:131], v[144:147], v[160:163], v[128:131]
	v_mfma_i32_16x16x64_i8 v[124:127], v[152:155], v[160:163], v[124:127]
	v_mfma_i32_16x16x64_i8 v[120:123], v[144:147], v[168:171], v[120:123]
	v_mfma_i32_16x16x64_i8 v[116:119], v[152:155], v[168:171], v[116:119]
	v_mfma_i32_16x16x64_i8 v[112:115], v[144:147], v[176:179], v[112:115]
	v_mfma_i32_16x16x64_i8 v[108:111], v[152:155], v[176:179], v[108:111]
	v_mfma_i32_16x16x64_i8 v[104:107], v[144:147], v[184:187], v[104:107]
	v_mfma_i32_16x16x64_i8 v[100:103], v[152:155], v[184:187], v[100:103]
	v_mfma_i32_16x16x64_i8 v[128:131], v[148:151], v[164:167], v[128:131]
	v_mfma_i32_16x16x64_i8 v[124:127], v[156:159], v[164:167], v[124:127]
	v_mfma_i32_16x16x64_i8 v[120:123], v[148:151], v[172:175], v[120:123]
	v_mfma_i32_16x16x64_i8 v[116:119], v[156:159], v[172:175], v[116:119]
	v_mfma_i32_16x16x64_i8 v[112:115], v[148:151], v[180:183], v[112:115]
	v_mfma_i32_16x16x64_i8 v[108:111], v[156:159], v[180:183], v[108:111]
	v_mfma_i32_16x16x64_i8 v[104:107], v[148:151], v[188:191], v[104:107]
	v_mfma_i32_16x16x64_i8 v[100:103], v[156:159], v[188:191], v[100:103]
	s_barrier
	s_add_i32 s48, 0, 0x14000
	s_add_i32 s26, s47, s5
	v_add_u32_e32 v142, s48, v1
	v_lshl_add_u64 v[208:209], s[30:31], 0, v[98:99]
	s_mov_b32 m0, s26
	ds_read_b128 v[192:195], v142
	ds_read_b128 v[196:199], v142 offset:1024
	ds_read_b128 v[200:203], v142 offset:2048
	ds_read_b128 v[204:207], v142 offset:3072
	global_load_lds_dwordx4 v[208:209], off
	s_add_i32 m0, s26, 0x2000
	v_lshl_add_u64 v[210:211], s[30:31], 0, v[132:133]
	global_load_lds_dwordx4 v[210:211], off
	s_barrier
	s_waitcnt lgkmcnt(0)
	v_mfma_i32_16x16x64_i8 v[94:97], v[192:195], v[160:163], v[94:97]
	v_mfma_i32_16x16x64_i8 v[90:93], v[200:203], v[160:163], v[90:93]
	v_mfma_i32_16x16x64_i8 v[86:89], v[192:195], v[168:171], v[86:89]
	v_mfma_i32_16x16x64_i8 v[82:85], v[200:203], v[168:171], v[82:85]
	v_mfma_i32_16x16x64_i8 v[78:81], v[192:195], v[176:179], v[78:81]
	v_mfma_i32_16x16x64_i8 v[74:77], v[200:203], v[176:179], v[74:77]
	v_mfma_i32_16x16x64_i8 v[70:73], v[192:195], v[184:187], v[70:73]
	v_mfma_i32_16x16x64_i8 v[66:69], v[200:203], v[184:187], v[66:69]
	v_mfma_i32_16x16x64_i8 v[94:97], v[196:199], v[164:167], v[94:97]
	v_mfma_i32_16x16x64_i8 v[90:93], v[204:207], v[164:167], v[90:93]
	v_mfma_i32_16x16x64_i8 v[86:89], v[196:199], v[172:175], v[86:89]
	v_mfma_i32_16x16x64_i8 v[82:85], v[204:207], v[172:175], v[82:85]
	v_mfma_i32_16x16x64_i8 v[78:81], v[196:199], v[180:183], v[78:81]
	v_mfma_i32_16x16x64_i8 v[74:77], v[204:207], v[180:183], v[74:77]
	v_mfma_i32_16x16x64_i8 v[70:73], v[196:199], v[188:191], v[70:73]
	v_mfma_i32_16x16x64_i8 v[66:69], v[204:207], v[188:191], v[66:69]
	s_mov_b32 m0, s20
	v_lshl_add_u64 v[212:213], s[34:35], 0, v[98:99]
	s_barrier
	ds_read_b128 v[160:163], v143 offset:16384
	ds_read_b128 v[164:167], v143 offset:17408
	ds_read_b128 v[168:171], v143 offset:18432
	ds_read_b128 v[172:175], v143 offset:19456
	ds_read_b128 v[176:179], v143 offset:20480
	ds_read_b128 v[180:183], v143 offset:21504
	ds_read_b128 v[184:187], v143 offset:22528
	ds_read_b128 v[188:191], v143 offset:23552
	global_load_lds_dwordx4 v[212:213], off
	s_mov_b32 m0, s21
	v_lshl_add_u64 v[214:215], s[34:35], 0, v[132:133]
	global_load_lds_dwordx4 v[214:215], off
	s_barrier
	s_waitcnt lgkmcnt(0)
	v_mfma_i32_16x16x64_i8 v[62:65], v[144:147], v[160:163], v[62:65]
	v_mfma_i32_16x16x64_i8 v[58:61], v[152:155], v[160:163], v[58:61]
	v_mfma_i32_16x16x64_i8 v[54:57], v[144:147], v[168:171], v[54:57]
	v_mfma_i32_16x16x64_i8 v[50:53], v[152:155], v[168:171], v[50:53]
	v_mfma_i32_16x16x64_i8 v[46:49], v[144:147], v[176:179], v[46:49]
	v_mfma_i32_16x16x64_i8 v[42:45], v[152:155], v[176:179], v[42:45]
	v_mfma_i32_16x16x64_i8 v[38:41], v[144:147], v[184:187], v[38:41]
	v_mfma_i32_16x16x64_i8 v[34:37], v[152:155], v[184:187], v[34:37]
	v_mfma_i32_16x16x64_i8 v[62:65], v[148:151], v[164:167], v[62:65]
	v_mfma_i32_16x16x64_i8 v[58:61], v[156:159], v[164:167], v[58:61]
	v_mfma_i32_16x16x64_i8 v[54:57], v[148:151], v[172:175], v[54:57]
	v_mfma_i32_16x16x64_i8 v[50:53], v[156:159], v[172:175], v[50:53]
	v_mfma_i32_16x16x64_i8 v[46:49], v[148:151], v[180:183], v[46:49]
	v_mfma_i32_16x16x64_i8 v[42:45], v[156:159], v[180:183], v[42:45]
	v_mfma_i32_16x16x64_i8 v[38:41], v[148:151], v[188:191], v[38:41]
	v_mfma_i32_16x16x64_i8 v[34:37], v[156:159], v[188:191], v[34:37]
	s_barrier
	s_add_u32 s26, s30, 0xb0000
	s_addc_u32 s27, s31, 0
	s_add_i32 s47, s48, s5
	s_mov_b32 m0, s47
	v_lshl_add_u64 v[144:145], s[26:27], 0, v[98:99]
	global_load_lds_dwordx4 v[144:145], off
	s_add_i32 m0, s47, 0x2000
	v_lshl_add_u64 v[144:145], s[26:27], 0, v[132:133]
	global_load_lds_dwordx4 v[144:145], off
	s_waitcnt vmcnt(6)
	s_barrier
	v_mfma_i32_16x16x64_i8 v[30:33], v[192:195], v[160:163], v[30:33]
	v_mfma_i32_16x16x64_i8 v[26:29], v[200:203], v[160:163], v[26:29]
	v_mfma_i32_16x16x64_i8 v[22:25], v[192:195], v[168:171], v[22:25]
	v_mfma_i32_16x16x64_i8 v[18:21], v[200:203], v[168:171], v[18:21]
	v_mfma_i32_16x16x64_i8 v[14:17], v[192:195], v[176:179], v[14:17]
	v_mfma_i32_16x16x64_i8 v[10:13], v[200:203], v[176:179], v[10:13]
	v_mfma_i32_16x16x64_i8 v[6:9], v[192:195], v[184:187], v[6:9]
	v_mfma_i32_16x16x64_i8 v[2:5], v[200:203], v[184:187], v[2:5]
	v_mfma_i32_16x16x64_i8 v[30:33], v[196:199], v[164:167], v[30:33]
	v_mfma_i32_16x16x64_i8 v[26:29], v[204:207], v[164:167], v[26:29]
	v_mfma_i32_16x16x64_i8 v[22:25], v[196:199], v[172:175], v[22:25]
	v_mfma_i32_16x16x64_i8 v[18:21], v[204:207], v[172:175], v[18:21]
	v_mfma_i32_16x16x64_i8 v[14:17], v[196:199], v[180:183], v[14:17]
	v_mfma_i32_16x16x64_i8 v[10:13], v[204:207], v[180:183], v[10:13]
	v_mfma_i32_16x16x64_i8 v[6:9], v[196:199], v[188:191], v[6:9]
	v_mfma_i32_16x16x64_i8 v[2:5], v[204:207], v[188:191], v[2:5]
	s_add_i32 s47, 0, 0x18000
	v_add_u32_e32 v142, s47, v1
	s_barrier
	ds_read_b128 v[144:147], v142
	ds_read_b128 v[148:151], v142 offset:1024
	ds_read_b128 v[152:155], v142 offset:2048
	ds_read_b128 v[156:159], v142 offset:3072
	s_add_u32 s26, s34, 0xb0000
	s_addc_u32 s27, s35, 0
	s_mov_b32 m0, s36
	v_lshl_add_u64 v[192:193], s[26:27], 0, v[98:99]
	ds_read_b128 v[160:163], v143 offset:32768
	ds_read_b128 v[164:167], v143 offset:33792
	ds_read_b128 v[168:171], v143 offset:34816
	ds_read_b128 v[172:175], v143 offset:35840
	ds_read_b128 v[176:179], v143 offset:36864
	ds_read_b128 v[180:183], v143 offset:37888
	ds_read_b128 v[184:187], v143 offset:38912
	ds_read_b128 v[188:191], v143 offset:39936
	global_load_lds_dwordx4 v[192:193], off
	s_mov_b32 m0, s37
	v_lshl_add_u64 v[192:193], s[26:27], 0, v[132:133]
	global_load_lds_dwordx4 v[192:193], off
	s_waitcnt lgkmcnt(8)
	s_barrier
	s_waitcnt lgkmcnt(0)
	v_mfma_i32_16x16x64_i8 v[128:131], v[144:147], v[160:163], v[128:131]
	v_mfma_i32_16x16x64_i8 v[124:127], v[152:155], v[160:163], v[124:127]
	v_mfma_i32_16x16x64_i8 v[120:123], v[144:147], v[168:171], v[120:123]
	v_mfma_i32_16x16x64_i8 v[116:119], v[152:155], v[168:171], v[116:119]
	v_mfma_i32_16x16x64_i8 v[112:115], v[144:147], v[176:179], v[112:115]
	v_mfma_i32_16x16x64_i8 v[108:111], v[152:155], v[176:179], v[108:111]
	v_mfma_i32_16x16x64_i8 v[104:107], v[144:147], v[184:187], v[104:107]
	v_mfma_i32_16x16x64_i8 v[100:103], v[152:155], v[184:187], v[100:103]
	v_mfma_i32_16x16x64_i8 v[128:131], v[148:151], v[164:167], v[128:131]
	v_mfma_i32_16x16x64_i8 v[124:127], v[156:159], v[164:167], v[124:127]
	v_mfma_i32_16x16x64_i8 v[120:123], v[148:151], v[172:175], v[120:123]
	v_mfma_i32_16x16x64_i8 v[116:119], v[156:159], v[172:175], v[116:119]
	v_mfma_i32_16x16x64_i8 v[112:115], v[148:151], v[180:183], v[112:115]
	v_mfma_i32_16x16x64_i8 v[108:111], v[156:159], v[180:183], v[108:111]
	v_mfma_i32_16x16x64_i8 v[104:107], v[148:151], v[188:191], v[104:107]
	v_mfma_i32_16x16x64_i8 v[100:103], v[156:159], v[188:191], v[100:103]
	s_barrier
	s_add_i32 s34, 0, 0x1c000
	s_add_i32 s26, s47, s5
	v_add_u32_e32 v142, s34, v1
	v_lshl_add_u64 v[208:209], v[208:209], 0, s[68:69]
	s_mov_b32 m0, s26
	ds_read_b128 v[192:195], v142
	ds_read_b128 v[196:199], v142 offset:1024
	ds_read_b128 v[200:203], v142 offset:2048
	ds_read_b128 v[204:207], v142 offset:3072
	global_load_lds_dwordx4 v[208:209], off
	s_add_i32 m0, s26, 0x2000
	v_lshl_add_u64 v[208:209], v[210:211], 0, s[68:69]
	global_load_lds_dwordx4 v[208:209], off
	s_barrier
	s_waitcnt lgkmcnt(0)
	v_mfma_i32_16x16x64_i8 v[94:97], v[192:195], v[160:163], v[94:97]
	v_mfma_i32_16x16x64_i8 v[90:93], v[200:203], v[160:163], v[90:93]
	v_mfma_i32_16x16x64_i8 v[86:89], v[192:195], v[168:171], v[86:89]
	v_mfma_i32_16x16x64_i8 v[82:85], v[200:203], v[168:171], v[82:85]
	v_mfma_i32_16x16x64_i8 v[78:81], v[192:195], v[176:179], v[78:81]
	v_mfma_i32_16x16x64_i8 v[74:77], v[200:203], v[176:179], v[74:77]
	v_mfma_i32_16x16x64_i8 v[70:73], v[192:195], v[184:187], v[70:73]
	v_mfma_i32_16x16x64_i8 v[66:69], v[200:203], v[184:187], v[66:69]
	v_mfma_i32_16x16x64_i8 v[94:97], v[196:199], v[164:167], v[94:97]
	v_mfma_i32_16x16x64_i8 v[90:93], v[204:207], v[164:167], v[90:93]
	v_mfma_i32_16x16x64_i8 v[86:89], v[196:199], v[172:175], v[86:89]
	v_mfma_i32_16x16x64_i8 v[82:85], v[204:207], v[172:175], v[82:85]
	v_mfma_i32_16x16x64_i8 v[78:81], v[196:199], v[180:183], v[78:81]
	v_mfma_i32_16x16x64_i8 v[74:77], v[204:207], v[180:183], v[74:77]
	v_mfma_i32_16x16x64_i8 v[70:73], v[196:199], v[188:191], v[70:73]
	v_mfma_i32_16x16x64_i8 v[66:69], v[204:207], v[188:191], v[66:69]
	s_mov_b32 m0, s38
	v_lshl_add_u64 v[208:209], v[212:213], 0, s[68:69]
	s_barrier
	ds_read_b128 v[160:163], v143 offset:49152
	ds_read_b128 v[164:167], v143 offset:50176
	ds_read_b128 v[168:171], v143 offset:51200
	ds_read_b128 v[172:175], v143 offset:52224
	ds_read_b128 v[176:179], v143 offset:53248
	ds_read_b128 v[180:183], v143 offset:54272
	ds_read_b128 v[184:187], v143 offset:55296
	ds_read_b128 v[188:191], v143 offset:56320
	global_load_lds_dwordx4 v[208:209], off
	s_mov_b32 m0, s39
	v_lshl_add_u64 v[208:209], v[214:215], 0, s[68:69]
	global_load_lds_dwordx4 v[208:209], off
	s_barrier
	s_waitcnt lgkmcnt(0)
	v_mfma_i32_16x16x64_i8 v[62:65], v[144:147], v[160:163], v[62:65]
	v_mfma_i32_16x16x64_i8 v[58:61], v[152:155], v[160:163], v[58:61]
	v_mfma_i32_16x16x64_i8 v[54:57], v[144:147], v[168:171], v[54:57]
	v_mfma_i32_16x16x64_i8 v[50:53], v[152:155], v[168:171], v[50:53]
	v_mfma_i32_16x16x64_i8 v[46:49], v[144:147], v[176:179], v[46:49]
	v_mfma_i32_16x16x64_i8 v[42:45], v[152:155], v[176:179], v[42:45]
	v_mfma_i32_16x16x64_i8 v[38:41], v[144:147], v[184:187], v[38:41]
	v_mfma_i32_16x16x64_i8 v[34:37], v[152:155], v[184:187], v[34:37]
	v_mfma_i32_16x16x64_i8 v[62:65], v[148:151], v[164:167], v[62:65]
	v_mfma_i32_16x16x64_i8 v[58:61], v[156:159], v[164:167], v[58:61]
	v_mfma_i32_16x16x64_i8 v[54:57], v[148:151], v[172:175], v[54:57]
	v_mfma_i32_16x16x64_i8 v[50:53], v[156:159], v[172:175], v[50:53]
	v_mfma_i32_16x16x64_i8 v[46:49], v[148:151], v[180:183], v[46:49]
	v_mfma_i32_16x16x64_i8 v[42:45], v[156:159], v[180:183], v[42:45]
	v_mfma_i32_16x16x64_i8 v[38:41], v[148:151], v[188:191], v[38:41]
	v_mfma_i32_16x16x64_i8 v[34:37], v[156:159], v[188:191], v[34:37]
	s_barrier
	s_add_u32 s26, s30, 0xb0080
	s_addc_u32 s27, s31, 0
	s_add_i32 s30, s34, s5
	s_mov_b32 m0, s30
	v_lshl_add_u64 v[144:145], s[26:27], 0, v[98:99]
	global_load_lds_dwordx4 v[144:145], off
	s_add_i32 m0, s30, 0x2000
	v_lshl_add_u64 v[144:145], s[26:27], 0, v[132:133]
	global_load_lds_dwordx4 v[144:145], off
	s_waitcnt vmcnt(6)
	s_barrier
	v_mfma_i32_16x16x64_i8 v[30:33], v[192:195], v[160:163], v[30:33]
	v_mfma_i32_16x16x64_i8 v[26:29], v[200:203], v[160:163], v[26:29]
	v_mfma_i32_16x16x64_i8 v[22:25], v[192:195], v[168:171], v[22:25]
	v_mfma_i32_16x16x64_i8 v[18:21], v[200:203], v[168:171], v[18:21]
	v_mfma_i32_16x16x64_i8 v[14:17], v[192:195], v[176:179], v[14:17]
	v_mfma_i32_16x16x64_i8 v[10:13], v[200:203], v[176:179], v[10:13]
	v_mfma_i32_16x16x64_i8 v[6:9], v[192:195], v[184:187], v[6:9]
	v_mfma_i32_16x16x64_i8 v[2:5], v[200:203], v[184:187], v[2:5]
	v_mfma_i32_16x16x64_i8 v[30:33], v[196:199], v[164:167], v[30:33]
	v_mfma_i32_16x16x64_i8 v[26:29], v[204:207], v[164:167], v[26:29]
	v_mfma_i32_16x16x64_i8 v[22:25], v[196:199], v[172:175], v[22:25]
	v_mfma_i32_16x16x64_i8 v[18:21], v[204:207], v[172:175], v[18:21]
	v_mfma_i32_16x16x64_i8 v[14:17], v[196:199], v[180:183], v[14:17]
	v_mfma_i32_16x16x64_i8 v[10:13], v[204:207], v[180:183], v[10:13]
	v_mfma_i32_16x16x64_i8 v[6:9], v[196:199], v[188:191], v[6:9]
	v_mfma_i32_16x16x64_i8 v[2:5], v[204:207], v[188:191], v[2:5]
	s_add_u32 s33, s33, 0x100
	s_addc_u32 s45, s45, 0
	s_cmp_ge_i32 s46, s8
	s_mov_b64 s[26:27], s[28:29]
	s_mov_b32 s30, s46
	s_barrier
	s_cbranch_scc0 .LBB0_2238
	v_lshl_add_u32 v190, s9, 8, v134
	v_readlane_b32 s8, v253, 57
	v_ashrrev_i32_e32 v191, 31, v190
	v_readlane_b32 s9, v253, 58
	v_lshl_or_b32 v192, s3, 8, v135
	v_ashrrev_i32_e32 v193, 31, v192
	v_lshl_add_u64 v[158:159], v[190:191], 2, s[8:9]
	v_readlane_b32 s8, v254, 30
	v_readlane_b32 s9, v254, 31
	v_cvt_f32_i32_e32 v161, v129
	v_cvt_f32_i32_e32 v160, v128
	v_cvt_f32_i32_e32 v129, v127
	v_cvt_f32_i32_e32 v128, v126
	v_cvt_f32_i32_e32 v127, v87
	v_cvt_f32_i32_e32 v126, v86
	v_cvt_f32_i32_e32 v87, v77
	v_cvt_f32_i32_e32 v86, v76
	v_cvt_f32_i32_e32 v77, v31
	v_cvt_f32_i32_e32 v76, v30
	v_cvt_f32_i32_e32 v31, v21
	v_cvt_f32_i32_e32 v30, v20
	v_cvt_f32_i32_e32 v21, v7
	v_cvt_f32_i32_e32 v20, v6
	v_lshl_add_u64 v[6:7], v[192:193], 2, s[8:9]
	global_load_dword v156, v[158:159], off
	global_load_dword v154, v[158:159], off offset:64
	global_load_dword v152, v[158:159], off offset:128
	global_load_dword v150, v[158:159], off offset:192
	global_load_dword v148, v[158:159], off offset:512
	global_load_dword v146, v[158:159], off offset:576
	global_load_dword v144, v[158:159], off offset:640
	global_load_dword v142, v[158:159], off offset:704
	v_cvt_f32_i32_e32 v163, v93
	v_cvt_f32_i32_e32 v162, v92
	v_cvt_f32_i32_e32 v165, v91
	v_cvt_f32_i32_e32 v164, v90
	v_cvt_f32_i32_e32 v91, v81
	v_cvt_f32_i32_e32 v90, v80
	v_cvt_f32_i32_e32 v93, v79
	v_cvt_f32_i32_e32 v92, v78
	v_cvt_f32_i32_e32 v79, v69
	v_cvt_f32_i32_e32 v78, v68
	v_cvt_f32_i32_e32 v81, v67
	v_cvt_f32_i32_e32 v80, v66
	v_cvt_f32_i32_e32 v67, v29
	v_cvt_f32_i32_e32 v66, v28
	v_cvt_f32_i32_e32 v69, v27
	v_cvt_f32_i32_e32 v68, v26
	v_cvt_f32_i32_e32 v27, v17
	v_cvt_f32_i32_e32 v26, v16
	v_cvt_f32_i32_e32 v29, v15
	v_cvt_f32_i32_e32 v28, v14
	v_cvt_f32_i32_e32 v15, v5
	v_cvt_f32_i32_e32 v14, v4
	v_cvt_f32_i32_e32 v17, v3
	v_cvt_f32_i32_e32 v16, v2
	global_load_dwordx4 v[2:5], v[6:7], off
	v_cvt_f32_i32_e32 v159, v131
	v_cvt_f32_i32_e32 v158, v130
	v_cvt_f32_i32_e32 v131, v125
	v_cvt_f32_i32_e32 v130, v124
	v_cvt_f32_i32_e32 v123, v123
	v_cvt_f32_i32_e32 v122, v122
	v_cvt_f32_i32_e32 v121, v121
	v_cvt_f32_i32_e32 v120, v120
	v_cvt_f32_i32_e32 v119, v119
	v_cvt_f32_i32_e32 v118, v118
	v_cvt_f32_i32_e32 v117, v117
	v_cvt_f32_i32_e32 v116, v116
	v_cvt_f32_i32_e32 v115, v115
	v_cvt_f32_i32_e32 v114, v114
	v_cvt_f32_i32_e32 v113, v113
	v_cvt_f32_i32_e32 v112, v112
	v_cvt_f32_i32_e32 v111, v111
	v_cvt_f32_i32_e32 v110, v110
	v_cvt_f32_i32_e32 v109, v109
	v_cvt_f32_i32_e32 v108, v108
	v_cvt_f32_i32_e32 v107, v107
	v_cvt_f32_i32_e32 v106, v106
	v_cvt_f32_i32_e32 v105, v105
	v_cvt_f32_i32_e32 v104, v104
	v_cvt_f32_i32_e32 v103, v103
	v_cvt_f32_i32_e32 v102, v102
	v_cvt_f32_i32_e32 v101, v101
	v_cvt_f32_i32_e32 v100, v100
	v_cvt_f32_i32_e32 v167, v97
	v_cvt_f32_i32_e32 v166, v96
	v_cvt_f32_i32_e32 v169, v95
	v_cvt_f32_i32_e32 v168, v94
	v_cvt_f32_i32_e32 v125, v89
	v_cvt_f32_i32_e32 v124, v88
	v_cvt_f32_i32_e32 v95, v85
	v_cvt_f32_i32_e32 v94, v84
	v_cvt_f32_i32_e32 v97, v83
	v_cvt_f32_i32_e32 v96, v82
	v_cvt_f32_i32_e32 v89, v75
	v_cvt_f32_i32_e32 v88, v74
	v_cvt_f32_i32_e32 v83, v73
	v_cvt_f32_i32_e32 v82, v72
	v_cvt_f32_i32_e32 v85, v71
	v_cvt_f32_i32_e32 v84, v70
	v_cvt_f32_i32_e32 v71, v65
	v_cvt_f32_i32_e32 v70, v64
	v_cvt_f32_i32_e32 v73, v63
	v_cvt_f32_i32_e32 v72, v62
	v_cvt_f32_i32_e32 v63, v61
	v_cvt_f32_i32_e32 v62, v60
	v_cvt_f32_i32_e32 v65, v59
	v_cvt_f32_i32_e32 v64, v58
	v_cvt_f32_i32_e32 v57, v57
	v_cvt_f32_i32_e32 v56, v56
	v_cvt_f32_i32_e32 v55, v55
	v_cvt_f32_i32_e32 v54, v54
	v_cvt_f32_i32_e32 v53, v53
	v_cvt_f32_i32_e32 v52, v52
	v_cvt_f32_i32_e32 v51, v51
	v_cvt_f32_i32_e32 v50, v50
	v_cvt_f32_i32_e32 v49, v49
	v_cvt_f32_i32_e32 v48, v48
	v_cvt_f32_i32_e32 v47, v47
	v_cvt_f32_i32_e32 v46, v46
	v_cvt_f32_i32_e32 v45, v45
	v_cvt_f32_i32_e32 v44, v44
	v_cvt_f32_i32_e32 v43, v43
	v_cvt_f32_i32_e32 v42, v42
	v_cvt_f32_i32_e32 v41, v41
	v_cvt_f32_i32_e32 v40, v40
	v_cvt_f32_i32_e32 v39, v39
	v_cvt_f32_i32_e32 v38, v38
	v_cvt_f32_i32_e32 v37, v37
	v_cvt_f32_i32_e32 v36, v36
	v_cvt_f32_i32_e32 v35, v35
	v_cvt_f32_i32_e32 v34, v34
	v_cvt_f32_i32_e32 v75, v33
	v_cvt_f32_i32_e32 v74, v32
	v_cvt_f32_i32_e32 v59, v25
	s_waitcnt vmcnt(0)
	v_pk_mul_f32 v[170:171], v[4:5], s[58:59] op_sel_hi:[1,0]
	v_pk_mul_f32 v[172:173], v[2:3], s[58:59] op_sel_hi:[1,0]
	global_load_dwordx4 v[2:5], v[6:7], off offset:64
	v_cvt_f32_i32_e32 v58, v24
	v_cvt_f32_i32_e32 v61, v23
	v_cvt_f32_i32_e32 v60, v22
	v_cvt_f32_i32_e32 v33, v19
	v_cvt_f32_i32_e32 v32, v18
	v_cvt_f32_i32_e32 v23, v13
	v_cvt_f32_i32_e32 v22, v12
	v_cvt_f32_i32_e32 v25, v11
	v_cvt_f32_i32_e32 v24, v10
	v_cvt_f32_i32_e32 v19, v9
	v_cvt_f32_i32_e32 v18, v8
	s_mov_b64 s[26:27], -1
	s_cmp_lt_i32 s62, 0
	s_waitcnt vmcnt(0)
	v_pk_mul_f32 v[174:175], v[4:5], s[58:59] op_sel_hi:[1,0]
	v_pk_mul_f32 v[180:181], v[2:3], s[58:59] op_sel_hi:[1,0]
	global_load_dwordx4 v[2:5], v[6:7], off offset:512
	s_waitcnt vmcnt(0)
	v_pk_mul_f32 v[182:183], v[4:5], s[58:59] op_sel_hi:[1,0]
	v_pk_mul_f32 v[184:185], v[2:3], s[58:59] op_sel_hi:[1,0]
	global_load_dwordx4 v[2:5], v[6:7], off offset:576
	s_waitcnt vmcnt(0)
	v_pk_mul_f32 v[186:187], v[4:5], s[58:59] op_sel_hi:[1,0]
	v_pk_mul_f32 v[188:189], v[2:3], s[58:59] op_sel_hi:[1,0]
	s_cbranch_scc0 .LBB0_2241
	v_readlane_b32 s8, v254, 28
	v_lshlrev_b64 v[2:3], 2, v[192:193]
	v_readlane_b32 s9, v254, 29
	v_pk_mul_f32 v[218:219], v[156:157], v[160:161] op_sel_hi:[0,1]
	v_pk_mul_f32 v[244:245], v[152:153], v[112:113] op_sel_hi:[0,1]
	v_lshl_add_u64 v[8:9], s[8:9], 0, v[2:3]
	global_load_dwordx4 v[4:7], v[8:9], off
	v_readlane_b32 s8, v253, 28
	v_readlane_b32 s9, v253, 29
	s_mov_b32 s3, 0x100000
	s_mov_b64 s[26:27], 0
	v_lshl_add_u64 v[212:213], s[8:9], 0, v[2:3]
	s_mov_b64 s[8:9], 0x100000
	s_waitcnt vmcnt(0)
	v_pk_mul_f32 v[206:207], v[170:171], v[6:7]
	v_pk_mul_f32 v[208:209], v[172:173], v[4:5]
	global_load_dwordx4 v[4:7], v[8:9], off offset:64
	s_waitcnt vmcnt(0)
	v_pk_mul_f32 v[202:203], v[174:175], v[6:7]
	v_pk_mul_f32 v[204:205], v[180:181], v[4:5]
	global_load_dwordx4 v[4:7], v[8:9], off offset:512
	s_waitcnt vmcnt(0)
	v_pk_mul_f32 v[198:199], v[182:183], v[6:7]
	v_pk_mul_f32 v[200:201], v[184:185], v[4:5]
	global_load_dwordx4 v[4:7], v[8:9], off offset:576
	s_waitcnt vmcnt(0)
	v_pk_mul_f32 v[196:197], v[188:189], v[4:5]
	v_add_u32_e32 v4, 0xffffff00, v190
	v_ashrrev_i32_e32 v5, 31, v4
	v_lshlrev_b64 v[4:5], 13, v[4:5]
	v_lshl_add_u64 v[12:13], v[212:213], 0, v[4:5]
	v_pk_mul_f32 v[194:195], v[186:187], v[6:7]
	global_load_dwordx4 v[4:7], v[12:13], off
	global_load_dwordx4 v[8:11], v[12:13], off offset:64
	global_load_dwordx4 v[176:179], v[12:13], off offset:512
	global_load_dwordx4 v[214:217], v[12:13], off offset:576
	v_add_u32_e32 v12, 0xffffff10, v190
	v_ashrrev_i32_e32 v13, 31, v12
	v_lshlrev_b64 v[12:13], 13, v[12:13]
	v_lshl_add_u64 v[12:13], v[212:213], 0, v[12:13]
	global_load_dwordx4 v[222:225], v[12:13], off
	global_load_dwordx4 v[230:233], v[12:13], off offset:64
	global_load_dwordx4 v[236:239], v[12:13], off offset:512
	global_load_dwordx4 v[240:243], v[12:13], off offset:576
	v_lshlrev_b64 v[12:13], 13, v[190:191]
	v_lshl_add_u64 v[12:13], s[76:77], 0, v[12:13]
	v_lshl_add_u64 v[210:211], v[12:13], 0, v[2:3]
	v_pk_mul_f32 v[12:13], v[156:157], v[158:159] op_sel_hi:[0,1]
	s_waitcnt vmcnt(0)
	v_pk_fma_f32 v[6:7], v[12:13], v[206:207], v[6:7]
	v_pk_fma_f32 v[4:5], v[218:219], v[208:209], v[4:5]
	global_store_dwordx4 v[210:211], v[4:7], off
	v_pk_mul_f32 v[12:13], v[156:157], v[130:131] op_sel_hi:[0,1]
	v_pk_mul_f32 v[218:219], v[152:153], v[114:115] op_sel_hi:[0,1]
	v_pk_mul_f32 v[4:5], v[156:157], v[128:129] op_sel_hi:[0,1]
	v_pk_fma_f32 v[6:7], v[4:5], v[202:203], v[10:11]
	v_pk_fma_f32 v[4:5], v[12:13], v[204:205], v[8:9]
	global_store_dwordx4 v[210:211], v[4:7], off offset:64
	v_pk_mul_f32 v[8:9], v[156:157], v[168:169] op_sel_hi:[0,1]
	v_pk_mul_f32 v[10:11], v[154:155], v[120:121] op_sel_hi:[0,1]
	v_pk_mul_f32 v[4:5], v[156:157], v[166:167] op_sel_hi:[0,1]
	v_pk_fma_f32 v[6:7], v[4:5], v[198:199], v[178:179]
	v_pk_fma_f32 v[4:5], v[8:9], v[200:201], v[176:177]
	global_store_dwordx4 v[210:211], v[4:7], off offset:512
	v_pk_mul_f32 v[8:9], v[156:157], v[164:165] op_sel_hi:[0,1]
	s_nop 0
	v_pk_mul_f32 v[4:5], v[156:157], v[162:163] op_sel_hi:[0,1]
	v_pk_fma_f32 v[6:7], v[4:5], v[194:195], v[216:217]
	v_pk_fma_f32 v[4:5], v[8:9], v[196:197], v[214:215]
	global_store_dwordx4 v[210:211], v[4:7], off offset:576
	s_nop 1
	v_or_b32_e32 v4, 16, v190
	v_ashrrev_i32_e32 v5, 31, v4
	v_lshlrev_b64 v[4:5], 13, v[4:5]
	v_lshl_add_u64 v[4:5], s[76:77], 0, v[4:5]
	v_lshl_add_u64 v[8:9], v[4:5], 0, v[2:3]
	v_pk_mul_f32 v[4:5], v[154:155], v[122:123] op_sel_hi:[0,1]
	v_pk_fma_f32 v[6:7], v[4:5], v[206:207], v[224:225]
	v_pk_fma_f32 v[4:5], v[10:11], v[208:209], v[222:223]
	global_store_dwordx4 v[8:9], v[4:7], off
	v_pk_mul_f32 v[10:11], v[154:155], v[116:117] op_sel_hi:[0,1]
	s_nop 0
	v_pk_mul_f32 v[4:5], v[154:155], v[118:119] op_sel_hi:[0,1]
	v_pk_fma_f32 v[6:7], v[4:5], v[202:203], v[232:233]
	v_pk_fma_f32 v[4:5], v[10:11], v[204:205], v[230:231]
	global_store_dwordx4 v[8:9], v[4:7], off offset:64
	v_pk_mul_f32 v[10:11], v[154:155], v[126:127] op_sel_hi:[0,1]
	s_nop 0
	v_pk_mul_f32 v[4:5], v[154:155], v[124:125] op_sel_hi:[0,1]
	v_pk_fma_f32 v[6:7], v[4:5], v[198:199], v[238:239]
	v_pk_fma_f32 v[4:5], v[10:11], v[200:201], v[236:237]
	global_store_dwordx4 v[8:9], v[4:7], off offset:512
	v_pk_mul_f32 v[10:11], v[154:155], v[96:97] op_sel_hi:[0,1]
	s_nop 0
	v_pk_mul_f32 v[4:5], v[154:155], v[94:95] op_sel_hi:[0,1]
	v_pk_fma_f32 v[6:7], v[4:5], v[194:195], v[242:243]
	v_pk_fma_f32 v[4:5], v[10:11], v[196:197], v[240:241]
	global_store_dwordx4 v[8:9], v[4:7], off offset:576
	s_nop 1
	v_add_u32_e32 v4, 0xffffff20, v190
	v_ashrrev_i32_e32 v5, 31, v4
	v_lshlrev_b64 v[4:5], 13, v[4:5]
	v_lshl_add_u64 v[12:13], v[212:213], 0, v[4:5]
	global_load_dwordx4 v[4:7], v[12:13], off
	global_load_dwordx4 v[8:11], v[12:13], off offset:64
	global_load_dwordx4 v[176:179], v[12:13], off offset:512
	global_load_dwordx4 v[214:217], v[12:13], off offset:576
	v_add_u32_e32 v12, 0xffffff30, v190
	v_ashrrev_i32_e32 v13, 31, v12
	v_lshlrev_b64 v[12:13], 13, v[12:13]
	v_lshl_add_u64 v[12:13], v[212:213], 0, v[12:13]
	global_load_dwordx4 v[222:225], v[12:13], off
	global_load_dwordx4 v[230:233], v[12:13], off offset:64
	global_load_dwordx4 v[236:239], v[12:13], off offset:512
	global_load_dwordx4 v[240:243], v[12:13], off offset:576
	v_or_b32_e32 v12, 32, v190
	v_ashrrev_i32_e32 v13, 31, v12
	v_lshlrev_b64 v[12:13], 13, v[12:13]
	v_lshl_add_u64 v[12:13], s[76:77], 0, v[12:13]
	v_lshl_add_u64 v[12:13], v[12:13], 0, v[2:3]
	s_waitcnt vmcnt(0)
	v_pk_fma_f32 v[6:7], v[218:219], v[206:207], v[6:7]
	v_pk_fma_f32 v[4:5], v[244:245], v[208:209], v[4:5]
	global_store_dwordx4 v[12:13], v[4:7], off
	v_pk_mul_f32 v[218:219], v[152:153], v[108:109] op_sel_hi:[0,1]
	s_nop 0
	v_pk_mul_f32 v[4:5], v[152:153], v[110:111] op_sel_hi:[0,1]
	v_pk_fma_f32 v[6:7], v[4:5], v[202:203], v[10:11]
	v_pk_fma_f32 v[4:5], v[218:219], v[204:205], v[8:9]
	global_store_dwordx4 v[12:13], v[4:7], off offset:64
	v_pk_mul_f32 v[8:9], v[152:153], v[92:93] op_sel_hi:[0,1]
	s_nop 0
	v_pk_mul_f32 v[4:5], v[152:153], v[90:91] op_sel_hi:[0,1]
	v_pk_fma_f32 v[6:7], v[4:5], v[198:199], v[178:179]
	v_pk_fma_f32 v[4:5], v[8:9], v[200:201], v[176:177]
	global_store_dwordx4 v[12:13], v[4:7], off offset:512
	v_pk_mul_f32 v[8:9], v[152:153], v[88:89] op_sel_hi:[0,1]
	s_nop 0
	v_pk_mul_f32 v[4:5], v[152:153], v[86:87] op_sel_hi:[0,1]
	v_pk_fma_f32 v[6:7], v[4:5], v[194:195], v[216:217]
	v_pk_fma_f32 v[4:5], v[8:9], v[196:197], v[214:215]
	global_store_dwordx4 v[12:13], v[4:7], off offset:576
	v_pk_mul_f32 v[8:9], v[150:151], v[104:105] op_sel_hi:[0,1]
	v_add_u32_e32 v214, 0xffffff90, v190
	v_or_b32_e32 v4, 48, v190
	v_ashrrev_i32_e32 v5, 31, v4
	v_lshlrev_b64 v[4:5], 13, v[4:5]
	v_lshl_add_u64 v[4:5], s[76:77], 0, v[4:5]
	v_lshl_add_u64 v[6:7], v[4:5], 0, v[2:3]
	v_pk_mul_f32 v[2:3], v[150:151], v[106:107] op_sel_hi:[0,1]
	v_pk_fma_f32 v[4:5], v[2:3], v[206:207], v[224:225]
	v_pk_fma_f32 v[2:3], v[8:9], v[208:209], v[222:223]
	global_store_dwordx4 v[6:7], v[2:5], off
	v_pk_mul_f32 v[8:9], v[150:151], v[100:101] op_sel_hi:[0,1]
	v_ashrrev_i32_e32 v215, 31, v214
	v_pk_mul_f32 v[2:3], v[150:151], v[102:103] op_sel_hi:[0,1]
	v_pk_fma_f32 v[4:5], v[2:3], v[202:203], v[232:233]
	v_pk_fma_f32 v[2:3], v[8:9], v[204:205], v[230:231]
	global_store_dwordx4 v[6:7], v[2:5], off offset:64
	v_pk_mul_f32 v[8:9], v[150:151], v[84:85] op_sel_hi:[0,1]
	v_lshlrev_b64 v[214:215], 13, v[214:215]
	v_pk_mul_f32 v[2:3], v[150:151], v[82:83] op_sel_hi:[0,1]
	v_pk_fma_f32 v[4:5], v[2:3], v[198:199], v[238:239]
	v_pk_fma_f32 v[2:3], v[8:9], v[200:201], v[236:237]
	global_store_dwordx4 v[6:7], v[2:5], off offset:512
	v_pk_mul_f32 v[8:9], v[150:151], v[80:81] op_sel_hi:[0,1]
	v_lshl_add_u64 v[218:219], v[212:213], 0, v[214:215]
	v_pk_mul_f32 v[2:3], v[150:151], v[78:79] op_sel_hi:[0,1]
	v_pk_fma_f32 v[4:5], v[2:3], v[194:195], v[242:243]
	v_pk_fma_f32 v[2:3], v[8:9], v[196:197], v[240:241]
	global_store_dwordx4 v[6:7], v[2:5], off offset:576
	v_pk_mul_f32 v[240:241], v[148:149], v[70:71] op_sel_hi:[0,1]
	v_pk_mul_f32 v[242:243], v[148:149], v[72:73] op_sel_hi:[0,1]
	v_add_u32_e32 v2, 0xffffff80, v190
	v_ashrrev_i32_e32 v3, 31, v2
	v_lshlrev_b64 v[2:3], 13, v[2:3]
	v_lshl_add_u64 v[2:3], v[212:213], 0, v[2:3]
	global_load_dwordx4 v[10:13], v[2:3], off
	global_load_dwordx4 v[176:179], v[2:3], off offset:64
	global_load_dwordx4 v[6:9], v[2:3], off offset:512
	s_nop 0
	global_load_dwordx4 v[2:5], v[2:3], off offset:576
	s_nop 0
	global_load_dwordx4 v[214:217], v[218:219], off
	global_load_dwordx4 v[222:225], v[218:219], off offset:64
	global_load_dwordx4 v[230:233], v[218:219], off offset:512
	global_load_dwordx4 v[236:239], v[218:219], off offset:576
	v_lshl_add_u64 v[218:219], v[210:211], 0, s[8:9]
	s_mov_b64 s[8:9], 0x120000
	s_waitcnt vmcnt(0)
	v_pk_fma_f32 v[12:13], v[240:241], v[206:207], v[12:13]
	v_add_co_u32_e32 v240, vcc, s3, v210
	v_pk_fma_f32 v[10:11], v[242:243], v[208:209], v[10:11]
	s_nop 0
	v_addc_co_u32_e32 v241, vcc, 0, v211, vcc
	global_store_dwordx4 v[240:241], v[10:13], off
	v_pk_mul_f32 v[240:241], v[148:149], v[64:65] op_sel_hi:[0,1]
	s_mov_b32 s3, 0x120000
	v_pk_mul_f32 v[10:11], v[148:149], v[62:63] op_sel_hi:[0,1]
	v_pk_fma_f32 v[12:13], v[10:11], v[202:203], v[178:179]
	v_pk_fma_f32 v[10:11], v[240:241], v[204:205], v[176:177]
	global_store_dwordx4 v[218:219], v[10:13], off offset:64
	s_nop 1
	v_pk_mul_f32 v[10:11], v[148:149], v[74:75] op_sel_hi:[0,1]
	v_pk_mul_f32 v[12:13], v[148:149], v[76:77] op_sel_hi:[0,1]
	v_pk_fma_f32 v[8:9], v[10:11], v[198:199], v[8:9]
	v_pk_fma_f32 v[6:7], v[12:13], v[200:201], v[6:7]
	global_store_dwordx4 v[218:219], v[6:9], off offset:512
	s_nop 1
	v_pk_mul_f32 v[6:7], v[148:149], v[66:67] op_sel_hi:[0,1]
	v_pk_mul_f32 v[8:9], v[148:149], v[68:69] op_sel_hi:[0,1]
	v_pk_fma_f32 v[4:5], v[6:7], v[194:195], v[4:5]
	v_pk_fma_f32 v[2:3], v[8:9], v[196:197], v[2:3]
	global_store_dwordx4 v[218:219], v[2:5], off offset:576
	v_pk_mul_f32 v[8:9], v[146:147], v[54:55] op_sel_hi:[0,1]
	v_lshl_add_u64 v[6:7], v[210:211], 0, s[8:9]
	v_pk_mul_f32 v[2:3], v[146:147], v[56:57] op_sel_hi:[0,1]
	v_pk_fma_f32 v[4:5], v[2:3], v[206:207], v[216:217]
	v_pk_fma_f32 v[2:3], v[8:9], v[208:209], v[214:215]
	v_add_co_u32_e32 v8, vcc, s3, v210
	s_mov_b32 s3, 0x140000
	s_nop 0
	v_addc_co_u32_e32 v9, vcc, 0, v211, vcc
	global_store_dwordx4 v[8:9], v[2:5], off
	v_pk_mul_f32 v[8:9], v[146:147], v[50:51] op_sel_hi:[0,1]
	v_pk_mul_f32 v[218:219], v[144:145], v[46:47] op_sel_hi:[0,1]
	v_pk_mul_f32 v[2:3], v[146:147], v[52:53] op_sel_hi:[0,1]
	v_pk_fma_f32 v[4:5], v[2:3], v[202:203], v[224:225]
	v_pk_fma_f32 v[2:3], v[8:9], v[204:205], v[222:223]
	global_store_dwordx4 v[6:7], v[2:5], off offset:64
	v_pk_mul_f32 v[8:9], v[146:147], v[60:61] op_sel_hi:[0,1]
	s_mov_b64 s[8:9], 0x140000
	v_pk_mul_f32 v[2:3], v[146:147], v[58:59] op_sel_hi:[0,1]
	v_pk_fma_f32 v[4:5], v[2:3], v[198:199], v[232:233]
	v_pk_fma_f32 v[2:3], v[8:9], v[200:201], v[230:231]
	global_store_dwordx4 v[6:7], v[2:5], off offset:512
	v_pk_mul_f32 v[8:9], v[146:147], v[32:33] op_sel_hi:[0,1]
	s_nop 0
	v_pk_mul_f32 v[2:3], v[146:147], v[30:31] op_sel_hi:[0,1]
	v_pk_fma_f32 v[4:5], v[2:3], v[194:195], v[238:239]
	v_pk_fma_f32 v[2:3], v[8:9], v[196:197], v[236:237]
	global_store_dwordx4 v[6:7], v[2:5], off offset:576
	s_nop 1
	v_add_u32_e32 v2, 0xffffffa0, v190
	v_ashrrev_i32_e32 v3, 31, v2
	v_lshlrev_b64 v[2:3], 13, v[2:3]
	v_lshl_add_u64 v[2:3], v[212:213], 0, v[2:3]
	global_load_dwordx4 v[176:179], v[2:3], off
	global_load_dwordx4 v[214:217], v[2:3], off offset:64
	global_load_dwordx4 v[10:13], v[2:3], off offset:512
	global_load_dwordx4 v[6:9], v[2:3], off offset:576
	v_add_u32_e32 v2, 0xffffffb0, v190
	v_ashrrev_i32_e32 v3, 31, v2
	v_lshlrev_b64 v[2:3], 13, v[2:3]
	v_lshl_add_u64 v[2:3], v[212:213], 0, v[2:3]
	global_load_dwordx4 v[222:225], v[2:3], off
	global_load_dwordx4 v[230:233], v[2:3], off offset:64
	global_load_dwordx4 v[236:239], v[2:3], off offset:512
	s_nop 0
	global_load_dwordx4 v[2:5], v[2:3], off offset:576
	v_pk_mul_f32 v[212:213], v[144:145], v[48:49] op_sel_hi:[0,1]
	v_lshl_add_u64 v[190:191], v[210:211], 0, s[8:9]
	s_mov_b64 s[8:9], 0x160000
	s_waitcnt vmcnt(0)
	v_pk_fma_f32 v[178:179], v[212:213], v[206:207], v[178:179]
	v_add_co_u32_e32 v212, vcc, s3, v210
	v_pk_fma_f32 v[176:177], v[218:219], v[208:209], v[176:177]
	s_nop 0
	v_addc_co_u32_e32 v213, vcc, 0, v211, vcc
	global_store_dwordx4 v[212:213], v[176:179], off
	v_pk_mul_f32 v[212:213], v[144:145], v[42:43] op_sel_hi:[0,1]
	s_mov_b32 s3, 0x160000
	v_pk_mul_f32 v[176:177], v[144:145], v[44:45] op_sel_hi:[0,1]
	v_pk_fma_f32 v[178:179], v[176:177], v[202:203], v[216:217]
	v_pk_fma_f32 v[176:177], v[212:213], v[204:205], v[214:215]
	global_store_dwordx4 v[190:191], v[176:179], off offset:64
	s_nop 1
	v_pk_mul_f32 v[176:177], v[144:145], v[26:27] op_sel_hi:[0,1]
	v_pk_mul_f32 v[178:179], v[144:145], v[28:29] op_sel_hi:[0,1]
	v_pk_fma_f32 v[12:13], v[176:177], v[198:199], v[12:13]
	v_pk_fma_f32 v[10:11], v[178:179], v[200:201], v[10:11]
	global_store_dwordx4 v[190:191], v[10:13], off offset:512
	s_nop 1
	v_pk_mul_f32 v[10:11], v[144:145], v[22:23] op_sel_hi:[0,1]
	v_pk_mul_f32 v[12:13], v[144:145], v[24:25] op_sel_hi:[0,1]
	v_pk_fma_f32 v[8:9], v[10:11], v[194:195], v[8:9]
	v_pk_fma_f32 v[6:7], v[12:13], v[196:197], v[6:7]
	global_store_dwordx4 v[190:191], v[6:9], off offset:576
	v_pk_mul_f32 v[12:13], v[142:143], v[38:39] op_sel_hi:[0,1]
	v_lshl_add_u64 v[10:11], v[210:211], 0, s[8:9]
	v_pk_mul_f32 v[6:7], v[142:143], v[40:41] op_sel_hi:[0,1]
	v_pk_fma_f32 v[8:9], v[6:7], v[206:207], v[224:225]
	v_pk_fma_f32 v[6:7], v[12:13], v[208:209], v[222:223]
	v_add_co_u32_e32 v12, vcc, s3, v210
	s_nop 1
	v_addc_co_u32_e32 v13, vcc, 0, v211, vcc
	global_store_dwordx4 v[12:13], v[6:9], off
	v_pk_mul_f32 v[12:13], v[142:143], v[34:35] op_sel_hi:[0,1]
	s_nop 0
	v_pk_mul_f32 v[6:7], v[142:143], v[36:37] op_sel_hi:[0,1]
	v_pk_fma_f32 v[8:9], v[6:7], v[202:203], v[232:233]
	v_pk_fma_f32 v[6:7], v[12:13], v[204:205], v[230:231]
	global_store_dwordx4 v[10:11], v[6:9], off offset:64
	v_pk_mul_f32 v[12:13], v[142:143], v[20:21] op_sel_hi:[0,1]
	s_nop 0
	v_pk_mul_f32 v[6:7], v[142:143], v[18:19] op_sel_hi:[0,1]
	v_pk_fma_f32 v[8:9], v[6:7], v[198:199], v[238:239]
	v_pk_fma_f32 v[6:7], v[12:13], v[200:201], v[236:237]
	global_store_dwordx4 v[10:11], v[6:9], off offset:512
	s_nop 1
	v_pk_mul_f32 v[6:7], v[142:143], v[14:15] op_sel_hi:[0,1]
	v_pk_mul_f32 v[8:9], v[142:143], v[16:17] op_sel_hi:[0,1]
	v_pk_fma_f32 v[4:5], v[6:7], v[194:195], v[4:5]
	v_pk_fma_f32 v[2:3], v[8:9], v[196:197], v[2:3]
	global_store_dwordx4 v[10:11], v[2:5], off offset:576
